# 8-phase GEMM K-loops: A1 fragment LDS reads of phases 2/6 issued right after the phase-1/5 barrier (behind that phase's MFMAs), lgkmcnt(4) before them; on top of the flip deletion
# speedup vs baseline: 1.0065x; 1.0065x over previous
.LBB0_545:
	s_add_u32 s34, s30, 0xfffc0080
	s_addc_u32 s35, s31, -1
	s_add_i32 s48, 0, 0x10000
	v_add_u32_e32 v142, s48, v143
	ds_read_b128 v[148:151], v142
	ds_read_b128 v[152:155], v142 offset:1024
	ds_read_b128 v[156:159], v142 offset:2048
	ds_read_b128 v[160:163], v142 offset:3072
	s_cmp_eq_u32 s47, 12
	s_cselect_b32 s37, s25, s35
	s_cselect_b32 s36, s43, s34
	s_cselect_b32 s35, s23, s46
	s_cselect_b32 s34, s44, s45
	v_lshl_add_u64 v[144:145], s[30:31], 0, v[138:139]
	s_add_i32 m0, s9, 0xc000
	ds_read_b128 v[166:169], v165
	ds_read_b128 v[170:173], v165 offset:1024
	ds_read_b128 v[180:183], v165 offset:2048
	ds_read_b128 v[184:187], v165 offset:3072
	ds_read_b128 v[188:191], v165 offset:4096
	ds_read_b128 v[192:195], v165 offset:5120
	ds_read_b128 v[196:199], v165 offset:6144
	ds_read_b128 v[200:203], v165 offset:7168
	global_load_lds_dwordx4 v[144:145], off
	v_lshl_add_u64 v[144:145], s[30:31], 0, v[140:141]
	s_add_i32 m0, s9, 0xe000
	s_nop 0
	global_load_lds_dwordx4 v[144:145], off
	s_waitcnt lgkmcnt(8)
	s_barrier
	v_add_u32_e32 v250, 0x14000, v143
	ds_read_b128 v[204:207], v250
	ds_read_b128 v[208:211], v250 offset:1024
	ds_read_b128 v[230:233], v250 offset:2048
	ds_read_b128 v[236:239], v250 offset:3072
	s_waitcnt lgkmcnt(4)
	s_waitcnt lgkmcnt(4)
	v_mfma_i32_16x16x64_i8 v[128:131], v[148:151], v[166:169], v[128:131]
	v_mfma_i32_16x16x64_i8 v[124:127], v[156:159], v[166:169], v[124:127]
	v_mfma_i32_16x16x64_i8 v[120:123], v[148:151], v[180:183], v[120:123]
	v_mfma_i32_16x16x64_i8 v[116:119], v[156:159], v[180:183], v[116:119]
	v_mfma_i32_16x16x64_i8 v[112:115], v[148:151], v[188:191], v[112:115]
	v_mfma_i32_16x16x64_i8 v[108:111], v[156:159], v[188:191], v[108:111]
	v_mfma_i32_16x16x64_i8 v[104:107], v[148:151], v[196:199], v[104:107]
	v_mfma_i32_16x16x64_i8 v[100:103], v[156:159], v[196:199], v[100:103]
	v_mfma_i32_16x16x64_i8 v[128:131], v[152:155], v[170:173], v[128:131]
	v_mfma_i32_16x16x64_i8 v[124:127], v[160:163], v[170:173], v[124:127]
	v_mfma_i32_16x16x64_i8 v[120:123], v[152:155], v[184:187], v[120:123]
	v_mfma_i32_16x16x64_i8 v[116:119], v[160:163], v[184:187], v[116:119]
	v_mfma_i32_16x16x64_i8 v[112:115], v[152:155], v[192:195], v[112:115]
	v_mfma_i32_16x16x64_i8 v[108:111], v[160:163], v[192:195], v[108:111]
	v_mfma_i32_16x16x64_i8 v[104:107], v[152:155], v[200:203], v[104:107]
	v_mfma_i32_16x16x64_i8 v[100:103], v[160:163], v[200:203], v[100:103]
	s_barrier
	s_add_i32 s50, 0, 0x14000
	s_add_i32 s48, s48, s8
	v_add_u32_e32 v142, s50, v143
	v_lshl_add_u64 v[144:145], s[34:35], 0, v[98:99]
	s_mov_b32 m0, s48
	global_load_lds_dwordx4 v[144:145], off
	v_lshl_add_u64 v[174:175], s[34:35], 0, v[132:133]
	s_add_i32 m0, s48, 0x2000
	s_nop 0
	global_load_lds_dwordx4 v[174:175], off
	s_barrier
	s_waitcnt lgkmcnt(0)
	s_waitcnt lgkmcnt(0)
	v_mfma_i32_16x16x64_i8 v[94:97], v[204:207], v[166:169], v[94:97]
	v_mfma_i32_16x16x64_i8 v[90:93], v[230:233], v[166:169], v[90:93]
	v_mfma_i32_16x16x64_i8 v[86:89], v[204:207], v[180:183], v[86:89]
	v_mfma_i32_16x16x64_i8 v[82:85], v[230:233], v[180:183], v[82:85]
	v_mfma_i32_16x16x64_i8 v[78:81], v[204:207], v[188:191], v[78:81]
	v_mfma_i32_16x16x64_i8 v[74:77], v[230:233], v[188:191], v[74:77]
	v_mfma_i32_16x16x64_i8 v[70:73], v[204:207], v[196:199], v[70:73]
	v_mfma_i32_16x16x64_i8 v[66:69], v[230:233], v[196:199], v[66:69]
	v_mfma_i32_16x16x64_i8 v[94:97], v[208:211], v[170:173], v[94:97]
	v_mfma_i32_16x16x64_i8 v[90:93], v[236:239], v[170:173], v[90:93]
	v_mfma_i32_16x16x64_i8 v[86:89], v[208:211], v[184:187], v[86:89]
	v_mfma_i32_16x16x64_i8 v[82:85], v[236:239], v[184:187], v[82:85]
	v_mfma_i32_16x16x64_i8 v[78:81], v[208:211], v[192:195], v[78:81]
	v_mfma_i32_16x16x64_i8 v[74:77], v[236:239], v[192:195], v[74:77]
	v_mfma_i32_16x16x64_i8 v[70:73], v[208:211], v[200:203], v[70:73]
	v_mfma_i32_16x16x64_i8 v[66:69], v[236:239], v[200:203], v[66:69]
	s_mov_b32 m0, s9
	v_lshl_add_u64 v[176:177], s[36:37], 0, v[136:137]
	s_barrier
	ds_read_b128 v[166:169], v165 offset:16384
	ds_read_b128 v[170:173], v165 offset:17408
	ds_read_b128 v[180:183], v165 offset:18432
	ds_read_b128 v[184:187], v165 offset:19456
	ds_read_b128 v[188:191], v165 offset:20480
	ds_read_b128 v[192:195], v165 offset:21504
	ds_read_b128 v[196:199], v165 offset:22528
	ds_read_b128 v[200:203], v165 offset:23552
	global_load_lds_dwordx4 v[176:177], off
	v_lshl_add_u64 v[178:179], s[36:37], 0, v[134:135]
	s_mov_b32 m0, s20
	s_nop 0
	global_load_lds_dwordx4 v[178:179], off
	s_barrier
	s_waitcnt lgkmcnt(0)
	s_waitcnt lgkmcnt(0)
	v_mfma_i32_16x16x64_i8 v[62:65], v[148:151], v[166:169], v[62:65]
	v_mfma_i32_16x16x64_i8 v[58:61], v[156:159], v[166:169], v[58:61]
	v_mfma_i32_16x16x64_i8 v[54:57], v[148:151], v[180:183], v[54:57]
	v_mfma_i32_16x16x64_i8 v[50:53], v[156:159], v[180:183], v[50:53]
	v_mfma_i32_16x16x64_i8 v[46:49], v[148:151], v[188:191], v[46:49]
	v_mfma_i32_16x16x64_i8 v[42:45], v[156:159], v[188:191], v[42:45]
	v_mfma_i32_16x16x64_i8 v[38:41], v[148:151], v[196:199], v[38:41]
	v_mfma_i32_16x16x64_i8 v[34:37], v[156:159], v[196:199], v[34:37]
	v_mfma_i32_16x16x64_i8 v[62:65], v[152:155], v[170:173], v[62:65]
	v_mfma_i32_16x16x64_i8 v[58:61], v[160:163], v[170:173], v[58:61]
	v_mfma_i32_16x16x64_i8 v[54:57], v[152:155], v[184:187], v[54:57]
	v_mfma_i32_16x16x64_i8 v[50:53], v[160:163], v[184:187], v[50:53]
	v_mfma_i32_16x16x64_i8 v[46:49], v[152:155], v[192:195], v[46:49]
	v_mfma_i32_16x16x64_i8 v[42:45], v[160:163], v[192:195], v[42:45]
	v_mfma_i32_16x16x64_i8 v[38:41], v[152:155], v[200:203], v[38:41]
	v_mfma_i32_16x16x64_i8 v[34:37], v[160:163], v[200:203], v[34:37]
	s_barrier
	s_add_u32 s48, s34, 0x40000
	s_addc_u32 s49, s35, 0
	s_add_i32 s50, s50, s8
	v_lshl_add_u64 v[148:149], s[48:49], 0, v[98:99]
	s_mov_b32 m0, s50
	s_nop 0
	global_load_lds_dwordx4 v[148:149], off
	v_lshl_add_u64 v[148:149], s[48:49], 0, v[132:133]
	s_add_i32 m0, s50, 0x2000
	s_nop 0
	global_load_lds_dwordx4 v[148:149], off
	s_waitcnt vmcnt(6)
	s_barrier
	v_mfma_i32_16x16x64_i8 v[30:33], v[204:207], v[166:169], v[30:33]
	v_mfma_i32_16x16x64_i8 v[26:29], v[230:233], v[166:169], v[26:29]
	v_mfma_i32_16x16x64_i8 v[22:25], v[204:207], v[180:183], v[22:25]
	v_mfma_i32_16x16x64_i8 v[18:21], v[230:233], v[180:183], v[18:21]
	v_mfma_i32_16x16x64_i8 v[14:17], v[204:207], v[188:191], v[14:17]
	v_mfma_i32_16x16x64_i8 v[10:13], v[230:233], v[188:191], v[10:13]
	v_mfma_i32_16x16x64_i8 v[6:9], v[204:207], v[196:199], v[6:9]
	v_mfma_i32_16x16x64_i8 v[2:5], v[230:233], v[196:199], v[2:5]
	v_mfma_i32_16x16x64_i8 v[30:33], v[208:211], v[170:173], v[30:33]
	v_mfma_i32_16x16x64_i8 v[26:29], v[236:239], v[170:173], v[26:29]
	v_mfma_i32_16x16x64_i8 v[22:25], v[208:211], v[184:187], v[22:25]
	v_mfma_i32_16x16x64_i8 v[18:21], v[236:239], v[184:187], v[18:21]
	v_mfma_i32_16x16x64_i8 v[14:17], v[208:211], v[192:195], v[14:17]
	v_mfma_i32_16x16x64_i8 v[10:13], v[236:239], v[192:195], v[10:13]
	v_mfma_i32_16x16x64_i8 v[6:9], v[208:211], v[200:203], v[6:9]
	v_mfma_i32_16x16x64_i8 v[2:5], v[236:239], v[200:203], v[2:5]
	s_add_i32 s48, 0, 0x18000
	v_add_u32_e32 v142, s48, v143
	s_barrier
	ds_read_b128 v[148:151], v142
	ds_read_b128 v[152:155], v142 offset:1024
	ds_read_b128 v[156:159], v142 offset:2048
	ds_read_b128 v[160:163], v142 offset:3072
	s_add_u32 s36, s36, 0x40000
	s_addc_u32 s37, s37, 0
	s_mov_b32 m0, s21
	v_lshl_add_u64 v[204:205], s[36:37], 0, v[136:137]
	ds_read_b128 v[166:169], v165 offset:32768
	ds_read_b128 v[170:173], v165 offset:33792
	ds_read_b128 v[180:183], v165 offset:34816
	ds_read_b128 v[184:187], v165 offset:35840
	ds_read_b128 v[188:191], v165 offset:36864
	ds_read_b128 v[192:195], v165 offset:37888
	ds_read_b128 v[196:199], v165 offset:38912
	ds_read_b128 v[200:203], v165 offset:39936
	global_load_lds_dwordx4 v[204:205], off
	v_lshl_add_u64 v[204:205], s[36:37], 0, v[134:135]
	s_mov_b32 m0, s33
	s_nop 0
	global_load_lds_dwordx4 v[204:205], off
	s_waitcnt lgkmcnt(8)
	s_barrier
	v_add_u32_e32 v250, 0x1c000, v143
	ds_read_b128 v[204:207], v250
	ds_read_b128 v[208:211], v250 offset:1024
	ds_read_b128 v[230:233], v250 offset:2048
	ds_read_b128 v[236:239], v250 offset:3072
	s_waitcnt lgkmcnt(4)
	s_waitcnt lgkmcnt(4)
	v_mfma_i32_16x16x64_i8 v[128:131], v[148:151], v[166:169], v[128:131]
	v_mfma_i32_16x16x64_i8 v[124:127], v[156:159], v[166:169], v[124:127]
	v_mfma_i32_16x16x64_i8 v[120:123], v[148:151], v[180:183], v[120:123]
	v_mfma_i32_16x16x64_i8 v[116:119], v[156:159], v[180:183], v[116:119]
	v_mfma_i32_16x16x64_i8 v[112:115], v[148:151], v[188:191], v[112:115]
	v_mfma_i32_16x16x64_i8 v[108:111], v[156:159], v[188:191], v[108:111]
	v_mfma_i32_16x16x64_i8 v[104:107], v[148:151], v[196:199], v[104:107]
	v_mfma_i32_16x16x64_i8 v[100:103], v[156:159], v[196:199], v[100:103]
	v_mfma_i32_16x16x64_i8 v[128:131], v[152:155], v[170:173], v[128:131]
	v_mfma_i32_16x16x64_i8 v[124:127], v[160:163], v[170:173], v[124:127]
	v_mfma_i32_16x16x64_i8 v[120:123], v[152:155], v[184:187], v[120:123]
	v_mfma_i32_16x16x64_i8 v[116:119], v[160:163], v[184:187], v[116:119]
	v_mfma_i32_16x16x64_i8 v[112:115], v[152:155], v[192:195], v[112:115]
	v_mfma_i32_16x16x64_i8 v[108:111], v[160:163], v[192:195], v[108:111]
	v_mfma_i32_16x16x64_i8 v[104:107], v[152:155], v[200:203], v[104:107]
	v_mfma_i32_16x16x64_i8 v[100:103], v[160:163], v[200:203], v[100:103]
	s_barrier
	s_add_i32 s36, 0, 0x1c000
	s_add_i32 s37, s48, s8
	v_add_u32_e32 v142, s36, v143
	v_lshl_add_u64 v[144:145], v[144:145], 0, s[68:69]
	s_mov_b32 m0, s37
	global_load_lds_dwordx4 v[144:145], off
	v_lshl_add_u64 v[144:145], v[174:175], 0, s[68:69]
	s_add_i32 m0, s37, 0x2000
	s_nop 0
	global_load_lds_dwordx4 v[144:145], off
	s_barrier
	s_waitcnt lgkmcnt(0)
	s_waitcnt lgkmcnt(0)
	v_mfma_i32_16x16x64_i8 v[94:97], v[204:207], v[166:169], v[94:97]
	v_mfma_i32_16x16x64_i8 v[90:93], v[230:233], v[166:169], v[90:93]
	v_mfma_i32_16x16x64_i8 v[86:89], v[204:207], v[180:183], v[86:89]
	v_mfma_i32_16x16x64_i8 v[82:85], v[230:233], v[180:183], v[82:85]
	v_mfma_i32_16x16x64_i8 v[78:81], v[204:207], v[188:191], v[78:81]
	v_mfma_i32_16x16x64_i8 v[74:77], v[230:233], v[188:191], v[74:77]
	v_mfma_i32_16x16x64_i8 v[70:73], v[204:207], v[196:199], v[70:73]
	v_mfma_i32_16x16x64_i8 v[66:69], v[230:233], v[196:199], v[66:69]
	v_mfma_i32_16x16x64_i8 v[94:97], v[208:211], v[170:173], v[94:97]
	v_mfma_i32_16x16x64_i8 v[90:93], v[236:239], v[170:173], v[90:93]
	v_mfma_i32_16x16x64_i8 v[86:89], v[208:211], v[184:187], v[86:89]
	v_mfma_i32_16x16x64_i8 v[82:85], v[236:239], v[184:187], v[82:85]
	v_mfma_i32_16x16x64_i8 v[78:81], v[208:211], v[192:195], v[78:81]
	v_mfma_i32_16x16x64_i8 v[74:77], v[236:239], v[192:195], v[74:77]
	v_mfma_i32_16x16x64_i8 v[70:73], v[208:211], v[200:203], v[70:73]
	v_mfma_i32_16x16x64_i8 v[66:69], v[236:239], v[200:203], v[66:69]
	s_mov_b32 m0, s38
	v_lshl_add_u64 v[144:145], v[176:177], 0, s[68:69]
	s_barrier
	ds_read_b128 v[166:169], v165 offset:49152
	ds_read_b128 v[170:173], v165 offset:50176
	ds_read_b128 v[180:183], v165 offset:51200
	ds_read_b128 v[184:187], v165 offset:52224
	ds_read_b128 v[188:191], v165 offset:53248
	ds_read_b128 v[192:195], v165 offset:54272
	ds_read_b128 v[196:199], v165 offset:55296
	ds_read_b128 v[200:203], v165 offset:56320
	global_load_lds_dwordx4 v[144:145], off
	v_lshl_add_u64 v[144:145], v[178:179], 0, s[68:69]
	s_mov_b32 m0, s39
	s_nop 0
	global_load_lds_dwordx4 v[144:145], off
	s_barrier
	s_waitcnt lgkmcnt(0)
	s_waitcnt lgkmcnt(0)
	v_mfma_i32_16x16x64_i8 v[62:65], v[148:151], v[166:169], v[62:65]
	v_mfma_i32_16x16x64_i8 v[58:61], v[156:159], v[166:169], v[58:61]
	v_mfma_i32_16x16x64_i8 v[54:57], v[148:151], v[180:183], v[54:57]
	v_mfma_i32_16x16x64_i8 v[50:53], v[156:159], v[180:183], v[50:53]
	v_mfma_i32_16x16x64_i8 v[46:49], v[148:151], v[188:191], v[46:49]
	v_mfma_i32_16x16x64_i8 v[42:45], v[156:159], v[188:191], v[42:45]
	v_mfma_i32_16x16x64_i8 v[38:41], v[148:151], v[196:199], v[38:41]
	v_mfma_i32_16x16x64_i8 v[34:37], v[156:159], v[196:199], v[34:37]
	v_mfma_i32_16x16x64_i8 v[62:65], v[152:155], v[170:173], v[62:65]
	v_mfma_i32_16x16x64_i8 v[58:61], v[160:163], v[170:173], v[58:61]
	v_mfma_i32_16x16x64_i8 v[54:57], v[152:155], v[184:187], v[54:57]
	v_mfma_i32_16x16x64_i8 v[50:53], v[160:163], v[184:187], v[50:53]
	v_mfma_i32_16x16x64_i8 v[46:49], v[152:155], v[192:195], v[46:49]
	v_mfma_i32_16x16x64_i8 v[42:45], v[160:163], v[192:195], v[42:45]
	v_mfma_i32_16x16x64_i8 v[38:41], v[152:155], v[200:203], v[38:41]
	v_mfma_i32_16x16x64_i8 v[34:37], v[160:163], v[200:203], v[34:37]
	s_barrier
	s_add_u32 s34, s34, 0x40080
	s_addc_u32 s35, s35, 0
	s_add_i32 s36, s36, s8
	v_lshl_add_u64 v[144:145], s[34:35], 0, v[98:99]
	s_mov_b32 m0, s36
	s_nop 0
	global_load_lds_dwordx4 v[144:145], off
	v_lshl_add_u64 v[144:145], s[34:35], 0, v[132:133]
	s_add_i32 m0, s36, 0x2000
	s_nop 0
	global_load_lds_dwordx4 v[144:145], off
	s_waitcnt vmcnt(6)
	s_barrier
	v_mfma_i32_16x16x64_i8 v[30:33], v[204:207], v[166:169], v[30:33]
	v_mfma_i32_16x16x64_i8 v[26:29], v[230:233], v[166:169], v[26:29]
	v_mfma_i32_16x16x64_i8 v[22:25], v[204:207], v[180:183], v[22:25]
	v_mfma_i32_16x16x64_i8 v[18:21], v[230:233], v[180:183], v[18:21]
	v_mfma_i32_16x16x64_i8 v[14:17], v[204:207], v[188:191], v[14:17]
	v_mfma_i32_16x16x64_i8 v[10:13], v[230:233], v[188:191], v[10:13]
	v_mfma_i32_16x16x64_i8 v[6:9], v[204:207], v[196:199], v[6:9]
	v_mfma_i32_16x16x64_i8 v[2:5], v[230:233], v[196:199], v[2:5]
	v_mfma_i32_16x16x64_i8 v[30:33], v[208:211], v[170:173], v[30:33]
	v_mfma_i32_16x16x64_i8 v[26:29], v[236:239], v[170:173], v[26:29]
	v_mfma_i32_16x16x64_i8 v[22:25], v[208:211], v[184:187], v[22:25]
	v_mfma_i32_16x16x64_i8 v[18:21], v[236:239], v[184:187], v[18:21]
	v_mfma_i32_16x16x64_i8 v[14:17], v[208:211], v[192:195], v[14:17]
	v_mfma_i32_16x16x64_i8 v[10:13], v[236:239], v[192:195], v[10:13]
	v_mfma_i32_16x16x64_i8 v[6:9], v[208:211], v[200:203], v[6:9]
	v_mfma_i32_16x16x64_i8 v[2:5], v[236:239], v[200:203], v[2:5]
	s_add_i32 s47, s47, 2
	s_add_u32 s30, s30, 0x100
	s_addc_u32 s31, s31, 0
	s_add_u32 s45, s45, 0x100
	s_addc_u32 s46, s46, 0
	s_cmp_gt_u32 s47, 13
	s_barrier
	s_cbranch_scc0 .LBB0_545
	v_lshl_add_u32 v144, s42, 8, v1
	v_or_b32_e32 v182, 16, v144
	v_ashrrev_i32_e32 v145, 31, v144
	v_ashrrev_i32_e32 v183, 31, v182
	v_or_b32_e32 v174, 32, v144
	v_lshl_add_u64 v[148:149], v[144:145], 2, s[54:55]
	v_lshl_add_u64 v[150:151], v[182:183], 2, s[54:55]
	v_ashrrev_i32_e32 v175, 31, v174
	v_or_b32_e32 v170, 48, v144
	v_lshl_or_b32 v186, s41, 8, v147
	global_load_dword v184, v[148:149], off
	global_load_dword v180, v[150:151], off
	v_lshl_add_u64 v[150:151], v[174:175], 2, s[54:55]
	v_ashrrev_i32_e32 v171, 31, v170
	v_ashrrev_i32_e32 v187, 31, v186
	global_load_dword v172, v[150:151], off
	v_lshl_add_u64 v[150:151], v[170:171], 2, s[54:55]
	v_lshl_add_u64 v[158:159], v[186:187], 2, s[18:19]
	global_load_dword v168, v[150:151], off
	global_load_dword v166, v[148:149], off offset:512
	global_load_dword v164, v[148:149], off offset:576
	global_load_dword v146, v[148:149], off offset:640
	global_load_dword v142, v[148:149], off offset:704
	global_load_dwordx4 v[154:157], v[158:159], off offset:16
	global_load_dwordx4 v[150:153], v[158:159], off
	global_load_dwordx4 v[188:191], v[158:159], off offset:528
	s_nop 0
	global_load_dwordx4 v[158:161], v[158:159], off offset:512
	v_cvt_f32_i32_e32 v129, v129
	v_cvt_f32_i32_e32 v128, v128
	v_cvt_f32_i32_e32 v127, v127
	v_cvt_f32_i32_e32 v126, v126
	v_cvt_f32_i32_e32 v131, v131
	v_cvt_f32_i32_e32 v130, v130
	v_readlane_b32 s30, v252, 59
	v_cvt_f32_i32_e32 v177, v125
	v_cvt_f32_i32_e32 v176, v124
	v_readlane_b32 s31, v252, 60
	v_cvt_f32_i32_e32 v97, v97
	v_cvt_f32_i32_e32 v96, v96
	v_cvt_f32_i32_e32 v179, v95
	v_cvt_f32_i32_e32 v178, v94
	v_cvt_f32_i32_e32 v95, v93
	v_cvt_f32_i32_e32 v94, v92
	v_cvt_f32_i32_e32 v93, v79
	v_cvt_f32_i32_e32 v92, v78
	v_cvt_f32_i32_e32 v79, v77
	v_cvt_f32_i32_e32 v78, v76
	v_cvt_f32_i32_e32 v77, v71
	v_cvt_f32_i32_e32 v76, v70
	v_cvt_f32_i32_e32 v71, v69
	v_cvt_f32_i32_e32 v70, v68
	v_cvt_f32_i32_e32 v69, v63
	v_cvt_f32_i32_e32 v68, v62
	v_cvt_f32_i32_e32 v63, v59
	v_cvt_f32_i32_e32 v62, v58
	v_cvt_f32_i32_e32 v59, v27
	v_cvt_f32_i32_e32 v58, v26
	v_cvt_f32_i32_e32 v27, v19
	v_cvt_f32_i32_e32 v26, v18
	v_cvt_f32_i32_e32 v19, v11
	v_cvt_f32_i32_e32 v18, v10
	v_mov_b64_e32 v[10:11], s[30:31]
	s_movk_i32 s23, 0x3200
	v_cvt_f32_i32_e32 v125, v91
	v_cvt_f32_i32_e32 v124, v90
	v_cvt_f32_i32_e32 v91, v75
	v_cvt_f32_i32_e32 v90, v74
	v_cvt_f32_i32_e32 v75, v67
	v_cvt_f32_i32_e32 v74, v66
	v_cvt_f32_i32_e32 v67, v31
	v_cvt_f32_i32_e32 v66, v30
	v_cvt_f32_i32_e32 v31, v29
	v_cvt_f32_i32_e32 v30, v28
	v_cvt_f32_i32_e32 v29, v23
	v_cvt_f32_i32_e32 v28, v22
	v_cvt_f32_i32_e32 v23, v21
	v_cvt_f32_i32_e32 v22, v20
	v_cvt_f32_i32_e32 v21, v15
	v_cvt_f32_i32_e32 v20, v14
	v_cvt_f32_i32_e32 v15, v13
	v_cvt_f32_i32_e32 v14, v12
	v_lshlrev_b64 v[12:13], 1, v[186:187]
	v_cvt_f32_i32_e32 v121, v121
	v_cvt_f32_i32_e32 v120, v120
	v_cvt_f32_i32_e32 v123, v123
	v_cvt_f32_i32_e32 v122, v122
	v_cvt_f32_i32_e32 v119, v119
	v_cvt_f32_i32_e32 v118, v118
	v_cvt_f32_i32_e32 v117, v117
	v_cvt_f32_i32_e32 v116, v116
	v_cvt_f32_i32_e32 v89, v89
	v_cvt_f32_i32_e32 v88, v88
	v_cvt_f32_i32_e32 v87, v87
	v_cvt_f32_i32_e32 v86, v86
	v_cvt_f32_i32_e32 v85, v85
	s_waitcnt vmcnt(0)
	v_pk_mul_f32 v[128:129], v[184:185], v[128:129] op_sel_hi:[0,1]
	v_pk_mul_f32 v[126:127], v[184:185], v[126:127] op_sel_hi:[0,1]
	v_pk_mul_f32 v[130:131], v[184:185], v[130:131] op_sel_hi:[0,1]
	v_pk_mul_f32 v[176:177], v[184:185], v[176:177] op_sel_hi:[0,1]
	v_pk_mul_f32 v[96:97], v[184:185], v[96:97] op_sel_hi:[0,1]
	v_pk_mul_f32 v[94:95], v[184:185], v[94:95] op_sel_hi:[0,1]
	v_cvt_f32_i32_e32 v84, v84
	v_cvt_f32_i32_e32 v83, v83
	v_cvt_f32_i32_e32 v82, v82
	v_pk_mul_f32 v[154:155], v[154:155], s[58:59] op_sel_hi:[1,0]
	v_pk_mul_f32 v[148:149], v[152:153], s[58:59] op_sel_hi:[1,0]
	v_pk_mul_f32 v[150:151], v[150:151], s[58:59] op_sel_hi:[1,0]
	v_pk_mul_f32 v[152:153], v[156:157], s[58:59] op_sel_hi:[1,0]
	v_pk_mul_f32 v[162:163], v[188:189], s[58:59] op_sel_hi:[1,0]
	v_mad_i64_i32 v[188:189], s[30:31], v144, s23, v[10:11]
	v_lshl_add_u64 v[186:187], v[188:189], 0, v[12:13]
	v_pk_mul_f32 v[188:189], v[152:153], v[126:127]
	v_pk_mul_f32 v[126:127], v[150:151], v[128:129]
	v_pk_mul_f32 v[130:131], v[148:149], v[130:131]
	v_cvt_pk_bf16_f32 v126, v126, v127
	v_pk_mul_f32 v[156:157], v[160:161], s[58:59] op_sel_hi:[1,0]
	v_cvt_pk_bf16_f32 v127, v130, v131
	v_pk_mul_f32 v[158:159], v[158:159], s[58:59] op_sel_hi:[1,0]
	v_pk_mul_f32 v[160:161], v[190:191], s[58:59] op_sel_hi:[1,0]
	v_pk_mul_f32 v[176:177], v[154:155], v[176:177]
	v_pk_mul_f32 v[124:125], v[184:185], v[124:125] op_sel_hi:[0,1]
	v_cvt_pk_bf16_f32 v128, v176, v177
	v_cvt_pk_bf16_f32 v129, v188, v189
	global_store_dwordx4 v[186:187], v[126:129], off
	v_pk_mul_f32 v[96:97], v[156:157], v[96:97]
	v_pk_mul_f32 v[124:125], v[162:163], v[124:125]
	v_pk_mul_f32 v[126:127], v[184:185], v[178:179] op_sel_hi:[0,1]
	v_pk_mul_f32 v[126:127], v[158:159], v[126:127]
	v_pk_mul_f32 v[128:129], v[160:161], v[94:95]
	v_cvt_pk_bf16_f32 v94, v126, v127
	v_cvt_pk_bf16_f32 v95, v96, v97
	v_cvt_pk_bf16_f32 v96, v124, v125
	v_cvt_f32_i32_e32 v113, v113
	v_cvt_pk_bf16_f32 v97, v128, v129
	global_store_dwordx4 v[186:187], v[94:97], off offset:256
	v_cvt_f32_i32_e32 v112, v112
	v_cvt_f32_i32_e32 v115, v115
	v_mad_i64_i32 v[94:95], s[30:31], v182, s23, v[10:11]
	v_lshl_add_u64 v[124:125], v[94:95], 0, v[12:13]
	v_pk_mul_f32 v[94:95], v[180:181], v[120:121] op_sel_hi:[0,1]
	v_pk_mul_f32 v[96:97], v[180:181], v[122:123] op_sel_hi:[0,1]
	v_pk_mul_f32 v[94:95], v[150:151], v[94:95]
	v_cvt_f32_i32_e32 v114, v114
	v_pk_mul_f32 v[116:117], v[180:181], v[116:117] op_sel_hi:[0,1]
	v_pk_mul_f32 v[118:119], v[180:181], v[118:119] op_sel_hi:[0,1]
	v_pk_mul_f32 v[96:97], v[148:149], v[96:97]
	v_cvt_pk_bf16_f32 v94, v94, v95
	v_pk_mul_f32 v[86:87], v[180:181], v[86:87] op_sel_hi:[0,1]
	v_cvt_pk_bf16_f32 v95, v96, v97
	v_pk_mul_f32 v[88:89], v[180:181], v[88:89] op_sel_hi:[0,1]
	v_pk_mul_f32 v[82:83], v[180:181], v[82:83] op_sel_hi:[0,1]
	v_pk_mul_f32 v[84:85], v[180:181], v[84:85] op_sel_hi:[0,1]
	v_cvt_f32_i32_e32 v111, v111
	v_cvt_f32_i32_e32 v110, v110
	v_cvt_f32_i32_e32 v109, v109
	v_cvt_f32_i32_e32 v108, v108
	v_pk_mul_f32 v[118:119], v[152:153], v[118:119]
	v_pk_mul_f32 v[116:117], v[154:155], v[116:117]
	v_pk_mul_f32 v[88:89], v[156:157], v[88:89]
	v_cvt_pk_bf16_f32 v96, v116, v117
	v_cvt_pk_bf16_f32 v97, v118, v119
	global_store_dwordx4 v[124:125], v[94:97], off
	v_pk_mul_f32 v[86:87], v[158:159], v[86:87]
	v_cvt_f32_i32_e32 v81, v81
	v_pk_mul_f32 v[94:95], v[160:161], v[84:85]
	v_pk_mul_f32 v[84:85], v[162:163], v[82:83]
	v_cvt_pk_bf16_f32 v82, v86, v87
	v_cvt_pk_bf16_f32 v83, v88, v89
	v_cvt_f32_i32_e32 v80, v80
	v_cvt_pk_bf16_f32 v84, v84, v85
	v_cvt_pk_bf16_f32 v85, v94, v95
	global_store_dwordx4 v[124:125], v[82:85], off offset:256
	v_cvt_f32_i32_e32 v105, v105
	v_cvt_f32_i32_e32 v104, v104
	v_mad_i64_i32 v[82:83], s[30:31], v174, s23, v[10:11]
	v_lshl_add_u64 v[86:87], v[82:83], 0, v[12:13]
	v_pk_mul_f32 v[82:83], v[172:173], v[112:113] op_sel_hi:[0,1]
	v_pk_mul_f32 v[84:85], v[172:173], v[114:115] op_sel_hi:[0,1]
	v_pk_mul_f32 v[82:83], v[150:151], v[82:83]
	v_pk_mul_f32 v[88:89], v[172:173], v[108:109] op_sel_hi:[0,1]
	v_pk_mul_f32 v[94:95], v[172:173], v[110:111] op_sel_hi:[0,1]
	v_pk_mul_f32 v[84:85], v[148:149], v[84:85]
	v_cvt_pk_bf16_f32 v82, v82, v83
	v_cvt_f32_i32_e32 v107, v107
	v_cvt_pk_bf16_f32 v83, v84, v85
	v_cvt_f32_i32_e32 v106, v106
	v_cvt_f32_i32_e32 v73, v73
	v_cvt_f32_i32_e32 v72, v72
	v_pk_mul_f32 v[94:95], v[152:153], v[94:95]
	v_pk_mul_f32 v[88:89], v[154:155], v[88:89]
	v_pk_mul_f32 v[80:81], v[172:173], v[80:81] op_sel_hi:[0,1]
	v_cvt_pk_bf16_f32 v84, v88, v89
	v_cvt_pk_bf16_f32 v85, v94, v95
	global_store_dwordx4 v[86:87], v[82:85], off
	v_pk_mul_f32 v[78:79], v[172:173], v[78:79] op_sel_hi:[0,1]
	v_cvt_f32_i32_e32 v103, v103
	v_pk_mul_f32 v[82:83], v[172:173], v[92:93] op_sel_hi:[0,1]
	v_cvt_f32_i32_e32 v102, v102
	v_cvt_f32_i32_e32 v101, v101
	v_cvt_f32_i32_e32 v100, v100
	v_pk_mul_f32 v[84:85], v[172:173], v[90:91] op_sel_hi:[0,1]
	v_pk_mul_f32 v[80:81], v[156:157], v[80:81]
	v_pk_mul_f32 v[82:83], v[158:159], v[82:83]
	v_pk_mul_f32 v[88:89], v[160:161], v[78:79]
	v_cvt_pk_bf16_f32 v78, v82, v83
	v_cvt_pk_bf16_f32 v79, v80, v81
	v_cvt_f32_i32_e32 v61, v61
	v_cvt_f32_i32_e32 v60, v60
	v_pk_mul_f32 v[84:85], v[162:163], v[84:85]
	v_cvt_f32_i32_e32 v65, v65
	v_cvt_pk_bf16_f32 v80, v84, v85
	v_cvt_pk_bf16_f32 v81, v88, v89
	global_store_dwordx4 v[86:87], v[78:81], off offset:256
	v_cvt_f32_i32_e32 v64, v64
	v_pk_mul_f32 v[72:73], v[168:169], v[72:73] op_sel_hi:[0,1]
	v_mad_i64_i32 v[78:79], s[30:31], v170, s23, v[10:11]
	v_lshl_add_u64 v[82:83], v[78:79], 0, v[12:13]
	v_pk_mul_f32 v[78:79], v[168:169], v[104:105] op_sel_hi:[0,1]
	v_pk_mul_f32 v[80:81], v[168:169], v[106:107] op_sel_hi:[0,1]
	v_pk_mul_f32 v[78:79], v[150:151], v[78:79]
	v_cvt_f32_i32_e32 v33, v33
	v_cvt_f32_i32_e32 v32, v32
	v_pk_mul_f32 v[84:85], v[168:169], v[100:101] op_sel_hi:[0,1]
	v_pk_mul_f32 v[86:87], v[168:169], v[102:103] op_sel_hi:[0,1]
	v_pk_mul_f32 v[80:81], v[148:149], v[80:81]
	v_cvt_pk_bf16_f32 v78, v78, v79
	v_pk_mul_f32 v[76:77], v[168:169], v[76:77] op_sel_hi:[0,1]
	v_cvt_pk_bf16_f32 v79, v80, v81
	v_pk_mul_f32 v[74:75], v[168:169], v[74:75] op_sel_hi:[0,1]
	v_pk_mul_f32 v[70:71], v[168:169], v[70:71] op_sel_hi:[0,1]
	v_pk_mul_f32 v[72:73], v[156:157], v[72:73]
	v_add_u32_e32 v145, 0x80, v144
	v_pk_mul_f32 v[86:87], v[152:153], v[86:87]
	v_pk_mul_f32 v[84:85], v[154:155], v[84:85]
	v_pk_mul_f32 v[76:77], v[158:159], v[76:77]
	v_cvt_pk_bf16_f32 v80, v84, v85
	v_cvt_pk_bf16_f32 v81, v86, v87
	global_store_dwordx4 v[82:83], v[78:81], off
	v_pk_mul_f32 v[74:75], v[162:163], v[74:75]
	v_pk_mul_f32 v[68:69], v[166:167], v[68:69] op_sel_hi:[0,1]
	v_pk_mul_f32 v[78:79], v[160:161], v[70:71]
	v_cvt_pk_bf16_f32 v70, v76, v77
	v_cvt_pk_bf16_f32 v71, v72, v73
	v_cvt_pk_bf16_f32 v72, v74, v75
	v_pk_mul_f32 v[60:61], v[166:167], v[60:61] op_sel_hi:[0,1]
	v_cvt_pk_bf16_f32 v73, v78, v79
	global_store_dwordx4 v[82:83], v[70:73], off offset:256
	v_pk_mul_f32 v[64:65], v[166:167], v[64:65] op_sel_hi:[0,1]
	v_pk_mul_f32 v[62:63], v[166:167], v[62:63] op_sel_hi:[0,1]
	v_mad_i64_i32 v[70:71], s[30:31], v145, s23, v[10:11]
	v_pk_mul_f32 v[72:73], v[152:153], v[60:61]
	v_pk_mul_f32 v[60:61], v[150:151], v[68:69]
	v_lshl_add_u64 v[70:71], v[70:71], 0, v[12:13]
	v_pk_mul_f32 v[62:63], v[154:155], v[62:63]
	v_pk_mul_f32 v[64:65], v[148:149], v[64:65]
	v_cvt_pk_bf16_f32 v60, v60, v61
	v_cvt_f32_i32_e32 v55, v55
	v_cvt_pk_bf16_f32 v61, v64, v65
	v_cvt_f32_i32_e32 v54, v54
	v_cvt_pk_bf16_f32 v62, v62, v63
	v_cvt_pk_bf16_f32 v63, v72, v73
	global_store_dwordx4 v[70:71], v[60:63], off
	v_pk_mul_f32 v[32:33], v[166:167], v[32:33] op_sel_hi:[0,1]
	v_pk_mul_f32 v[30:31], v[166:167], v[30:31] op_sel_hi:[0,1]
	v_pk_mul_f32 v[60:61], v[166:167], v[66:67] op_sel_hi:[0,1]
	v_cvt_f32_i32_e32 v57, v57
	v_cvt_f32_i32_e32 v56, v56
	v_pk_mul_f32 v[58:59], v[166:167], v[58:59] op_sel_hi:[0,1]
	v_pk_mul_f32 v[32:33], v[156:157], v[32:33]
	v_pk_mul_f32 v[60:61], v[158:159], v[60:61]
	v_pk_mul_f32 v[62:63], v[160:161], v[30:31]
	v_cvt_pk_bf16_f32 v30, v60, v61
	v_cvt_f32_i32_e32 v53, v53
	v_cvt_f32_i32_e32 v52, v52
	v_cvt_f32_i32_e32 v51, v51
	v_cvt_f32_i32_e32 v50, v50
	v_cvt_f32_i32_e32 v25, v25
	v_cvt_f32_i32_e32 v24, v24
	v_pk_mul_f32 v[58:59], v[162:163], v[58:59]
	v_cvt_pk_bf16_f32 v31, v32, v33
	v_cvt_f32_i32_e32 v47, v47
	v_cvt_pk_bf16_f32 v32, v58, v59
	v_cvt_pk_bf16_f32 v33, v62, v63
	global_store_dwordx4 v[70:71], v[30:33], off offset:256
	v_cvt_f32_i32_e32 v46, v46
	v_pk_mul_f32 v[50:51], v[164:165], v[50:51] op_sel_hi:[0,1]
	v_add_u32_e32 v30, 0x90, v144
	v_mad_i64_i32 v[30:31], s[30:31], v30, s23, v[10:11]
	v_lshl_add_u64 v[58:59], v[30:31], 0, v[12:13]
	v_pk_mul_f32 v[30:31], v[164:165], v[54:55] op_sel_hi:[0,1]
	v_pk_mul_f32 v[32:33], v[164:165], v[56:57] op_sel_hi:[0,1]
	v_pk_mul_f32 v[30:31], v[150:151], v[30:31]
	v_pk_mul_f32 v[52:53], v[164:165], v[52:53] op_sel_hi:[0,1]
	v_pk_mul_f32 v[32:33], v[148:149], v[32:33]
	v_cvt_pk_bf16_f32 v30, v30, v31
	v_pk_mul_f32 v[28:29], v[164:165], v[28:29] op_sel_hi:[0,1]
	v_cvt_pk_bf16_f32 v31, v32, v33
	v_pk_mul_f32 v[24:25], v[164:165], v[24:25] op_sel_hi:[0,1]
	v_pk_mul_f32 v[22:23], v[164:165], v[22:23] op_sel_hi:[0,1]
	v_cvt_f32_i32_e32 v49, v49
	v_cvt_f32_i32_e32 v48, v48
	v_pk_mul_f32 v[52:53], v[152:153], v[52:53]
	v_pk_mul_f32 v[50:51], v[154:155], v[50:51]
	v_pk_mul_f32 v[26:27], v[164:165], v[26:27] op_sel_hi:[0,1]
	v_cvt_pk_bf16_f32 v32, v50, v51
	v_cvt_pk_bf16_f32 v33, v52, v53
	global_store_dwordx4 v[58:59], v[30:33], off
	v_pk_mul_f32 v[24:25], v[156:157], v[24:25]
	v_pk_mul_f32 v[28:29], v[158:159], v[28:29]
	v_pk_mul_f32 v[30:31], v[160:161], v[22:23]
	v_cvt_pk_bf16_f32 v22, v28, v29
	v_cvt_f32_i32_e32 v45, v45
	v_cvt_f32_i32_e32 v44, v44
	v_cvt_f32_i32_e32 v43, v43
	v_cvt_f32_i32_e32 v42, v42
	v_cvt_f32_i32_e32 v17, v17
	v_cvt_f32_i32_e32 v16, v16
	v_pk_mul_f32 v[26:27], v[162:163], v[26:27]
	v_cvt_pk_bf16_f32 v23, v24, v25
	v_cvt_f32_i32_e32 v39, v39
	v_cvt_pk_bf16_f32 v24, v26, v27
	v_cvt_pk_bf16_f32 v25, v30, v31
	global_store_dwordx4 v[58:59], v[22:25], off offset:256
	v_cvt_f32_i32_e32 v38, v38
	v_pk_mul_f32 v[28:29], v[146:147], v[42:43] op_sel_hi:[0,1]
	v_add_u32_e32 v22, 0xa0, v144
	v_mad_i64_i32 v[22:23], s[30:31], v22, s23, v[10:11]
	v_lshl_add_u64 v[26:27], v[22:23], 0, v[12:13]
	v_pk_mul_f32 v[22:23], v[146:147], v[46:47] op_sel_hi:[0,1]
	v_pk_mul_f32 v[24:25], v[146:147], v[48:49] op_sel_hi:[0,1]
	v_pk_mul_f32 v[22:23], v[150:151], v[22:23]
	v_pk_mul_f32 v[30:31], v[146:147], v[44:45] op_sel_hi:[0,1]
	v_pk_mul_f32 v[24:25], v[148:149], v[24:25]
	v_cvt_pk_bf16_f32 v22, v22, v23
	v_pk_mul_f32 v[20:21], v[146:147], v[20:21] op_sel_hi:[0,1]
	v_cvt_pk_bf16_f32 v23, v24, v25
	v_pk_mul_f32 v[16:17], v[146:147], v[16:17] op_sel_hi:[0,1]
	v_pk_mul_f32 v[14:15], v[146:147], v[14:15] op_sel_hi:[0,1]
	v_cvt_f32_i32_e32 v41, v41
	v_cvt_f32_i32_e32 v40, v40
	v_pk_mul_f32 v[30:31], v[152:153], v[30:31]
	v_pk_mul_f32 v[28:29], v[154:155], v[28:29]
	v_pk_mul_f32 v[18:19], v[146:147], v[18:19] op_sel_hi:[0,1]
	v_cvt_pk_bf16_f32 v24, v28, v29
	v_cvt_pk_bf16_f32 v25, v30, v31
	global_store_dwordx4 v[26:27], v[22:25], off
	v_pk_mul_f32 v[16:17], v[156:157], v[16:17]
	v_pk_mul_f32 v[20:21], v[158:159], v[20:21]
	v_pk_mul_f32 v[22:23], v[160:161], v[14:15]
	v_cvt_pk_bf16_f32 v14, v20, v21
	v_cvt_f32_i32_e32 v37, v37
	v_cvt_f32_i32_e32 v36, v36
	v_cvt_f32_i32_e32 v35, v35
	v_cvt_f32_i32_e32 v34, v34
	v_cvt_f32_i32_e32 v5, v5
	v_cvt_f32_i32_e32 v4, v4
	v_cvt_f32_i32_e32 v3, v3
	v_cvt_f32_i32_e32 v2, v2
	v_pk_mul_f32 v[18:19], v[162:163], v[18:19]
	v_cvt_pk_bf16_f32 v15, v16, v17
	v_cvt_f32_i32_e32 v9, v9
	v_cvt_pk_bf16_f32 v16, v18, v19
	v_cvt_pk_bf16_f32 v17, v22, v23
	global_store_dwordx4 v[26:27], v[14:17], off offset:256
	v_cvt_f32_i32_e32 v8, v8
	v_cvt_f32_i32_e32 v7, v7
	v_add_u32_e32 v14, 0xb0, v144
	v_cvt_f32_i32_e32 v6, v6
	v_mad_i64_i32 v[10:11], s[30:31], v14, s23, v[10:11]
	v_lshl_add_u64 v[14:15], v[10:11], 0, v[12:13]
	v_pk_mul_f32 v[10:11], v[142:143], v[38:39] op_sel_hi:[0,1]
	v_pk_mul_f32 v[12:13], v[142:143], v[40:41] op_sel_hi:[0,1]
	v_pk_mul_f32 v[10:11], v[150:151], v[10:11]
	v_pk_mul_f32 v[16:17], v[142:143], v[34:35] op_sel_hi:[0,1]
	v_pk_mul_f32 v[18:19], v[142:143], v[36:37] op_sel_hi:[0,1]
	v_pk_mul_f32 v[12:13], v[148:149], v[12:13]
	v_cvt_pk_bf16_f32 v10, v10, v11
	v_pk_mul_f32 v[2:3], v[142:143], v[2:3] op_sel_hi:[0,1]
	v_cvt_pk_bf16_f32 v11, v12, v13
	v_pk_mul_f32 v[4:5], v[142:143], v[4:5] op_sel_hi:[0,1]
	v_pk_mul_f32 v[18:19], v[152:153], v[18:19]
	v_pk_mul_f32 v[16:17], v[154:155], v[16:17]
	v_pk_mul_f32 v[6:7], v[142:143], v[6:7] op_sel_hi:[0,1]
	v_cvt_pk_bf16_f32 v12, v16, v17
	v_cvt_pk_bf16_f32 v13, v18, v19
	global_store_dwordx4 v[14:15], v[10:13], off
	v_pk_mul_f32 v[8:9], v[142:143], v[8:9] op_sel_hi:[0,1]
	s_and_b64 vcc, exec, s[0:1]
	v_pk_mul_f32 v[10:11], v[160:161], v[4:5]
	v_pk_mul_f32 v[4:5], v[162:163], v[2:3]
	s_mov_b32 s42, s24
	s_mov_b32 s41, s22
	s_mov_b64 s[34:35], s[28:29]
	s_mov_b64 s[30:31], s[26:27]
	v_pk_mul_f32 v[8:9], v[156:157], v[8:9]
	v_pk_mul_f32 v[6:7], v[158:159], v[6:7]
	s_nop 0
	v_cvt_pk_bf16_f32 v2, v6, v7
	v_cvt_pk_bf16_f32 v3, v8, v9
	v_cvt_pk_bf16_f32 v4, v4, v5
	v_cvt_pk_bf16_f32 v5, v10, v11
	global_store_dwordx4 v[14:15], v[2:5], off offset:256
	s_cbranch_vccz .LBB0_538
	s_waitcnt vmcnt(0)
	s_cmpk_gt_u32 s3, 0xff
	s_cbranch_scc1 .LBB0_549
	s_barrier

.LBB0_690:
	s_add_u32 s26, s24, 0x100
	s_addc_u32 s27, s25, 0
	s_add_i32 s45, 0, 0x10000
	v_add_u32_e32 v142, s45, v143
	ds_read_b128 v[146:149], v142
	ds_read_b128 v[152:155], v142 offset:1024
	ds_read_b128 v[156:159], v142 offset:2048
	ds_read_b128 v[160:163], v142 offset:3072
	s_cmp_eq_u32 s44, 6
	s_cselect_b32 s31, s19, s27
	s_cselect_b32 s30, s18, s26
	s_cselect_b32 s29, s23, s43
	s_cselect_b32 s28, s22, s42
	v_lshl_add_u64 v[176:177], s[24:25], 0, v[138:139]
	s_add_i32 m0, s9, 0xc000
	ds_read_b128 v[164:167], v151
	ds_read_b128 v[168:171], v151 offset:1024
	ds_read_b128 v[172:175], v151 offset:2048
	ds_read_b128 v[180:183], v151 offset:3072
	ds_read_b128 v[184:187], v151 offset:4096
	ds_read_b128 v[188:191], v151 offset:5120
	ds_read_b128 v[192:195], v151 offset:6144
	ds_read_b128 v[196:199], v151 offset:7168
	global_load_lds_dwordx4 v[176:177], off
	v_lshl_add_u64 v[176:177], s[24:25], 0, v[140:141]
	s_add_i32 m0, s9, 0xe000
	s_nop 0
	global_load_lds_dwordx4 v[176:177], off
	s_waitcnt lgkmcnt(8)
	s_barrier
	v_add_u32_e32 v250, 0x14000, v143
	ds_read_b128 v[200:203], v250
	ds_read_b128 v[204:207], v250 offset:1024
	ds_read_b128 v[208:211], v250 offset:2048
	ds_read_b128 v[230:233], v250 offset:3072
	s_waitcnt lgkmcnt(4)
	s_waitcnt lgkmcnt(4)
	v_mfma_f32_16x16x32_bf16 v[128:131], v[146:149], v[164:167], v[128:131]
	v_mfma_f32_16x16x32_bf16 v[124:127], v[156:159], v[164:167], v[124:127]
	v_mfma_f32_16x16x32_bf16 v[112:115], v[146:149], v[172:175], v[112:115]
	v_mfma_f32_16x16x32_bf16 v[108:111], v[156:159], v[172:175], v[108:111]
	v_mfma_f32_16x16x32_bf16 v[94:97], v[146:149], v[184:187], v[94:97]
	v_mfma_f32_16x16x32_bf16 v[90:93], v[156:159], v[184:187], v[90:93]
	v_mfma_f32_16x16x32_bf16 v[78:81], v[146:149], v[192:195], v[78:81]
	v_mfma_f32_16x16x32_bf16 v[74:77], v[156:159], v[192:195], v[74:77]
	v_mfma_f32_16x16x32_bf16 v[128:131], v[152:155], v[168:171], v[128:131]
	v_mfma_f32_16x16x32_bf16 v[124:127], v[160:163], v[168:171], v[124:127]
	v_mfma_f32_16x16x32_bf16 v[112:115], v[152:155], v[180:183], v[112:115]
	v_mfma_f32_16x16x32_bf16 v[108:111], v[160:163], v[180:183], v[108:111]
	v_mfma_f32_16x16x32_bf16 v[94:97], v[152:155], v[188:191], v[94:97]
	v_mfma_f32_16x16x32_bf16 v[90:93], v[160:163], v[188:191], v[90:93]
	v_mfma_f32_16x16x32_bf16 v[78:81], v[152:155], v[196:199], v[78:81]
	v_mfma_f32_16x16x32_bf16 v[74:77], v[160:163], v[196:199], v[74:77]
	s_barrier
	s_add_i32 s46, 0, 0x14000
	s_add_i32 s24, s45, s8
	v_add_u32_e32 v142, s46, v143
	v_lshl_add_u64 v[176:177], s[28:29], 0, v[98:99]
	s_mov_b32 m0, s24
	global_load_lds_dwordx4 v[176:177], off
	v_lshl_add_u64 v[178:179], s[28:29], 0, v[132:133]
	s_add_i32 m0, s24, 0x2000
	s_nop 0
	global_load_lds_dwordx4 v[178:179], off
	s_barrier
	s_waitcnt lgkmcnt(0)
	s_waitcnt lgkmcnt(0)
	v_mfma_f32_16x16x32_bf16 v[120:123], v[200:203], v[164:167], v[120:123]
	v_mfma_f32_16x16x32_bf16 v[116:119], v[208:211], v[164:167], v[116:119]
	v_mfma_f32_16x16x32_bf16 v[104:107], v[200:203], v[172:175], v[104:107]
	v_mfma_f32_16x16x32_bf16 v[100:103], v[208:211], v[172:175], v[100:103]
	v_mfma_f32_16x16x32_bf16 v[86:89], v[200:203], v[184:187], v[86:89]
	v_mfma_f32_16x16x32_bf16 v[82:85], v[208:211], v[184:187], v[82:85]
	v_mfma_f32_16x16x32_bf16 v[70:73], v[200:203], v[192:195], v[70:73]
	v_mfma_f32_16x16x32_bf16 v[66:69], v[208:211], v[192:195], v[66:69]
	v_mfma_f32_16x16x32_bf16 v[120:123], v[204:207], v[168:171], v[120:123]
	v_mfma_f32_16x16x32_bf16 v[116:119], v[230:233], v[168:171], v[116:119]
	v_mfma_f32_16x16x32_bf16 v[104:107], v[204:207], v[180:183], v[104:107]
	v_mfma_f32_16x16x32_bf16 v[100:103], v[230:233], v[180:183], v[100:103]
	v_mfma_f32_16x16x32_bf16 v[86:89], v[204:207], v[188:191], v[86:89]
	v_mfma_f32_16x16x32_bf16 v[82:85], v[230:233], v[188:191], v[82:85]
	v_mfma_f32_16x16x32_bf16 v[70:73], v[204:207], v[196:199], v[70:73]
	v_mfma_f32_16x16x32_bf16 v[66:69], v[230:233], v[196:199], v[66:69]
	s_mov_b32 m0, s9
	v_lshl_add_u64 v[212:213], s[30:31], 0, v[136:137]
	s_barrier
	ds_read_b128 v[164:167], v151 offset:16384
	ds_read_b128 v[168:171], v151 offset:17408
	ds_read_b128 v[172:175], v151 offset:18432
	ds_read_b128 v[180:183], v151 offset:19456
	ds_read_b128 v[184:187], v151 offset:20480
	ds_read_b128 v[188:191], v151 offset:21504
	ds_read_b128 v[192:195], v151 offset:22528
	ds_read_b128 v[196:199], v151 offset:23552
	global_load_lds_dwordx4 v[212:213], off
	v_lshl_add_u64 v[214:215], s[30:31], 0, v[134:135]
	s_mov_b32 m0, s20
	s_nop 0
	global_load_lds_dwordx4 v[214:215], off
	s_barrier
	s_waitcnt lgkmcnt(0)
	s_waitcnt lgkmcnt(0)
	v_mfma_f32_16x16x32_bf16 v[62:65], v[146:149], v[164:167], v[62:65]
	v_mfma_f32_16x16x32_bf16 v[58:61], v[156:159], v[164:167], v[58:61]
	v_mfma_f32_16x16x32_bf16 v[50:53], v[146:149], v[172:175], v[50:53]
	v_mfma_f32_16x16x32_bf16 v[42:45], v[156:159], v[172:175], v[42:45]
	v_mfma_f32_16x16x32_bf16 v[34:37], v[146:149], v[184:187], v[34:37]
	v_mfma_f32_16x16x32_bf16 v[26:29], v[156:159], v[184:187], v[26:29]
	v_mfma_f32_16x16x32_bf16 v[18:21], v[146:149], v[192:195], v[18:21]
	v_mfma_f32_16x16x32_bf16 v[10:13], v[156:159], v[192:195], v[10:13]
	v_mfma_f32_16x16x32_bf16 v[62:65], v[152:155], v[168:171], v[62:65]
	v_mfma_f32_16x16x32_bf16 v[58:61], v[160:163], v[168:171], v[58:61]
	v_mfma_f32_16x16x32_bf16 v[50:53], v[152:155], v[180:183], v[50:53]
	v_mfma_f32_16x16x32_bf16 v[42:45], v[160:163], v[180:183], v[42:45]
	v_mfma_f32_16x16x32_bf16 v[34:37], v[152:155], v[188:191], v[34:37]
	v_mfma_f32_16x16x32_bf16 v[26:29], v[160:163], v[188:191], v[26:29]
	v_mfma_f32_16x16x32_bf16 v[18:21], v[152:155], v[196:199], v[18:21]
	v_mfma_f32_16x16x32_bf16 v[10:13], v[160:163], v[196:199], v[10:13]
	s_barrier
	s_add_u32 s24, s28, 0x28000
	s_addc_u32 s25, s29, 0
	s_add_i32 s45, s46, s8
	v_lshl_add_u64 v[146:147], s[24:25], 0, v[98:99]
	s_mov_b32 m0, s45
	s_nop 0
	global_load_lds_dwordx4 v[146:147], off
	v_lshl_add_u64 v[146:147], s[24:25], 0, v[132:133]
	s_add_i32 m0, s45, 0x2000
	s_nop 0
	global_load_lds_dwordx4 v[146:147], off
	s_waitcnt vmcnt(6)
	s_barrier
	v_mfma_f32_16x16x32_bf16 v[54:57], v[200:203], v[164:167], v[54:57]
	v_mfma_f32_16x16x32_bf16 v[46:49], v[208:211], v[164:167], v[46:49]
	v_mfma_f32_16x16x32_bf16 v[38:41], v[200:203], v[172:175], v[38:41]
	v_mfma_f32_16x16x32_bf16 v[30:33], v[208:211], v[172:175], v[30:33]
	v_mfma_f32_16x16x32_bf16 v[22:25], v[200:203], v[184:187], v[22:25]
	v_mfma_f32_16x16x32_bf16 v[14:17], v[208:211], v[184:187], v[14:17]
	v_mfma_f32_16x16x32_bf16 v[6:9], v[200:203], v[192:195], v[6:9]
	v_mfma_f32_16x16x32_bf16 v[2:5], v[208:211], v[192:195], v[2:5]
	v_mfma_f32_16x16x32_bf16 v[54:57], v[204:207], v[168:171], v[54:57]
	v_mfma_f32_16x16x32_bf16 v[46:49], v[230:233], v[168:171], v[46:49]
	v_mfma_f32_16x16x32_bf16 v[38:41], v[204:207], v[180:183], v[38:41]
	v_mfma_f32_16x16x32_bf16 v[30:33], v[230:233], v[180:183], v[30:33]
	v_mfma_f32_16x16x32_bf16 v[22:25], v[204:207], v[188:191], v[22:25]
	v_mfma_f32_16x16x32_bf16 v[14:17], v[230:233], v[188:191], v[14:17]
	v_mfma_f32_16x16x32_bf16 v[6:9], v[204:207], v[196:199], v[6:9]
	v_mfma_f32_16x16x32_bf16 v[2:5], v[230:233], v[196:199], v[2:5]
	s_add_i32 s45, 0, 0x18000
	v_add_u32_e32 v142, s45, v143
	s_barrier
	ds_read_b128 v[146:149], v142
	ds_read_b128 v[152:155], v142 offset:1024
	ds_read_b128 v[156:159], v142 offset:2048
	ds_read_b128 v[160:163], v142 offset:3072
	s_add_u32 s24, s30, 0x190000
	s_addc_u32 s25, s31, 0
	s_mov_b32 m0, s21
	v_lshl_add_u64 v[200:201], s[24:25], 0, v[136:137]
	ds_read_b128 v[164:167], v151 offset:32768
	ds_read_b128 v[168:171], v151 offset:33792
	ds_read_b128 v[172:175], v151 offset:34816
	ds_read_b128 v[180:183], v151 offset:35840
	ds_read_b128 v[184:187], v151 offset:36864
	ds_read_b128 v[188:191], v151 offset:37888
	ds_read_b128 v[192:195], v151 offset:38912
	ds_read_b128 v[196:199], v151 offset:39936
	global_load_lds_dwordx4 v[200:201], off
	v_lshl_add_u64 v[200:201], s[24:25], 0, v[134:135]
	s_mov_b32 m0, s33
	s_nop 0
	global_load_lds_dwordx4 v[200:201], off
	s_waitcnt lgkmcnt(8)
	s_barrier
	v_add_u32_e32 v250, 0x1c000, v143
	ds_read_b128 v[200:203], v250
	ds_read_b128 v[204:207], v250 offset:1024
	ds_read_b128 v[208:211], v250 offset:2048
	ds_read_b128 v[230:233], v250 offset:3072
	s_waitcnt lgkmcnt(4)
	s_waitcnt lgkmcnt(4)
	v_mfma_f32_16x16x32_bf16 v[128:131], v[146:149], v[164:167], v[128:131]
	v_mfma_f32_16x16x32_bf16 v[124:127], v[156:159], v[164:167], v[124:127]
	v_mfma_f32_16x16x32_bf16 v[112:115], v[146:149], v[172:175], v[112:115]
	v_mfma_f32_16x16x32_bf16 v[108:111], v[156:159], v[172:175], v[108:111]
	v_mfma_f32_16x16x32_bf16 v[94:97], v[146:149], v[184:187], v[94:97]
	v_mfma_f32_16x16x32_bf16 v[90:93], v[156:159], v[184:187], v[90:93]
	v_mfma_f32_16x16x32_bf16 v[78:81], v[146:149], v[192:195], v[78:81]
	v_mfma_f32_16x16x32_bf16 v[74:77], v[156:159], v[192:195], v[74:77]
	v_mfma_f32_16x16x32_bf16 v[128:131], v[152:155], v[168:171], v[128:131]
	v_mfma_f32_16x16x32_bf16 v[124:127], v[160:163], v[168:171], v[124:127]
	v_mfma_f32_16x16x32_bf16 v[112:115], v[152:155], v[180:183], v[112:115]
	v_mfma_f32_16x16x32_bf16 v[108:111], v[160:163], v[180:183], v[108:111]
	v_mfma_f32_16x16x32_bf16 v[94:97], v[152:155], v[188:191], v[94:97]
	v_mfma_f32_16x16x32_bf16 v[90:93], v[160:163], v[188:191], v[90:93]
	v_mfma_f32_16x16x32_bf16 v[78:81], v[152:155], v[196:199], v[78:81]
	v_mfma_f32_16x16x32_bf16 v[74:77], v[160:163], v[196:199], v[74:77]
	s_barrier
	s_add_i32 s30, 0, 0x1c000
	s_add_i32 s24, s45, s8
	v_add_u32_e32 v142, s30, v143
	v_lshl_add_u64 v[176:177], v[176:177], 0, s[68:69]
	s_mov_b32 m0, s24
	global_load_lds_dwordx4 v[176:177], off
	v_lshl_add_u64 v[176:177], v[178:179], 0, s[68:69]
	s_add_i32 m0, s24, 0x2000
	s_nop 0
	global_load_lds_dwordx4 v[176:177], off
	s_barrier
	s_waitcnt lgkmcnt(0)
	s_waitcnt lgkmcnt(0)
	v_mfma_f32_16x16x32_bf16 v[120:123], v[200:203], v[164:167], v[120:123]
	v_mfma_f32_16x16x32_bf16 v[116:119], v[208:211], v[164:167], v[116:119]
	v_mfma_f32_16x16x32_bf16 v[104:107], v[200:203], v[172:175], v[104:107]
	v_mfma_f32_16x16x32_bf16 v[100:103], v[208:211], v[172:175], v[100:103]
	v_mfma_f32_16x16x32_bf16 v[86:89], v[200:203], v[184:187], v[86:89]
	v_mfma_f32_16x16x32_bf16 v[82:85], v[208:211], v[184:187], v[82:85]
	v_mfma_f32_16x16x32_bf16 v[70:73], v[200:203], v[192:195], v[70:73]
	v_mfma_f32_16x16x32_bf16 v[66:69], v[208:211], v[192:195], v[66:69]
	v_mfma_f32_16x16x32_bf16 v[120:123], v[204:207], v[168:171], v[120:123]
	v_mfma_f32_16x16x32_bf16 v[116:119], v[230:233], v[168:171], v[116:119]
	v_mfma_f32_16x16x32_bf16 v[104:107], v[204:207], v[180:183], v[104:107]
	v_mfma_f32_16x16x32_bf16 v[100:103], v[230:233], v[180:183], v[100:103]
	v_mfma_f32_16x16x32_bf16 v[86:89], v[204:207], v[188:191], v[86:89]
	v_mfma_f32_16x16x32_bf16 v[82:85], v[230:233], v[188:191], v[82:85]
	v_mfma_f32_16x16x32_bf16 v[70:73], v[204:207], v[196:199], v[70:73]
	v_mfma_f32_16x16x32_bf16 v[66:69], v[230:233], v[196:199], v[66:69]
	s_mov_b32 m0, s34
	v_lshl_add_u64 v[176:177], v[212:213], 0, s[68:69]
	s_barrier
	ds_read_b128 v[164:167], v151 offset:49152
	ds_read_b128 v[168:171], v151 offset:50176
	ds_read_b128 v[172:175], v151 offset:51200
	ds_read_b128 v[180:183], v151 offset:52224
	ds_read_b128 v[184:187], v151 offset:53248
	ds_read_b128 v[188:191], v151 offset:54272
	ds_read_b128 v[192:195], v151 offset:55296
	ds_read_b128 v[196:199], v151 offset:56320
	global_load_lds_dwordx4 v[176:177], off
	v_lshl_add_u64 v[176:177], v[214:215], 0, s[68:69]
	s_mov_b32 m0, s35
	s_nop 0
	global_load_lds_dwordx4 v[176:177], off
	s_barrier
	s_waitcnt lgkmcnt(0)
	s_waitcnt lgkmcnt(0)
	v_mfma_f32_16x16x32_bf16 v[62:65], v[146:149], v[164:167], v[62:65]
	v_mfma_f32_16x16x32_bf16 v[58:61], v[156:159], v[164:167], v[58:61]
	v_mfma_f32_16x16x32_bf16 v[50:53], v[146:149], v[172:175], v[50:53]
	v_mfma_f32_16x16x32_bf16 v[42:45], v[156:159], v[172:175], v[42:45]
	v_mfma_f32_16x16x32_bf16 v[34:37], v[146:149], v[184:187], v[34:37]
	v_mfma_f32_16x16x32_bf16 v[26:29], v[156:159], v[184:187], v[26:29]
	v_mfma_f32_16x16x32_bf16 v[18:21], v[146:149], v[192:195], v[18:21]
	v_mfma_f32_16x16x32_bf16 v[10:13], v[156:159], v[192:195], v[10:13]
	v_mfma_f32_16x16x32_bf16 v[62:65], v[152:155], v[168:171], v[62:65]
	v_mfma_f32_16x16x32_bf16 v[58:61], v[160:163], v[168:171], v[58:61]
	v_mfma_f32_16x16x32_bf16 v[50:53], v[152:155], v[180:183], v[50:53]
	v_mfma_f32_16x16x32_bf16 v[42:45], v[160:163], v[180:183], v[42:45]
	v_mfma_f32_16x16x32_bf16 v[34:37], v[152:155], v[188:191], v[34:37]
	v_mfma_f32_16x16x32_bf16 v[26:29], v[160:163], v[188:191], v[26:29]
	v_mfma_f32_16x16x32_bf16 v[18:21], v[152:155], v[196:199], v[18:21]
	v_mfma_f32_16x16x32_bf16 v[10:13], v[160:163], v[196:199], v[10:13]
	s_barrier
	s_add_u32 s24, s28, 0x28080
	s_addc_u32 s25, s29, 0
	s_add_i32 s28, s30, s8
	v_lshl_add_u64 v[146:147], s[24:25], 0, v[98:99]
	s_mov_b32 m0, s28
	s_nop 0
	global_load_lds_dwordx4 v[146:147], off
	v_lshl_add_u64 v[146:147], s[24:25], 0, v[132:133]
	s_add_i32 m0, s28, 0x2000
	s_nop 0
	global_load_lds_dwordx4 v[146:147], off
	s_waitcnt vmcnt(6)
	s_barrier
	v_mfma_f32_16x16x32_bf16 v[54:57], v[200:203], v[164:167], v[54:57]
	v_mfma_f32_16x16x32_bf16 v[46:49], v[208:211], v[164:167], v[46:49]
	v_mfma_f32_16x16x32_bf16 v[38:41], v[200:203], v[172:175], v[38:41]
	v_mfma_f32_16x16x32_bf16 v[30:33], v[208:211], v[172:175], v[30:33]
	v_mfma_f32_16x16x32_bf16 v[22:25], v[200:203], v[184:187], v[22:25]
	v_mfma_f32_16x16x32_bf16 v[14:17], v[208:211], v[184:187], v[14:17]
	v_mfma_f32_16x16x32_bf16 v[6:9], v[200:203], v[192:195], v[6:9]
	v_mfma_f32_16x16x32_bf16 v[2:5], v[208:211], v[192:195], v[2:5]
	v_mfma_f32_16x16x32_bf16 v[54:57], v[204:207], v[168:171], v[54:57]
	v_mfma_f32_16x16x32_bf16 v[46:49], v[230:233], v[168:171], v[46:49]
	v_mfma_f32_16x16x32_bf16 v[38:41], v[204:207], v[180:183], v[38:41]
	v_mfma_f32_16x16x32_bf16 v[30:33], v[230:233], v[180:183], v[30:33]
	v_mfma_f32_16x16x32_bf16 v[22:25], v[204:207], v[188:191], v[22:25]
	v_mfma_f32_16x16x32_bf16 v[14:17], v[230:233], v[188:191], v[14:17]
	v_mfma_f32_16x16x32_bf16 v[6:9], v[204:207], v[196:199], v[6:9]
	v_mfma_f32_16x16x32_bf16 v[2:5], v[230:233], v[196:199], v[2:5]
	s_add_i32 s44, s44, 2
	s_add_u32 s42, s42, 0x100
	s_addc_u32 s43, s43, 0
	s_cmp_gt_u32 s44, 7
	s_mov_b64 s[24:25], s[26:27]
	s_barrier
	s_cbranch_scc0 .LBB0_690
	s_cmp_gt_i32 s40, 2
	s_cselect_b64 s[24:25], -1, 0
	v_cndmask_b32_e64 v142, 0, 1, s[24:25]
	v_lshl_add_u32 v153, s41, 8, v1
	v_lshl_or_b32 v146, v153, 1, v142
	v_readlane_b32 s24, v253, 3
	v_ashrrev_i32_e32 v147, 31, v146
	v_readlane_b32 s25, v253, 4
	v_or_b32_e32 v159, 16, v153
	v_or_b32_e32 v161, 32, v153
	v_lshl_add_u64 v[146:147], v[146:147], 2, s[24:25]
	global_load_dword v158, v[146:147], off
	v_lshl_or_b32 v146, v159, 1, v142
	v_ashrrev_i32_e32 v147, 31, v146
	v_lshl_add_u64 v[146:147], v[146:147], 2, s[24:25]
	global_load_dword v160, v[146:147], off
	v_lshl_or_b32 v146, v161, 1, v142
	v_ashrrev_i32_e32 v147, 31, v146
	v_lshl_add_u64 v[146:147], v[146:147], 2, s[24:25]
	v_or_b32_e32 v157, 48, v153
	global_load_dword v156, v[146:147], off
	v_lshl_or_b32 v146, v157, 1, v142
	v_ashrrev_i32_e32 v147, 31, v146
	v_lshl_add_u64 v[146:147], v[146:147], 2, s[24:25]
	global_load_dword v154, v[146:147], off
	v_add_u32_e32 v155, 0x80, v153
	v_lshl_or_b32 v146, v155, 1, v142
	v_ashrrev_i32_e32 v147, 31, v146
	v_lshl_add_u64 v[146:147], v[146:147], 2, s[24:25]
	global_load_dword v152, v[146:147], off
	global_load_dword v150, v[146:147], off offset:128
	global_load_dword v144, v[146:147], off offset:256
	global_load_dword v142, v[146:147], off offset:384
	v_readlane_b32 s24, v253, 7
	v_lshl_or_b32 v148, s40, 8, v145
	v_readlane_b32 s25, v253, 8
	v_ashrrev_i32_e32 v149, 31, v148
	v_lshlrev_b64 v[148:149], 1, v[148:149]
	v_mov_b64_e32 v[146:147], s[24:25]
	v_mad_i64_i32 v[162:163], s[24:25], v153, s49, v[146:147]
	v_lshl_add_u64 v[162:163], v[162:163], 0, v[148:149]
	s_and_b64 vcc, exec, s[0:1]
	s_mov_b32 s41, s39
	s_mov_b32 s40, s37
	s_mov_b64 s[26:27], s[22:23]
	s_waitcnt vmcnt(0)
	v_pk_mul_f32 v[130:131], v[130:131], v[158:159] op_sel_hi:[1,0]
	v_pk_mul_f32 v[128:129], v[128:129], v[158:159] op_sel_hi:[1,0]
	v_pk_mul_f32 v[164:165], v[126:127], v[158:159] op_sel_hi:[1,0]
	v_pk_mul_f32 v[126:127], v[124:125], v[158:159] op_sel_hi:[1,0]
	v_cvt_pk_bf16_f32 v124, v128, v129
	v_cvt_pk_bf16_f32 v125, v130, v131
	v_pk_mul_f32 v[122:123], v[122:123], v[158:159] op_sel_hi:[1,0]
	v_cvt_pk_bf16_f32 v126, v126, v127
	v_cvt_pk_bf16_f32 v127, v164, v165
	global_store_dwordx4 v[162:163], v[124:127], off
	v_pk_mul_f32 v[120:121], v[120:121], v[158:159] op_sel_hi:[1,0]
	v_pk_mul_f32 v[114:115], v[114:115], v[160:161] op_sel_hi:[1,0]
	v_pk_mul_f32 v[124:125], v[118:119], v[158:159] op_sel_hi:[1,0]
	v_pk_mul_f32 v[118:119], v[116:117], v[158:159] op_sel_hi:[1,0]
	v_cvt_pk_bf16_f32 v116, v120, v121
	v_cvt_pk_bf16_f32 v117, v122, v123
	v_pk_mul_f32 v[112:113], v[112:113], v[160:161] op_sel_hi:[1,0]
	v_cvt_pk_bf16_f32 v118, v118, v119
	v_cvt_pk_bf16_f32 v119, v124, v125
	global_store_dwordx4 v[162:163], v[116:119], off offset:256
	v_pk_mul_f32 v[106:107], v[106:107], v[160:161] op_sel_hi:[1,0]
	v_pk_mul_f32 v[104:105], v[104:105], v[160:161] op_sel_hi:[1,0]
	v_mad_i64_i32 v[116:117], s[24:25], v159, s49, v[146:147]
	v_lshl_add_u64 v[116:117], v[116:117], 0, v[148:149]
	v_pk_mul_f32 v[118:119], v[110:111], v[160:161] op_sel_hi:[1,0]
	v_pk_mul_f32 v[110:111], v[108:109], v[160:161] op_sel_hi:[1,0]
	v_cvt_pk_bf16_f32 v108, v112, v113
	v_cvt_pk_bf16_f32 v109, v114, v115
	v_pk_mul_f32 v[96:97], v[96:97], v[156:157] op_sel_hi:[1,0]
	v_cvt_pk_bf16_f32 v110, v110, v111
	v_cvt_pk_bf16_f32 v111, v118, v119
	global_store_dwordx4 v[116:117], v[108:111], off
	v_pk_mul_f32 v[94:95], v[94:95], v[156:157] op_sel_hi:[1,0]
	v_pk_mul_f32 v[88:89], v[88:89], v[156:157] op_sel_hi:[1,0]
	v_pk_mul_f32 v[108:109], v[102:103], v[160:161] op_sel_hi:[1,0]
	v_pk_mul_f32 v[102:103], v[100:101], v[160:161] op_sel_hi:[1,0]
	v_cvt_pk_bf16_f32 v100, v104, v105
	v_cvt_pk_bf16_f32 v101, v106, v107
	v_pk_mul_f32 v[86:87], v[86:87], v[156:157] op_sel_hi:[1,0]
	v_cvt_pk_bf16_f32 v102, v102, v103
	v_cvt_pk_bf16_f32 v103, v108, v109
	global_store_dwordx4 v[116:117], v[100:103], off offset:256
	v_pk_mul_f32 v[80:81], v[80:81], v[154:155] op_sel_hi:[1,0]
	v_pk_mul_f32 v[78:79], v[78:79], v[154:155] op_sel_hi:[1,0]
	v_mad_i64_i32 v[100:101], s[24:25], v161, s49, v[146:147]
	v_lshl_add_u64 v[100:101], v[100:101], 0, v[148:149]
	v_pk_mul_f32 v[102:103], v[92:93], v[156:157] op_sel_hi:[1,0]
	v_pk_mul_f32 v[92:93], v[90:91], v[156:157] op_sel_hi:[1,0]
	v_cvt_pk_bf16_f32 v90, v94, v95
	v_cvt_pk_bf16_f32 v91, v96, v97
	v_pk_mul_f32 v[72:73], v[72:73], v[154:155] op_sel_hi:[1,0]
	v_cvt_pk_bf16_f32 v92, v92, v93
	v_cvt_pk_bf16_f32 v93, v102, v103
	global_store_dwordx4 v[100:101], v[90:93], off
	v_pk_mul_f32 v[70:71], v[70:71], v[154:155] op_sel_hi:[1,0]
	v_pk_mul_f32 v[64:65], v[64:65], v[152:153] op_sel_hi:[1,0]
	v_pk_mul_f32 v[90:91], v[84:85], v[156:157] op_sel_hi:[1,0]
	v_pk_mul_f32 v[84:85], v[82:83], v[156:157] op_sel_hi:[1,0]
	v_cvt_pk_bf16_f32 v82, v86, v87
	v_cvt_pk_bf16_f32 v83, v88, v89
	v_pk_mul_f32 v[62:63], v[62:63], v[152:153] op_sel_hi:[1,0]
	v_cvt_pk_bf16_f32 v84, v84, v85
	v_cvt_pk_bf16_f32 v85, v90, v91
	global_store_dwordx4 v[100:101], v[82:85], off offset:256
	v_pk_mul_f32 v[54:55], v[54:55], v[152:153] op_sel_hi:[1,0]
	v_pk_mul_f32 v[56:57], v[56:57], v[152:153] op_sel_hi:[1,0]
	v_mad_i64_i32 v[82:83], s[24:25], v157, s49, v[146:147]
	v_lshl_add_u64 v[82:83], v[82:83], 0, v[148:149]
	v_pk_mul_f32 v[84:85], v[76:77], v[154:155] op_sel_hi:[1,0]
	v_pk_mul_f32 v[76:77], v[74:75], v[154:155] op_sel_hi:[1,0]
	v_cvt_pk_bf16_f32 v74, v78, v79
	v_cvt_pk_bf16_f32 v75, v80, v81
	v_pk_mul_f32 v[50:51], v[50:51], v[150:151] op_sel_hi:[1,0]
	v_cvt_pk_bf16_f32 v76, v76, v77
	v_cvt_pk_bf16_f32 v77, v84, v85
	global_store_dwordx4 v[82:83], v[74:77], off
	v_pk_mul_f32 v[38:39], v[38:39], v[150:151] op_sel_hi:[1,0]
	v_pk_mul_f32 v[40:41], v[40:41], v[150:151] op_sel_hi:[1,0]
	v_pk_mul_f32 v[74:75], v[68:69], v[154:155] op_sel_hi:[1,0]
	v_pk_mul_f32 v[68:69], v[66:67], v[154:155] op_sel_hi:[1,0]
	v_cvt_pk_bf16_f32 v66, v70, v71
	v_cvt_pk_bf16_f32 v67, v72, v73
	v_pk_mul_f32 v[34:35], v[34:35], v[144:145] op_sel_hi:[1,0]
	v_cvt_pk_bf16_f32 v68, v68, v69
	v_cvt_pk_bf16_f32 v69, v74, v75
	global_store_dwordx4 v[82:83], v[66:69], off offset:256
	v_pk_mul_f32 v[22:23], v[22:23], v[144:145] op_sel_hi:[1,0]
	v_pk_mul_f32 v[24:25], v[24:25], v[144:145] op_sel_hi:[1,0]
	v_mad_i64_i32 v[66:67], s[24:25], v155, s49, v[146:147]
	v_lshl_add_u64 v[66:67], v[66:67], 0, v[148:149]
	v_pk_mul_f32 v[68:69], v[60:61], v[152:153] op_sel_hi:[1,0]
	v_pk_mul_f32 v[60:61], v[58:59], v[152:153] op_sel_hi:[1,0]
	v_cvt_pk_bf16_f32 v58, v62, v63
	v_cvt_pk_bf16_f32 v59, v64, v65
	v_pk_mul_f32 v[18:19], v[18:19], v[142:143] op_sel_hi:[1,0]
	v_cvt_pk_bf16_f32 v60, v60, v61
	v_cvt_pk_bf16_f32 v61, v68, v69
	global_store_dwordx4 v[66:67], v[58:61], off
	v_pk_mul_f32 v[8:9], v[8:9], v[142:143] op_sel_hi:[1,0]
	v_pk_mul_f32 v[6:7], v[6:7], v[142:143] op_sel_hi:[1,0]
	v_pk_mul_f32 v[58:59], v[48:49], v[152:153] op_sel_hi:[1,0]
	v_pk_mul_f32 v[48:49], v[46:47], v[152:153] op_sel_hi:[1,0]
	v_cvt_pk_bf16_f32 v46, v54, v55
	v_cvt_pk_bf16_f32 v47, v56, v57
	s_nop 0
	v_cvt_pk_bf16_f32 v48, v48, v49
	v_cvt_pk_bf16_f32 v49, v58, v59
	global_store_dwordx4 v[66:67], v[46:49], off offset:256
	s_nop 1
	v_add_u32_e32 v46, 0x90, v153
	v_mad_i64_i32 v[46:47], s[24:25], v46, s49, v[146:147]
	v_lshl_add_u64 v[46:47], v[46:47], 0, v[148:149]
	v_pk_mul_f32 v[48:49], v[52:53], v[150:151] op_sel_hi:[1,0]
	v_pk_mul_f32 v[52:53], v[44:45], v[150:151] op_sel_hi:[1,0]
	v_pk_mul_f32 v[44:45], v[42:43], v[150:151] op_sel_hi:[1,0]
	v_cvt_pk_bf16_f32 v42, v50, v51
	v_cvt_pk_bf16_f32 v43, v48, v49
	s_nop 0
	v_cvt_pk_bf16_f32 v44, v44, v45
	v_cvt_pk_bf16_f32 v45, v52, v53
	global_store_dwordx4 v[46:47], v[42:45], off
	s_nop 1
	v_pk_mul_f32 v[42:43], v[32:33], v[150:151] op_sel_hi:[1,0]
	v_pk_mul_f32 v[32:33], v[30:31], v[150:151] op_sel_hi:[1,0]
	v_cvt_pk_bf16_f32 v30, v38, v39
	v_cvt_pk_bf16_f32 v31, v40, v41
	s_nop 0
	v_cvt_pk_bf16_f32 v32, v32, v33
	v_cvt_pk_bf16_f32 v33, v42, v43
	global_store_dwordx4 v[46:47], v[30:33], off offset:256
	s_nop 1
	v_add_u32_e32 v30, 0xa0, v153
	v_mad_i64_i32 v[30:31], s[24:25], v30, s49, v[146:147]
	v_lshl_add_u64 v[30:31], v[30:31], 0, v[148:149]
	v_pk_mul_f32 v[32:33], v[36:37], v[144:145] op_sel_hi:[1,0]
	v_pk_mul_f32 v[36:37], v[28:29], v[144:145] op_sel_hi:[1,0]
	v_pk_mul_f32 v[28:29], v[26:27], v[144:145] op_sel_hi:[1,0]
	v_cvt_pk_bf16_f32 v26, v34, v35
	v_cvt_pk_bf16_f32 v27, v32, v33
	s_nop 0
	v_cvt_pk_bf16_f32 v28, v28, v29
	v_cvt_pk_bf16_f32 v29, v36, v37
	global_store_dwordx4 v[30:31], v[26:29], off
	s_nop 1
	v_pk_mul_f32 v[26:27], v[16:17], v[144:145] op_sel_hi:[1,0]
	v_pk_mul_f32 v[16:17], v[14:15], v[144:145] op_sel_hi:[1,0]
	v_cvt_pk_bf16_f32 v14, v22, v23
	v_cvt_pk_bf16_f32 v15, v24, v25
	s_nop 0
	v_cvt_pk_bf16_f32 v16, v16, v17
	v_cvt_pk_bf16_f32 v17, v26, v27
	global_store_dwordx4 v[30:31], v[14:17], off offset:256
	s_nop 1
	v_add_u32_e32 v14, 0xb0, v153
	v_mad_i64_i32 v[14:15], s[24:25], v14, s49, v[146:147]
	v_lshl_add_u64 v[14:15], v[14:15], 0, v[148:149]
	v_pk_mul_f32 v[16:17], v[20:21], v[142:143] op_sel_hi:[1,0]
	v_pk_mul_f32 v[20:21], v[12:13], v[142:143] op_sel_hi:[1,0]
	v_pk_mul_f32 v[12:13], v[10:11], v[142:143] op_sel_hi:[1,0]
	v_cvt_pk_bf16_f32 v10, v18, v19
	v_cvt_pk_bf16_f32 v11, v16, v17
	s_mov_b64 s[24:25], s[18:19]
	v_cvt_pk_bf16_f32 v12, v12, v13
	v_cvt_pk_bf16_f32 v13, v20, v21
	global_store_dwordx4 v[14:15], v[10:13], off
	s_nop 1
	v_pk_mul_f32 v[10:11], v[4:5], v[142:143] op_sel_hi:[1,0]
	v_pk_mul_f32 v[4:5], v[2:3], v[142:143] op_sel_hi:[1,0]
	v_cvt_pk_bf16_f32 v2, v6, v7
	v_cvt_pk_bf16_f32 v3, v8, v9
	s_nop 0
	v_cvt_pk_bf16_f32 v4, v4, v5
	v_cvt_pk_bf16_f32 v5, v10, v11
	global_store_dwordx4 v[14:15], v[2:5], off offset:256
	s_cbranch_vccz .LBB0_683
	s_waitcnt vmcnt(0)
	s_cmpk_gt_u32 s3, 0xff
	s_cbranch_scc1 .LBB0_694
	s_barrier

.LBB0_1592:
	s_add_u32 s34, s30, 0xfff80080
	s_addc_u32 s35, s31, -1
	s_add_i32 s46, 0, 0x10000
	v_add_u32_e32 v86, s46, v160
	ds_read_b128 v[70:73], v86
	ds_read_b128 v[78:81], v86 offset:1024
	ds_read_b128 v[82:85], v86 offset:2048
	ds_read_b128 v[86:89], v86 offset:3072
	s_cmp_eq_u32 s45, 28
	s_cselect_b32 s37, s25, s35
	s_cselect_b32 s36, s41, s34
	s_cselect_b32 s35, s19, s44
	s_cselect_b32 s34, s42, s43
	v_lshl_add_u64 v[158:159], s[30:31], 0, v[150:151]
	s_add_i32 m0, s5, 0xc000
	ds_read_b128 v[154:157], v162
	ds_read_b128 v[164:167], v162 offset:1024
	ds_read_b128 v[168:171], v162 offset:2048
	ds_read_b128 v[172:175], v162 offset:3072
	ds_read_b128 v[176:179], v162 offset:4096
	ds_read_b128 v[180:183], v162 offset:5120
	ds_read_b128 v[184:187], v162 offset:6144
	ds_read_b128 v[188:191], v162 offset:7168
	global_load_lds_dwordx4 v[158:159], off
	v_lshl_add_u64 v[158:159], s[30:31], 0, v[152:153]
	s_add_i32 m0, s5, 0xe000
	s_nop 0
	global_load_lds_dwordx4 v[158:159], off
	s_waitcnt lgkmcnt(8)
	s_barrier
	v_add_u32_e32 v250, 0x14000, v160
	ds_read_b128 v[192:195], v250
	ds_read_b128 v[196:199], v250 offset:1024
	ds_read_b128 v[200:203], v250 offset:2048
	ds_read_b128 v[204:207], v250 offset:3072
	s_waitcnt lgkmcnt(4)
	s_waitcnt lgkmcnt(4)
	v_mfma_f32_16x16x32_bf16 v[144:147], v[70:73], v[154:157], v[144:147]
	v_mfma_f32_16x16x32_bf16 v[140:143], v[82:85], v[154:157], v[140:143]
	v_mfma_f32_16x16x32_bf16 v[128:131], v[70:73], v[168:171], v[128:131]
	v_mfma_f32_16x16x32_bf16 v[124:127], v[82:85], v[168:171], v[124:127]
	v_mfma_f32_16x16x32_bf16 v[112:115], v[70:73], v[176:179], v[112:115]
	v_mfma_f32_16x16x32_bf16 v[108:111], v[82:85], v[176:179], v[108:111]
	v_mfma_f32_16x16x32_bf16 v[94:97], v[70:73], v[184:187], v[94:97]
	v_mfma_f32_16x16x32_bf16 v[90:93], v[82:85], v[184:187], v[90:93]
	v_mfma_f32_16x16x32_bf16 v[144:147], v[78:81], v[164:167], v[144:147]
	v_mfma_f32_16x16x32_bf16 v[140:143], v[86:89], v[164:167], v[140:143]
	v_mfma_f32_16x16x32_bf16 v[128:131], v[78:81], v[172:175], v[128:131]
	v_mfma_f32_16x16x32_bf16 v[124:127], v[86:89], v[172:175], v[124:127]
	v_mfma_f32_16x16x32_bf16 v[112:115], v[78:81], v[180:183], v[112:115]
	v_mfma_f32_16x16x32_bf16 v[108:111], v[86:89], v[180:183], v[108:111]
	v_mfma_f32_16x16x32_bf16 v[94:97], v[78:81], v[188:191], v[94:97]
	v_mfma_f32_16x16x32_bf16 v[90:93], v[86:89], v[188:191], v[90:93]
	s_barrier
	s_add_i32 s48, 0, 0x14000
	v_add_u32_e32 v158, s48, v160
	s_add_i32 s46, s46, s4
	v_lshl_add_u64 v[158:159], s[34:35], 0, v[98:99]
	s_mov_b32 m0, s46
	v_lshl_add_u64 v[208:209], s[34:35], 0, v[148:149]
	global_load_lds_dwordx4 v[158:159], off
	s_add_i32 m0, s46, 0x2000
	s_nop 0
	global_load_lds_dwordx4 v[208:209], off
	s_barrier
	s_waitcnt lgkmcnt(0)
	s_waitcnt lgkmcnt(0)
	v_mfma_f32_16x16x32_bf16 v[136:139], v[192:195], v[154:157], v[136:139]
	v_mfma_f32_16x16x32_bf16 v[132:135], v[200:203], v[154:157], v[132:135]
	v_mfma_f32_16x16x32_bf16 v[120:123], v[192:195], v[168:171], v[120:123]
	v_mfma_f32_16x16x32_bf16 v[116:119], v[200:203], v[168:171], v[116:119]
	v_mfma_f32_16x16x32_bf16 v[104:107], v[192:195], v[176:179], v[104:107]
	v_mfma_f32_16x16x32_bf16 v[100:103], v[200:203], v[176:179], v[100:103]
	v_mfma_f32_16x16x32_bf16 v[74:77], v[192:195], v[184:187], v[74:77]
	v_mfma_f32_16x16x32_bf16 v[66:69], v[200:203], v[184:187], v[66:69]
	v_mfma_f32_16x16x32_bf16 v[136:139], v[196:199], v[164:167], v[136:139]
	v_mfma_f32_16x16x32_bf16 v[132:135], v[204:207], v[164:167], v[132:135]
	v_mfma_f32_16x16x32_bf16 v[120:123], v[196:199], v[172:175], v[120:123]
	v_mfma_f32_16x16x32_bf16 v[116:119], v[204:207], v[172:175], v[116:119]
	v_mfma_f32_16x16x32_bf16 v[104:107], v[196:199], v[180:183], v[104:107]
	v_mfma_f32_16x16x32_bf16 v[100:103], v[204:207], v[180:183], v[100:103]
	v_mfma_f32_16x16x32_bf16 v[74:77], v[196:199], v[188:191], v[74:77]
	v_mfma_f32_16x16x32_bf16 v[66:69], v[204:207], v[188:191], v[66:69]
	s_mov_b32 m0, s5
	v_lshl_add_u64 v[210:211], s[36:37], 0, v[98:99]
	s_barrier
	ds_read_b128 v[154:157], v162 offset:16384
	ds_read_b128 v[164:167], v162 offset:17408
	ds_read_b128 v[168:171], v162 offset:18432
	ds_read_b128 v[172:175], v162 offset:19456
	ds_read_b128 v[176:179], v162 offset:20480
	ds_read_b128 v[180:183], v162 offset:21504
	ds_read_b128 v[184:187], v162 offset:22528
	ds_read_b128 v[188:191], v162 offset:23552
	global_load_lds_dwordx4 v[210:211], off
	v_lshl_add_u64 v[212:213], s[36:37], 0, v[148:149]
	s_mov_b32 m0, s8
	s_nop 0
	global_load_lds_dwordx4 v[212:213], off
	s_barrier
	s_waitcnt lgkmcnt(0)
	s_waitcnt lgkmcnt(0)
	v_mfma_f32_16x16x32_bf16 v[62:65], v[70:73], v[154:157], v[62:65]
	v_mfma_f32_16x16x32_bf16 v[58:61], v[82:85], v[154:157], v[58:61]
	v_mfma_f32_16x16x32_bf16 v[46:49], v[70:73], v[168:171], v[46:49]
	v_mfma_f32_16x16x32_bf16 v[42:45], v[82:85], v[168:171], v[42:45]
	v_mfma_f32_16x16x32_bf16 v[30:33], v[70:73], v[176:179], v[30:33]
	v_mfma_f32_16x16x32_bf16 v[26:29], v[82:85], v[176:179], v[26:29]
	v_mfma_f32_16x16x32_bf16 v[22:25], v[70:73], v[184:187], v[22:25]
	v_mfma_f32_16x16x32_bf16 v[18:21], v[82:85], v[184:187], v[18:21]
	v_mfma_f32_16x16x32_bf16 v[62:65], v[78:81], v[164:167], v[62:65]
	v_mfma_f32_16x16x32_bf16 v[58:61], v[86:89], v[164:167], v[58:61]
	v_mfma_f32_16x16x32_bf16 v[46:49], v[78:81], v[172:175], v[46:49]
	v_mfma_f32_16x16x32_bf16 v[42:45], v[86:89], v[172:175], v[42:45]
	v_mfma_f32_16x16x32_bf16 v[30:33], v[78:81], v[180:183], v[30:33]
	v_mfma_f32_16x16x32_bf16 v[26:29], v[86:89], v[180:183], v[26:29]
	v_mfma_f32_16x16x32_bf16 v[22:25], v[78:81], v[188:191], v[22:25]
	v_mfma_f32_16x16x32_bf16 v[18:21], v[86:89], v[188:191], v[18:21]
	s_barrier
	s_add_u32 s46, s34, 0x80000
	s_addc_u32 s47, s35, 0
	s_add_i32 s48, s48, s4
	v_lshl_add_u64 v[70:71], s[46:47], 0, v[98:99]
	s_mov_b32 m0, s48
	s_nop 0
	global_load_lds_dwordx4 v[70:71], off
	v_lshl_add_u64 v[70:71], s[46:47], 0, v[148:149]
	s_add_i32 m0, s48, 0x2000
	s_nop 0
	global_load_lds_dwordx4 v[70:71], off
	s_waitcnt vmcnt(6)
	s_barrier
	v_mfma_f32_16x16x32_bf16 v[54:57], v[192:195], v[154:157], v[54:57]
	v_mfma_f32_16x16x32_bf16 v[50:53], v[200:203], v[154:157], v[50:53]
	v_mfma_f32_16x16x32_bf16 v[38:41], v[192:195], v[168:171], v[38:41]
	v_mfma_f32_16x16x32_bf16 v[34:37], v[200:203], v[168:171], v[34:37]
	v_mfma_f32_16x16x32_bf16 v[14:17], v[192:195], v[176:179], v[14:17]
	v_mfma_f32_16x16x32_bf16 v[10:13], v[200:203], v[176:179], v[10:13]
	v_mfma_f32_16x16x32_bf16 v[6:9], v[192:195], v[184:187], v[6:9]
	v_mfma_f32_16x16x32_bf16 v[2:5], v[200:203], v[184:187], v[2:5]
	v_mfma_f32_16x16x32_bf16 v[54:57], v[196:199], v[164:167], v[54:57]
	v_mfma_f32_16x16x32_bf16 v[50:53], v[204:207], v[164:167], v[50:53]
	v_mfma_f32_16x16x32_bf16 v[38:41], v[196:199], v[172:175], v[38:41]
	v_mfma_f32_16x16x32_bf16 v[34:37], v[204:207], v[172:175], v[34:37]
	v_mfma_f32_16x16x32_bf16 v[14:17], v[196:199], v[180:183], v[14:17]
	v_mfma_f32_16x16x32_bf16 v[10:13], v[204:207], v[180:183], v[10:13]
	v_mfma_f32_16x16x32_bf16 v[6:9], v[196:199], v[188:191], v[6:9]
	v_mfma_f32_16x16x32_bf16 v[2:5], v[204:207], v[188:191], v[2:5]
	s_add_i32 s46, 0, 0x18000
	v_add_u32_e32 v86, s46, v160
	s_barrier
	ds_read_b128 v[70:73], v86
	ds_read_b128 v[78:81], v86 offset:1024
	ds_read_b128 v[82:85], v86 offset:2048
	ds_read_b128 v[86:89], v86 offset:3072
	s_add_u32 s36, s36, 0x80000
	s_addc_u32 s37, s37, 0
	s_mov_b32 m0, s9
	v_lshl_add_u64 v[192:193], s[36:37], 0, v[98:99]
	ds_read_b128 v[154:157], v162 offset:32768
	ds_read_b128 v[164:167], v162 offset:33792
	ds_read_b128 v[168:171], v162 offset:34816
	ds_read_b128 v[172:175], v162 offset:35840
	ds_read_b128 v[176:179], v162 offset:36864
	ds_read_b128 v[180:183], v162 offset:37888
	ds_read_b128 v[184:187], v162 offset:38912
	ds_read_b128 v[188:191], v162 offset:39936
	global_load_lds_dwordx4 v[192:193], off
	v_lshl_add_u64 v[192:193], s[36:37], 0, v[148:149]
	s_mov_b32 m0, s20
	s_nop 0
	global_load_lds_dwordx4 v[192:193], off
	s_waitcnt lgkmcnt(8)
	s_barrier
	v_add_u32_e32 v250, 0x1c000, v160
	ds_read_b128 v[192:195], v250
	ds_read_b128 v[196:199], v250 offset:1024
	ds_read_b128 v[200:203], v250 offset:2048
	ds_read_b128 v[204:207], v250 offset:3072
	s_waitcnt lgkmcnt(4)
	s_waitcnt lgkmcnt(4)
	v_mfma_f32_16x16x32_bf16 v[144:147], v[70:73], v[154:157], v[144:147]
	v_mfma_f32_16x16x32_bf16 v[140:143], v[82:85], v[154:157], v[140:143]
	v_mfma_f32_16x16x32_bf16 v[128:131], v[70:73], v[168:171], v[128:131]
	v_mfma_f32_16x16x32_bf16 v[124:127], v[82:85], v[168:171], v[124:127]
	v_mfma_f32_16x16x32_bf16 v[112:115], v[70:73], v[176:179], v[112:115]
	v_mfma_f32_16x16x32_bf16 v[108:111], v[82:85], v[176:179], v[108:111]
	v_mfma_f32_16x16x32_bf16 v[94:97], v[70:73], v[184:187], v[94:97]
	v_mfma_f32_16x16x32_bf16 v[90:93], v[82:85], v[184:187], v[90:93]
	v_mfma_f32_16x16x32_bf16 v[144:147], v[78:81], v[164:167], v[144:147]
	v_mfma_f32_16x16x32_bf16 v[140:143], v[86:89], v[164:167], v[140:143]
	v_mfma_f32_16x16x32_bf16 v[128:131], v[78:81], v[172:175], v[128:131]
	v_mfma_f32_16x16x32_bf16 v[124:127], v[86:89], v[172:175], v[124:127]
	v_mfma_f32_16x16x32_bf16 v[112:115], v[78:81], v[180:183], v[112:115]
	v_mfma_f32_16x16x32_bf16 v[108:111], v[86:89], v[180:183], v[108:111]
	v_mfma_f32_16x16x32_bf16 v[94:97], v[78:81], v[188:191], v[94:97]
	v_mfma_f32_16x16x32_bf16 v[90:93], v[86:89], v[188:191], v[90:93]
	s_barrier
	s_add_i32 s36, 0, 0x1c000
	s_add_i32 s37, s46, s4
	v_add_u32_e32 v163, s36, v160
	v_lshl_add_u64 v[158:159], v[158:159], 0, s[68:69]
	s_mov_b32 m0, s37
	global_load_lds_dwordx4 v[158:159], off
	v_lshl_add_u64 v[158:159], v[208:209], 0, s[68:69]
	s_add_i32 m0, s37, 0x2000
	s_nop 0
	global_load_lds_dwordx4 v[158:159], off
	s_barrier
	s_waitcnt lgkmcnt(0)
	s_waitcnt lgkmcnt(0)
	v_mfma_f32_16x16x32_bf16 v[136:139], v[192:195], v[154:157], v[136:139]
	v_mfma_f32_16x16x32_bf16 v[132:135], v[200:203], v[154:157], v[132:135]
	v_mfma_f32_16x16x32_bf16 v[120:123], v[192:195], v[168:171], v[120:123]
	v_mfma_f32_16x16x32_bf16 v[116:119], v[200:203], v[168:171], v[116:119]
	v_mfma_f32_16x16x32_bf16 v[104:107], v[192:195], v[176:179], v[104:107]
	v_mfma_f32_16x16x32_bf16 v[100:103], v[200:203], v[176:179], v[100:103]
	v_mfma_f32_16x16x32_bf16 v[74:77], v[192:195], v[184:187], v[74:77]
	v_mfma_f32_16x16x32_bf16 v[66:69], v[200:203], v[184:187], v[66:69]
	v_mfma_f32_16x16x32_bf16 v[136:139], v[196:199], v[164:167], v[136:139]
	v_mfma_f32_16x16x32_bf16 v[132:135], v[204:207], v[164:167], v[132:135]
	v_mfma_f32_16x16x32_bf16 v[120:123], v[196:199], v[172:175], v[120:123]
	v_mfma_f32_16x16x32_bf16 v[116:119], v[204:207], v[172:175], v[116:119]
	v_mfma_f32_16x16x32_bf16 v[104:107], v[196:199], v[180:183], v[104:107]
	v_mfma_f32_16x16x32_bf16 v[100:103], v[204:207], v[180:183], v[100:103]
	v_mfma_f32_16x16x32_bf16 v[74:77], v[196:199], v[188:191], v[74:77]
	v_mfma_f32_16x16x32_bf16 v[66:69], v[204:207], v[188:191], v[66:69]
	s_mov_b32 m0, s21
	v_lshl_add_u64 v[158:159], v[210:211], 0, s[68:69]
	s_barrier
	ds_read_b128 v[154:157], v162 offset:49152
	ds_read_b128 v[164:167], v162 offset:50176
	ds_read_b128 v[168:171], v162 offset:51200
	ds_read_b128 v[172:175], v162 offset:52224
	ds_read_b128 v[176:179], v162 offset:53248
	ds_read_b128 v[180:183], v162 offset:54272
	ds_read_b128 v[184:187], v162 offset:55296
	ds_read_b128 v[188:191], v162 offset:56320
	global_load_lds_dwordx4 v[158:159], off
	v_lshl_add_u64 v[158:159], v[212:213], 0, s[68:69]
	s_mov_b32 m0, s33
	s_nop 0
	global_load_lds_dwordx4 v[158:159], off
	s_barrier
	s_waitcnt lgkmcnt(0)
	s_waitcnt lgkmcnt(0)
	v_mfma_f32_16x16x32_bf16 v[62:65], v[70:73], v[154:157], v[62:65]
	v_mfma_f32_16x16x32_bf16 v[58:61], v[82:85], v[154:157], v[58:61]
	v_mfma_f32_16x16x32_bf16 v[46:49], v[70:73], v[168:171], v[46:49]
	v_mfma_f32_16x16x32_bf16 v[42:45], v[82:85], v[168:171], v[42:45]
	v_mfma_f32_16x16x32_bf16 v[30:33], v[70:73], v[176:179], v[30:33]
	v_mfma_f32_16x16x32_bf16 v[26:29], v[82:85], v[176:179], v[26:29]
	v_mfma_f32_16x16x32_bf16 v[22:25], v[70:73], v[184:187], v[22:25]
	v_mfma_f32_16x16x32_bf16 v[18:21], v[82:85], v[184:187], v[18:21]
	v_mfma_f32_16x16x32_bf16 v[62:65], v[78:81], v[164:167], v[62:65]
	v_mfma_f32_16x16x32_bf16 v[58:61], v[86:89], v[164:167], v[58:61]
	v_mfma_f32_16x16x32_bf16 v[46:49], v[78:81], v[172:175], v[46:49]
	v_mfma_f32_16x16x32_bf16 v[42:45], v[86:89], v[172:175], v[42:45]
	v_mfma_f32_16x16x32_bf16 v[30:33], v[78:81], v[180:183], v[30:33]
	v_mfma_f32_16x16x32_bf16 v[26:29], v[86:89], v[180:183], v[26:29]
	v_mfma_f32_16x16x32_bf16 v[22:25], v[78:81], v[188:191], v[22:25]
	v_mfma_f32_16x16x32_bf16 v[18:21], v[86:89], v[188:191], v[18:21]
	s_barrier
	s_add_u32 s34, s34, 0x80080
	s_addc_u32 s35, s35, 0
	s_add_i32 s36, s36, s4
	v_lshl_add_u64 v[70:71], s[34:35], 0, v[98:99]
	s_mov_b32 m0, s36
	s_nop 0
	global_load_lds_dwordx4 v[70:71], off
	v_lshl_add_u64 v[70:71], s[34:35], 0, v[148:149]
	s_add_i32 m0, s36, 0x2000
	s_nop 0
	global_load_lds_dwordx4 v[70:71], off
	s_waitcnt vmcnt(6)
	s_barrier
	v_mfma_f32_16x16x32_bf16 v[54:57], v[192:195], v[154:157], v[54:57]
	v_mfma_f32_16x16x32_bf16 v[50:53], v[200:203], v[154:157], v[50:53]
	v_mfma_f32_16x16x32_bf16 v[38:41], v[192:195], v[168:171], v[38:41]
	v_mfma_f32_16x16x32_bf16 v[34:37], v[200:203], v[168:171], v[34:37]
	v_mfma_f32_16x16x32_bf16 v[14:17], v[192:195], v[176:179], v[14:17]
	v_mfma_f32_16x16x32_bf16 v[10:13], v[200:203], v[176:179], v[10:13]
	v_mfma_f32_16x16x32_bf16 v[6:9], v[192:195], v[184:187], v[6:9]
	v_mfma_f32_16x16x32_bf16 v[2:5], v[200:203], v[184:187], v[2:5]
	v_mfma_f32_16x16x32_bf16 v[54:57], v[196:199], v[164:167], v[54:57]
	v_mfma_f32_16x16x32_bf16 v[50:53], v[204:207], v[164:167], v[50:53]
	v_mfma_f32_16x16x32_bf16 v[38:41], v[196:199], v[172:175], v[38:41]
	v_mfma_f32_16x16x32_bf16 v[34:37], v[204:207], v[172:175], v[34:37]
	v_mfma_f32_16x16x32_bf16 v[14:17], v[196:199], v[180:183], v[14:17]
	v_mfma_f32_16x16x32_bf16 v[10:13], v[204:207], v[180:183], v[10:13]
	v_mfma_f32_16x16x32_bf16 v[6:9], v[196:199], v[188:191], v[6:9]
	v_mfma_f32_16x16x32_bf16 v[2:5], v[204:207], v[188:191], v[2:5]
	s_add_i32 s45, s45, 2
	s_add_u32 s30, s30, 0x100
	s_addc_u32 s31, s31, 0
	s_add_u32 s43, s43, 0x100
	s_addc_u32 s44, s44, 0
	s_cmp_gt_u32 s45, 29
	s_barrier
	s_cbranch_scc0 .LBB0_1592
	v_lshl_or_b32 v70, s39, 8, v161
	v_lshl_add_u32 v154, s40, 8, v1
	v_ashrrev_i32_e32 v71, 31, v70
	v_readlane_b32 s30, v253, 28
	v_lshlrev_b64 v[156:157], 2, v[70:71]
	v_readlane_b32 s31, v253, 29
	v_ashrrev_i32_e32 v155, 31, v154
	v_lshlrev_b64 v[164:165], 13, v[154:155]
	v_lshl_add_u64 v[158:159], s[30:31], 0, v[156:157]
	v_lshl_add_u64 v[70:71], s[22:23], 0, v[156:157]
	v_lshl_add_u64 v[176:177], v[158:159], 0, v[164:165]
	global_load_dwordx4 v[86:89], v[70:71], off
	global_load_dwordx4 v[82:85], v[70:71], off offset:64
	global_load_dwordx4 v[78:81], v[70:71], off offset:512
	s_nop 0
	global_load_dwordx4 v[70:73], v[70:71], off offset:576
	s_nop 0
	global_load_dwordx4 v[164:167], v[176:177], off
	global_load_dwordx4 v[168:171], v[176:177], off offset:64
	global_load_dwordx4 v[172:175], v[176:177], off offset:512
	s_nop 0
	global_load_dwordx4 v[176:179], v[176:177], off offset:576
	v_or_b32_e32 v180, 16, v154
	v_ashrrev_i32_e32 v181, 31, v180
	v_lshlrev_b64 v[180:181], 13, v[180:181]
	v_lshl_add_u64 v[192:193], v[158:159], 0, v[180:181]
	global_load_dwordx4 v[180:183], v[192:193], off
	global_load_dwordx4 v[184:187], v[192:193], off offset:64
	global_load_dwordx4 v[188:191], v[192:193], off offset:512
	s_nop 0
	global_load_dwordx4 v[192:195], v[192:193], off offset:576
	v_add_u32_e32 v196, 0x100, v154
	v_ashrrev_i32_e32 v197, 31, v196
	v_lshlrev_b64 v[196:197], 13, v[196:197]
	v_lshl_add_u64 v[196:197], s[76:77], 0, v[196:197]
	v_lshl_add_u64 v[196:197], v[196:197], 0, v[156:157]
	s_and_b64 vcc, exec, s[0:1]
	s_mov_b32 s39, s18
	s_mov_b32 s40, s24
	s_mov_b64 s[34:35], s[28:29]
	s_mov_b64 s[30:31], s[26:27]
	s_waitcnt vmcnt(0)
	v_pk_fma_f32 v[146:147], v[146:147], v[88:89], v[166:167]
	v_pk_fma_f32 v[144:145], v[144:145], v[86:87], v[164:165]
	v_pk_fma_f32 v[142:143], v[142:143], v[84:85], v[170:171]
	v_pk_fma_f32 v[134:135], v[134:135], v[72:73], v[178:179]
	v_pk_fma_f32 v[132:133], v[132:133], v[70:71], v[176:177]
	global_store_dwordx4 v[196:197], v[132:135], off offset:576
	v_pk_fma_f32 v[140:141], v[140:141], v[82:83], v[168:169]
	v_pk_fma_f32 v[138:139], v[138:139], v[80:81], v[174:175]
	v_add_u32_e32 v132, 0x110, v154
	v_ashrrev_i32_e32 v133, 31, v132
	v_lshlrev_b64 v[132:133], 13, v[132:133]
	v_lshl_add_u64 v[132:133], s[76:77], 0, v[132:133]
	v_lshl_add_u64 v[132:133], v[132:133], 0, v[156:157]
	v_pk_fma_f32 v[118:119], v[118:119], v[72:73], v[194:195]
	v_pk_fma_f32 v[116:117], v[116:117], v[70:71], v[192:193]
	global_store_dwordx4 v[132:133], v[116:119], off offset:576
	v_pk_fma_f32 v[136:137], v[136:137], v[78:79], v[172:173]
	v_pk_fma_f32 v[130:131], v[130:131], v[88:89], v[182:183]
	v_or_b32_e32 v116, 32, v154
	v_ashrrev_i32_e32 v117, 31, v116
	v_pk_fma_f32 v[128:129], v[128:129], v[86:87], v[180:181]
	v_pk_fma_f32 v[126:127], v[126:127], v[84:85], v[186:187]
	v_pk_fma_f32 v[124:125], v[124:125], v[82:83], v[184:185]
	v_pk_fma_f32 v[122:123], v[122:123], v[80:81], v[190:191]
	v_pk_fma_f32 v[120:121], v[120:121], v[78:79], v[188:189]
	v_lshlrev_b64 v[116:117], 13, v[116:117]
	global_store_dwordx4 v[196:197], v[144:147], off
	global_store_dwordx4 v[196:197], v[140:143], off offset:64
	global_store_dwordx4 v[196:197], v[136:139], off offset:512
	global_store_dwordx4 v[132:133], v[128:131], off
	global_store_dwordx4 v[132:133], v[124:127], off offset:64
	global_store_dwordx4 v[132:133], v[120:123], off offset:512
	v_lshl_add_u64 v[128:129], v[158:159], 0, v[116:117]
	global_load_dwordx4 v[116:119], v[128:129], off
	global_load_dwordx4 v[120:123], v[128:129], off offset:64
	global_load_dwordx4 v[124:127], v[128:129], off offset:512
	s_nop 0
	global_load_dwordx4 v[128:131], v[128:129], off offset:576
	v_or_b32_e32 v132, 48, v154
	v_ashrrev_i32_e32 v133, 31, v132
	v_lshlrev_b64 v[132:133], 13, v[132:133]
	v_lshl_add_u64 v[144:145], v[158:159], 0, v[132:133]
	global_load_dwordx4 v[132:135], v[144:145], off
	global_load_dwordx4 v[136:139], v[144:145], off offset:64
	global_load_dwordx4 v[140:143], v[144:145], off offset:512
	s_nop 0
	global_load_dwordx4 v[144:147], v[144:145], off offset:576
	v_add_u32_e32 v164, 0x120, v154
	v_ashrrev_i32_e32 v165, 31, v164
	v_lshlrev_b64 v[164:165], 13, v[164:165]
	v_lshl_add_u64 v[164:165], s[76:77], 0, v[164:165]
	v_lshl_add_u64 v[164:165], v[164:165], 0, v[156:157]
	s_waitcnt vmcnt(0)
	v_pk_fma_f32 v[114:115], v[114:115], v[88:89], v[118:119]
	v_pk_fma_f32 v[112:113], v[112:113], v[86:87], v[116:117]
	v_pk_fma_f32 v[110:111], v[110:111], v[84:85], v[122:123]
	v_pk_fma_f32 v[102:103], v[102:103], v[72:73], v[130:131]
	v_pk_fma_f32 v[100:101], v[100:101], v[70:71], v[128:129]
	global_store_dwordx4 v[164:165], v[100:103], off offset:576
	v_pk_fma_f32 v[108:109], v[108:109], v[82:83], v[120:121]
	v_pk_fma_f32 v[106:107], v[106:107], v[80:81], v[126:127]
	v_add_u32_e32 v100, 0x130, v154
	v_ashrrev_i32_e32 v101, 31, v100
	v_lshlrev_b64 v[100:101], 13, v[100:101]
	v_lshl_add_u64 v[100:101], s[76:77], 0, v[100:101]
	v_lshl_add_u64 v[100:101], v[100:101], 0, v[156:157]
	v_pk_fma_f32 v[68:69], v[68:69], v[72:73], v[146:147]
	v_pk_fma_f32 v[66:67], v[66:67], v[70:71], v[144:145]
	global_store_dwordx4 v[100:101], v[66:69], off offset:576
	v_pk_fma_f32 v[104:105], v[104:105], v[78:79], v[124:125]
	v_pk_fma_f32 v[96:97], v[96:97], v[88:89], v[134:135]
	v_add_u32_e32 v66, 0x80, v154
	v_ashrrev_i32_e32 v67, 31, v66
	v_pk_fma_f32 v[94:95], v[94:95], v[86:87], v[132:133]
	v_pk_fma_f32 v[92:93], v[92:93], v[84:85], v[138:139]
	v_pk_fma_f32 v[90:91], v[90:91], v[82:83], v[136:137]
	v_pk_fma_f32 v[76:77], v[76:77], v[80:81], v[142:143]
	v_pk_fma_f32 v[74:75], v[74:75], v[78:79], v[140:141]
	v_lshlrev_b64 v[66:67], 13, v[66:67]
	global_store_dwordx4 v[164:165], v[112:115], off
	global_store_dwordx4 v[164:165], v[108:111], off offset:64
	global_store_dwordx4 v[164:165], v[104:107], off offset:512
	global_store_dwordx4 v[100:101], v[94:97], off
	global_store_dwordx4 v[100:101], v[90:93], off offset:64
	global_store_dwordx4 v[100:101], v[74:77], off offset:512
	v_lshl_add_u64 v[94:95], v[158:159], 0, v[66:67]
	global_load_dwordx4 v[66:69], v[94:95], off
	global_load_dwordx4 v[74:77], v[94:95], off offset:64
	global_load_dwordx4 v[90:93], v[94:95], off offset:512
	s_nop 0
	global_load_dwordx4 v[94:97], v[94:95], off offset:576
	v_add_u32_e32 v100, 0x90, v154
	v_ashrrev_i32_e32 v101, 31, v100
	v_lshlrev_b64 v[100:101], 13, v[100:101]
	v_lshl_add_u64 v[112:113], v[158:159], 0, v[100:101]
	global_load_dwordx4 v[100:103], v[112:113], off
	global_load_dwordx4 v[104:107], v[112:113], off offset:64
	global_load_dwordx4 v[108:111], v[112:113], off offset:512
	s_nop 0
	global_load_dwordx4 v[112:115], v[112:113], off offset:576
	v_add_u32_e32 v116, 0x180, v154
	v_ashrrev_i32_e32 v117, 31, v116
	v_lshlrev_b64 v[116:117], 13, v[116:117]
	v_lshl_add_u64 v[116:117], s[76:77], 0, v[116:117]
	v_lshl_add_u64 v[116:117], v[116:117], 0, v[156:157]
	s_waitcnt vmcnt(0)
	v_pk_fma_f32 v[64:65], v[64:65], v[88:89], v[68:69]
	v_pk_fma_f32 v[62:63], v[62:63], v[86:87], v[66:67]
	v_pk_fma_f32 v[60:61], v[60:61], v[84:85], v[76:77]
	v_pk_fma_f32 v[52:53], v[52:53], v[72:73], v[96:97]
	v_pk_fma_f32 v[50:51], v[50:51], v[70:71], v[94:95]
	global_store_dwordx4 v[116:117], v[50:53], off offset:576
	v_pk_fma_f32 v[58:59], v[58:59], v[82:83], v[74:75]
	v_pk_fma_f32 v[56:57], v[56:57], v[80:81], v[92:93]
	v_add_u32_e32 v50, 0x190, v154
	v_ashrrev_i32_e32 v51, 31, v50
	v_lshlrev_b64 v[50:51], 13, v[50:51]
	v_lshl_add_u64 v[50:51], s[76:77], 0, v[50:51]
	v_lshl_add_u64 v[50:51], v[50:51], 0, v[156:157]
	v_pk_fma_f32 v[36:37], v[36:37], v[72:73], v[114:115]
	v_pk_fma_f32 v[34:35], v[34:35], v[70:71], v[112:113]
	global_store_dwordx4 v[50:51], v[34:37], off offset:576
	v_pk_fma_f32 v[54:55], v[54:55], v[78:79], v[90:91]
	v_pk_fma_f32 v[48:49], v[48:49], v[88:89], v[102:103]
	v_add_u32_e32 v34, 0xa0, v154
	v_ashrrev_i32_e32 v35, 31, v34
	v_pk_fma_f32 v[46:47], v[46:47], v[86:87], v[100:101]
	v_pk_fma_f32 v[44:45], v[44:45], v[84:85], v[106:107]
	v_pk_fma_f32 v[42:43], v[42:43], v[82:83], v[104:105]
	v_pk_fma_f32 v[40:41], v[40:41], v[80:81], v[110:111]
	v_pk_fma_f32 v[38:39], v[38:39], v[78:79], v[108:109]
	v_lshlrev_b64 v[34:35], 13, v[34:35]
	global_store_dwordx4 v[116:117], v[62:65], off
	global_store_dwordx4 v[116:117], v[58:61], off offset:64
	global_store_dwordx4 v[116:117], v[54:57], off offset:512
	global_store_dwordx4 v[50:51], v[46:49], off
	global_store_dwordx4 v[50:51], v[42:45], off offset:64
	global_store_dwordx4 v[50:51], v[38:41], off offset:512
	v_lshl_add_u64 v[46:47], v[158:159], 0, v[34:35]
	global_load_dwordx4 v[34:37], v[46:47], off
	global_load_dwordx4 v[38:41], v[46:47], off offset:64
	global_load_dwordx4 v[42:45], v[46:47], off offset:512
	s_nop 0
	global_load_dwordx4 v[46:49], v[46:47], off offset:576
	v_add_u32_e32 v50, 0xb0, v154
	v_ashrrev_i32_e32 v51, 31, v50
	v_lshlrev_b64 v[50:51], 13, v[50:51]
	v_lshl_add_u64 v[62:63], v[158:159], 0, v[50:51]
	global_load_dwordx4 v[50:53], v[62:63], off
	global_load_dwordx4 v[54:57], v[62:63], off offset:64
	global_load_dwordx4 v[58:61], v[62:63], off offset:512
	s_nop 0
	global_load_dwordx4 v[62:65], v[62:63], off offset:576
	v_add_u32_e32 v66, 0x1a0, v154
	v_ashrrev_i32_e32 v67, 31, v66
	v_lshlrev_b64 v[66:67], 13, v[66:67]
	v_lshl_add_u64 v[66:67], s[76:77], 0, v[66:67]
	v_lshl_add_u64 v[66:67], v[66:67], 0, v[156:157]
	s_waitcnt vmcnt(0)
	v_pk_fma_f32 v[32:33], v[32:33], v[88:89], v[36:37]
	v_pk_fma_f32 v[30:31], v[30:31], v[86:87], v[34:35]
	v_pk_fma_f32 v[16:17], v[16:17], v[80:81], v[44:45]
	v_pk_fma_f32 v[12:13], v[12:13], v[72:73], v[48:49]
	v_pk_fma_f32 v[10:11], v[10:11], v[70:71], v[46:47]
	global_store_dwordx4 v[66:67], v[10:13], off offset:576
	v_pk_fma_f32 v[14:15], v[14:15], v[78:79], v[42:43]
	global_store_dwordx4 v[66:67], v[14:17], off offset:512
	v_add_u32_e32 v10, 0x1b0, v154
	v_ashrrev_i32_e32 v11, 31, v10
	v_lshlrev_b64 v[10:11], 13, v[10:11]
	v_lshl_add_u64 v[10:11], s[76:77], 0, v[10:11]
	v_lshl_add_u64 v[14:15], v[10:11], 0, v[156:157]
	v_pk_fma_f32 v[12:13], v[24:25], v[88:89], v[52:53]
	v_pk_fma_f32 v[10:11], v[22:23], v[86:87], v[50:51]
	v_pk_fma_f32 v[28:29], v[28:29], v[84:85], v[40:41]
	v_pk_fma_f32 v[26:27], v[26:27], v[82:83], v[38:39]
	global_store_dwordx4 v[14:15], v[10:13], off
	v_pk_fma_f32 v[8:9], v[8:9], v[80:81], v[60:61]
	v_pk_fma_f32 v[6:7], v[6:7], v[78:79], v[58:59]
	v_pk_fma_f32 v[12:13], v[20:21], v[84:85], v[56:57]
	v_pk_fma_f32 v[10:11], v[18:19], v[82:83], v[54:55]
	v_pk_fma_f32 v[4:5], v[4:5], v[72:73], v[64:65]
	v_pk_fma_f32 v[2:3], v[2:3], v[70:71], v[62:63]
	global_store_dwordx4 v[66:67], v[30:33], off
	global_store_dwordx4 v[66:67], v[26:29], off offset:64
	global_store_dwordx4 v[14:15], v[10:13], off offset:64
	global_store_dwordx4 v[14:15], v[6:9], off offset:512
	global_store_dwordx4 v[14:15], v[2:5], off offset:576
	s_cbranch_vccz .LBB0_1585
	s_waitcnt vmcnt(0)
	s_cmpk_gt_u32 s3, 0xff
	v_readlane_b32 s33, v255, 42
	s_cbranch_scc1 .LBB0_1596
	s_barrier

.LBB0_1616:
	s_add_i32 s50, s42, 2
	s_add_u32 s43, s40, 0xfff80080
	s_addc_u32 s44, s41, -1
	s_add_i32 s51, 0, 0x10000
	v_add_u32_e32 v144, s51, v1
	ds_read_b128 v[132:135], v144
	ds_read_b128 v[136:139], v144 offset:1024
	ds_read_b128 v[140:143], v144 offset:2048
	ds_read_b128 v[144:147], v144 offset:3072
	s_cmp_eq_u32 s47, s42
	s_cselect_b32 s42, s39, s48
	s_cselect_b32 s45, s1, s44
	s_cselect_b32 s44, s27, s43
	s_cselect_b32 s43, s25, s49
	v_lshl_add_u64 v[166:167], s[40:41], 0, v[154:155]
	s_add_i32 m0, s5, 0xc000
	ds_read_b128 v[158:161], v168
	ds_read_b128 v[162:165], v168 offset:1024
	ds_read_b128 v[170:173], v168 offset:2048
	ds_read_b128 v[174:177], v168 offset:3072
	ds_read_b128 v[178:181], v168 offset:4096
	ds_read_b128 v[182:185], v168 offset:5120
	ds_read_b128 v[186:189], v168 offset:6144
	ds_read_b128 v[190:193], v168 offset:7168
	global_load_lds_dwordx4 v[166:167], off
	v_lshl_add_u64 v[166:167], s[40:41], 0, v[156:157]
	s_add_i32 m0, s5, 0xe000
	s_nop 0
	global_load_lds_dwordx4 v[166:167], off
	s_waitcnt lgkmcnt(8)
	s_barrier
	v_add_u32_e32 v250, 0x14000, v1
	ds_read_b128 v[194:197], v250
	ds_read_b128 v[198:201], v250 offset:1024
	ds_read_b128 v[202:205], v250 offset:2048
	ds_read_b128 v[206:209], v250 offset:3072
	s_waitcnt lgkmcnt(4)
	s_waitcnt lgkmcnt(4)
	v_mfma_f32_16x16x32_bf16 v[128:131], v[132:135], v[158:161], v[128:131]
	v_mfma_f32_16x16x32_bf16 v[124:127], v[140:143], v[158:161], v[124:127]
	v_mfma_f32_16x16x32_bf16 v[120:123], v[132:135], v[170:173], v[120:123]
	v_mfma_f32_16x16x32_bf16 v[116:119], v[140:143], v[170:173], v[116:119]
	v_mfma_f32_16x16x32_bf16 v[108:111], v[132:135], v[178:181], v[108:111]
	v_mfma_f32_16x16x32_bf16 v[100:103], v[140:143], v[178:181], v[100:103]
	v_mfma_f32_16x16x32_bf16 v[90:93], v[132:135], v[186:189], v[90:93]
	v_mfma_f32_16x16x32_bf16 v[82:85], v[140:143], v[186:189], v[82:85]
	v_mfma_f32_16x16x32_bf16 v[128:131], v[136:139], v[162:165], v[128:131]
	v_mfma_f32_16x16x32_bf16 v[124:127], v[144:147], v[162:165], v[124:127]
	v_mfma_f32_16x16x32_bf16 v[120:123], v[136:139], v[174:177], v[120:123]
	v_mfma_f32_16x16x32_bf16 v[116:119], v[144:147], v[174:177], v[116:119]
	v_mfma_f32_16x16x32_bf16 v[108:111], v[136:139], v[182:185], v[108:111]
	v_mfma_f32_16x16x32_bf16 v[100:103], v[144:147], v[182:185], v[100:103]
	v_mfma_f32_16x16x32_bf16 v[90:93], v[136:139], v[190:193], v[90:93]
	v_mfma_f32_16x16x32_bf16 v[82:85], v[144:147], v[190:193], v[82:85]
	s_barrier
	s_add_i32 s64, 0, 0x14000
	v_add_u32_e32 v166, s64, v1
	s_add_i32 s51, s51, s4
	v_lshl_add_u64 v[166:167], s[42:43], 0, v[98:99]
	s_mov_b32 m0, s51
	v_lshl_add_u64 v[210:211], s[42:43], 0, v[148:149]
	global_load_lds_dwordx4 v[166:167], off
	s_add_i32 m0, s51, 0x2000
	s_nop 0
	global_load_lds_dwordx4 v[210:211], off
	s_barrier
	s_waitcnt lgkmcnt(0)
	s_waitcnt lgkmcnt(0)
	v_mfma_f32_16x16x32_bf16 v[112:115], v[194:197], v[158:161], v[112:115]
	v_mfma_f32_16x16x32_bf16 v[104:107], v[202:205], v[158:161], v[104:107]
	v_mfma_f32_16x16x32_bf16 v[94:97], v[194:197], v[170:173], v[94:97]
	v_mfma_f32_16x16x32_bf16 v[86:89], v[202:205], v[170:173], v[86:89]
	v_mfma_f32_16x16x32_bf16 v[78:81], v[194:197], v[178:181], v[78:81]
	v_mfma_f32_16x16x32_bf16 v[74:77], v[202:205], v[178:181], v[74:77]
	v_mfma_f32_16x16x32_bf16 v[70:73], v[194:197], v[186:189], v[70:73]
	v_mfma_f32_16x16x32_bf16 v[66:69], v[202:205], v[186:189], v[66:69]
	v_mfma_f32_16x16x32_bf16 v[112:115], v[198:201], v[162:165], v[112:115]
	v_mfma_f32_16x16x32_bf16 v[104:107], v[206:209], v[162:165], v[104:107]
	v_mfma_f32_16x16x32_bf16 v[94:97], v[198:201], v[174:177], v[94:97]
	v_mfma_f32_16x16x32_bf16 v[86:89], v[206:209], v[174:177], v[86:89]
	v_mfma_f32_16x16x32_bf16 v[78:81], v[198:201], v[182:185], v[78:81]
	v_mfma_f32_16x16x32_bf16 v[74:77], v[206:209], v[182:185], v[74:77]
	v_mfma_f32_16x16x32_bf16 v[70:73], v[198:201], v[190:193], v[70:73]
	v_mfma_f32_16x16x32_bf16 v[66:69], v[206:209], v[190:193], v[66:69]
	s_mov_b32 m0, s5
	v_lshl_add_u64 v[212:213], s[44:45], 0, v[98:99]
	s_barrier
	ds_read_b128 v[158:161], v168 offset:16384
	ds_read_b128 v[162:165], v168 offset:17408
	ds_read_b128 v[170:173], v168 offset:18432
	ds_read_b128 v[174:177], v168 offset:19456
	ds_read_b128 v[178:181], v168 offset:20480
	ds_read_b128 v[182:185], v168 offset:21504
	ds_read_b128 v[186:189], v168 offset:22528
	ds_read_b128 v[190:193], v168 offset:23552
	global_load_lds_dwordx4 v[212:213], off
	v_lshl_add_u64 v[214:215], s[44:45], 0, v[148:149]
	s_mov_b32 m0, s8
	s_nop 0
	global_load_lds_dwordx4 v[214:215], off
	s_barrier
	s_waitcnt lgkmcnt(0)
	s_waitcnt lgkmcnt(0)
	v_mfma_f32_16x16x32_bf16 v[62:65], v[132:135], v[158:161], v[62:65]
	v_mfma_f32_16x16x32_bf16 v[58:61], v[140:143], v[158:161], v[58:61]
	v_mfma_f32_16x16x32_bf16 v[54:57], v[132:135], v[170:173], v[54:57]
	v_mfma_f32_16x16x32_bf16 v[50:53], v[140:143], v[170:173], v[50:53]
	v_mfma_f32_16x16x32_bf16 v[42:45], v[132:135], v[178:181], v[42:45]
	v_mfma_f32_16x16x32_bf16 v[34:37], v[140:143], v[178:181], v[34:37]
	v_mfma_f32_16x16x32_bf16 v[26:29], v[132:135], v[186:189], v[26:29]
	v_mfma_f32_16x16x32_bf16 v[18:21], v[140:143], v[186:189], v[18:21]
	v_mfma_f32_16x16x32_bf16 v[62:65], v[136:139], v[162:165], v[62:65]
	v_mfma_f32_16x16x32_bf16 v[58:61], v[144:147], v[162:165], v[58:61]
	v_mfma_f32_16x16x32_bf16 v[54:57], v[136:139], v[174:177], v[54:57]
	v_mfma_f32_16x16x32_bf16 v[50:53], v[144:147], v[174:177], v[50:53]
	v_mfma_f32_16x16x32_bf16 v[42:45], v[136:139], v[182:185], v[42:45]
	v_mfma_f32_16x16x32_bf16 v[34:37], v[144:147], v[182:185], v[34:37]
	v_mfma_f32_16x16x32_bf16 v[26:29], v[136:139], v[190:193], v[26:29]
	v_mfma_f32_16x16x32_bf16 v[18:21], v[144:147], v[190:193], v[18:21]
	s_barrier
	s_add_u32 s52, s42, 0x80000
	s_addc_u32 s53, s43, 0
	s_add_i32 s51, s64, s4
	v_lshl_add_u64 v[132:133], s[52:53], 0, v[98:99]
	s_mov_b32 m0, s51
	s_nop 0
	global_load_lds_dwordx4 v[132:133], off
	v_lshl_add_u64 v[132:133], s[52:53], 0, v[148:149]
	s_add_i32 m0, s51, 0x2000
	s_nop 0
	global_load_lds_dwordx4 v[132:133], off
	s_waitcnt vmcnt(6)
	s_barrier
	v_mfma_f32_16x16x32_bf16 v[46:49], v[194:197], v[158:161], v[46:49]
	v_mfma_f32_16x16x32_bf16 v[38:41], v[202:205], v[158:161], v[38:41]
	v_mfma_f32_16x16x32_bf16 v[30:33], v[194:197], v[170:173], v[30:33]
	v_mfma_f32_16x16x32_bf16 v[22:25], v[202:205], v[170:173], v[22:25]
	v_mfma_f32_16x16x32_bf16 v[14:17], v[194:197], v[178:181], v[14:17]
	v_mfma_f32_16x16x32_bf16 v[10:13], v[202:205], v[178:181], v[10:13]
	v_mfma_f32_16x16x32_bf16 v[6:9], v[194:197], v[186:189], v[6:9]
	v_mfma_f32_16x16x32_bf16 v[2:5], v[202:205], v[186:189], v[2:5]
	v_mfma_f32_16x16x32_bf16 v[46:49], v[198:201], v[162:165], v[46:49]
	v_mfma_f32_16x16x32_bf16 v[38:41], v[206:209], v[162:165], v[38:41]
	v_mfma_f32_16x16x32_bf16 v[30:33], v[198:201], v[174:177], v[30:33]
	v_mfma_f32_16x16x32_bf16 v[22:25], v[206:209], v[174:177], v[22:25]
	v_mfma_f32_16x16x32_bf16 v[14:17], v[198:201], v[182:185], v[14:17]
	v_mfma_f32_16x16x32_bf16 v[10:13], v[206:209], v[182:185], v[10:13]
	v_mfma_f32_16x16x32_bf16 v[6:9], v[198:201], v[190:193], v[6:9]
	v_mfma_f32_16x16x32_bf16 v[2:5], v[206:209], v[190:193], v[2:5]
	s_add_i32 s51, 0, 0x18000
	v_add_u32_e32 v144, s51, v1
	s_barrier
	ds_read_b128 v[132:135], v144
	ds_read_b128 v[136:139], v144 offset:1024
	ds_read_b128 v[140:143], v144 offset:2048
	ds_read_b128 v[144:147], v144 offset:3072
	s_add_u32 s44, s44, 0x80000
	s_addc_u32 s45, s45, 0
	s_mov_b32 m0, s9
	v_lshl_add_u64 v[194:195], s[44:45], 0, v[98:99]
	ds_read_b128 v[158:161], v168 offset:32768
	ds_read_b128 v[162:165], v168 offset:33792
	ds_read_b128 v[170:173], v168 offset:34816
	ds_read_b128 v[174:177], v168 offset:35840
	ds_read_b128 v[178:181], v168 offset:36864
	ds_read_b128 v[182:185], v168 offset:37888
	ds_read_b128 v[186:189], v168 offset:38912
	ds_read_b128 v[190:193], v168 offset:39936
	global_load_lds_dwordx4 v[194:195], off
	v_lshl_add_u64 v[194:195], s[44:45], 0, v[148:149]
	s_mov_b32 m0, s18
	s_nop 0
	global_load_lds_dwordx4 v[194:195], off
	s_waitcnt lgkmcnt(8)
	s_barrier
	v_add_u32_e32 v250, 0x1c000, v1
	ds_read_b128 v[194:197], v250
	ds_read_b128 v[198:201], v250 offset:1024
	ds_read_b128 v[202:205], v250 offset:2048
	ds_read_b128 v[206:209], v250 offset:3072
	s_waitcnt lgkmcnt(4)
	s_waitcnt lgkmcnt(4)
	v_mfma_f32_16x16x32_bf16 v[128:131], v[132:135], v[158:161], v[128:131]
	v_mfma_f32_16x16x32_bf16 v[124:127], v[140:143], v[158:161], v[124:127]
	v_mfma_f32_16x16x32_bf16 v[120:123], v[132:135], v[170:173], v[120:123]
	v_mfma_f32_16x16x32_bf16 v[116:119], v[140:143], v[170:173], v[116:119]
	v_mfma_f32_16x16x32_bf16 v[108:111], v[132:135], v[178:181], v[108:111]
	v_mfma_f32_16x16x32_bf16 v[100:103], v[140:143], v[178:181], v[100:103]
	v_mfma_f32_16x16x32_bf16 v[90:93], v[132:135], v[186:189], v[90:93]
	v_mfma_f32_16x16x32_bf16 v[82:85], v[140:143], v[186:189], v[82:85]
	v_mfma_f32_16x16x32_bf16 v[128:131], v[136:139], v[162:165], v[128:131]
	v_mfma_f32_16x16x32_bf16 v[124:127], v[144:147], v[162:165], v[124:127]
	v_mfma_f32_16x16x32_bf16 v[120:123], v[136:139], v[174:177], v[120:123]
	v_mfma_f32_16x16x32_bf16 v[116:119], v[144:147], v[174:177], v[116:119]
	v_mfma_f32_16x16x32_bf16 v[108:111], v[136:139], v[182:185], v[108:111]
	v_mfma_f32_16x16x32_bf16 v[100:103], v[144:147], v[182:185], v[100:103]
	v_mfma_f32_16x16x32_bf16 v[90:93], v[136:139], v[190:193], v[90:93]
	v_mfma_f32_16x16x32_bf16 v[82:85], v[144:147], v[190:193], v[82:85]
	s_barrier
	s_add_i32 s44, 0, 0x1c000
	s_add_i32 s45, s51, s4
	v_add_u32_e32 v169, s44, v1
	v_lshl_add_u64 v[166:167], v[166:167], 0, s[68:69]
	s_mov_b32 m0, s45
	global_load_lds_dwordx4 v[166:167], off
	v_lshl_add_u64 v[166:167], v[210:211], 0, s[68:69]
	s_add_i32 m0, s45, 0x2000
	s_nop 0
	global_load_lds_dwordx4 v[166:167], off
	s_barrier
	s_waitcnt lgkmcnt(0)
	s_waitcnt lgkmcnt(0)
	v_mfma_f32_16x16x32_bf16 v[112:115], v[194:197], v[158:161], v[112:115]
	v_mfma_f32_16x16x32_bf16 v[104:107], v[202:205], v[158:161], v[104:107]
	v_mfma_f32_16x16x32_bf16 v[94:97], v[194:197], v[170:173], v[94:97]
	v_mfma_f32_16x16x32_bf16 v[86:89], v[202:205], v[170:173], v[86:89]
	v_mfma_f32_16x16x32_bf16 v[78:81], v[194:197], v[178:181], v[78:81]
	v_mfma_f32_16x16x32_bf16 v[74:77], v[202:205], v[178:181], v[74:77]
	v_mfma_f32_16x16x32_bf16 v[70:73], v[194:197], v[186:189], v[70:73]
	v_mfma_f32_16x16x32_bf16 v[66:69], v[202:205], v[186:189], v[66:69]
	v_mfma_f32_16x16x32_bf16 v[112:115], v[198:201], v[162:165], v[112:115]
	v_mfma_f32_16x16x32_bf16 v[104:107], v[206:209], v[162:165], v[104:107]
	v_mfma_f32_16x16x32_bf16 v[94:97], v[198:201], v[174:177], v[94:97]
	v_mfma_f32_16x16x32_bf16 v[86:89], v[206:209], v[174:177], v[86:89]
	v_mfma_f32_16x16x32_bf16 v[78:81], v[198:201], v[182:185], v[78:81]
	v_mfma_f32_16x16x32_bf16 v[74:77], v[206:209], v[182:185], v[74:77]
	v_mfma_f32_16x16x32_bf16 v[70:73], v[198:201], v[190:193], v[70:73]
	v_mfma_f32_16x16x32_bf16 v[66:69], v[206:209], v[190:193], v[66:69]
	s_mov_b32 m0, s19
	v_lshl_add_u64 v[166:167], v[212:213], 0, s[68:69]
	s_barrier
	ds_read_b128 v[158:161], v168 offset:49152
	ds_read_b128 v[162:165], v168 offset:50176
	ds_read_b128 v[170:173], v168 offset:51200
	ds_read_b128 v[174:177], v168 offset:52224
	ds_read_b128 v[178:181], v168 offset:53248
	ds_read_b128 v[182:185], v168 offset:54272
	ds_read_b128 v[186:189], v168 offset:55296
	ds_read_b128 v[190:193], v168 offset:56320
	global_load_lds_dwordx4 v[166:167], off
	v_lshl_add_u64 v[166:167], v[214:215], 0, s[68:69]
	s_mov_b32 m0, s20
	s_nop 0
	global_load_lds_dwordx4 v[166:167], off
	s_barrier
	s_waitcnt lgkmcnt(0)
	s_waitcnt lgkmcnt(0)
	v_mfma_f32_16x16x32_bf16 v[62:65], v[132:135], v[158:161], v[62:65]
	v_mfma_f32_16x16x32_bf16 v[58:61], v[140:143], v[158:161], v[58:61]
	v_mfma_f32_16x16x32_bf16 v[54:57], v[132:135], v[170:173], v[54:57]
	v_mfma_f32_16x16x32_bf16 v[50:53], v[140:143], v[170:173], v[50:53]
	v_mfma_f32_16x16x32_bf16 v[42:45], v[132:135], v[178:181], v[42:45]
	v_mfma_f32_16x16x32_bf16 v[34:37], v[140:143], v[178:181], v[34:37]
	v_mfma_f32_16x16x32_bf16 v[26:29], v[132:135], v[186:189], v[26:29]
	v_mfma_f32_16x16x32_bf16 v[18:21], v[140:143], v[186:189], v[18:21]
	v_mfma_f32_16x16x32_bf16 v[62:65], v[136:139], v[162:165], v[62:65]
	v_mfma_f32_16x16x32_bf16 v[58:61], v[144:147], v[162:165], v[58:61]
	v_mfma_f32_16x16x32_bf16 v[54:57], v[136:139], v[174:177], v[54:57]
	v_mfma_f32_16x16x32_bf16 v[50:53], v[144:147], v[174:177], v[50:53]
	v_mfma_f32_16x16x32_bf16 v[42:45], v[136:139], v[182:185], v[42:45]
	v_mfma_f32_16x16x32_bf16 v[34:37], v[144:147], v[182:185], v[34:37]
	v_mfma_f32_16x16x32_bf16 v[26:29], v[136:139], v[190:193], v[26:29]
	v_mfma_f32_16x16x32_bf16 v[18:21], v[144:147], v[190:193], v[18:21]
	s_barrier
	s_add_u32 s42, s42, 0x80080
	s_addc_u32 s43, s43, 0
	s_add_i32 s44, s44, s4
	v_lshl_add_u64 v[132:133], s[42:43], 0, v[98:99]
	s_mov_b32 m0, s44
	s_nop 0
	global_load_lds_dwordx4 v[132:133], off
	v_lshl_add_u64 v[132:133], s[42:43], 0, v[148:149]
	s_add_i32 m0, s44, 0x2000
	s_nop 0
	global_load_lds_dwordx4 v[132:133], off
	s_waitcnt vmcnt(6)
	s_barrier
	v_mfma_f32_16x16x32_bf16 v[46:49], v[194:197], v[158:161], v[46:49]
	v_mfma_f32_16x16x32_bf16 v[38:41], v[202:205], v[158:161], v[38:41]
	v_mfma_f32_16x16x32_bf16 v[30:33], v[194:197], v[170:173], v[30:33]
	v_mfma_f32_16x16x32_bf16 v[22:25], v[202:205], v[170:173], v[22:25]
	v_mfma_f32_16x16x32_bf16 v[14:17], v[194:197], v[178:181], v[14:17]
	v_mfma_f32_16x16x32_bf16 v[10:13], v[202:205], v[178:181], v[10:13]
	v_mfma_f32_16x16x32_bf16 v[6:9], v[194:197], v[186:189], v[6:9]
	v_mfma_f32_16x16x32_bf16 v[2:5], v[202:205], v[186:189], v[2:5]
	v_mfma_f32_16x16x32_bf16 v[46:49], v[198:201], v[162:165], v[46:49]
	v_mfma_f32_16x16x32_bf16 v[38:41], v[206:209], v[162:165], v[38:41]
	v_mfma_f32_16x16x32_bf16 v[30:33], v[198:201], v[174:177], v[30:33]
	v_mfma_f32_16x16x32_bf16 v[22:25], v[206:209], v[174:177], v[22:25]
	v_mfma_f32_16x16x32_bf16 v[14:17], v[198:201], v[182:185], v[14:17]
	v_mfma_f32_16x16x32_bf16 v[10:13], v[206:209], v[182:185], v[10:13]
	v_mfma_f32_16x16x32_bf16 v[6:9], v[198:201], v[190:193], v[6:9]
	v_mfma_f32_16x16x32_bf16 v[2:5], v[206:209], v[190:193], v[2:5]
	s_add_u32 s40, s40, 0x100
	s_addc_u32 s41, s41, 0
	s_add_u32 s48, s48, 0x100
	s_addc_u32 s49, s49, 0
	s_cmp_ge_i32 s50, s46
	s_mov_b32 s42, s50
	s_barrier
	s_cbranch_scc0 .LBB0_1616
	v_lshl_or_b32 v158, s38, 8, v151
	v_ashrrev_i32_e32 v159, 31, v158
	s_cmp_lt_i32 s62, 0
	s_mov_b64 s[38:39], -1
	s_cbranch_scc0 .LBB0_1619
	v_lshl_add_u32 v162, s36, 8, v150
	v_add_u32_e32 v160, 0xffffff00, v162
	v_readlane_b32 s40, v251, 9
	v_lshlrev_b64 v[166:167], 2, v[158:159]
	v_readlane_b32 s41, v251, 10
	v_ashrrev_i32_e32 v161, 31, v160
	v_lshlrev_b64 v[160:161], 13, v[160:161]
	v_lshl_add_u64 v[164:165], s[40:41], 0, v[166:167]
	v_lshl_add_u64 v[132:133], s[22:23], 0, v[166:167]
	v_lshl_add_u64 v[160:161], v[164:165], 0, v[160:161]
	global_load_dwordx4 v[144:147], v[132:133], off
	global_load_dwordx4 v[140:143], v[132:133], off offset:64
	global_load_dwordx4 v[136:139], v[132:133], off offset:512
	s_nop 0
	global_load_dwordx4 v[132:135], v[132:133], off offset:576
	s_nop 0
	global_load_dwordx4 v[170:173], v[160:161], off
	global_load_dwordx4 v[174:177], v[160:161], off offset:64
	global_load_dwordx4 v[178:181], v[160:161], off offset:512
	global_load_dwordx4 v[182:185], v[160:161], off offset:576
	v_add_u32_e32 v160, 0xffffff10, v162
	v_ashrrev_i32_e32 v161, 31, v160
	v_lshlrev_b64 v[160:161], 13, v[160:161]
	v_lshl_add_u64 v[160:161], v[164:165], 0, v[160:161]
	global_load_dwordx4 v[186:189], v[160:161], off
	global_load_dwordx4 v[190:193], v[160:161], off offset:64
	global_load_dwordx4 v[194:197], v[160:161], off offset:512
	global_load_dwordx4 v[198:201], v[160:161], off offset:576
	v_ashrrev_i32_e32 v163, 31, v162
	v_lshlrev_b64 v[160:161], 13, v[162:163]
	v_lshl_add_u64 v[160:161], s[76:77], 0, v[160:161]
	v_lshl_add_u64 v[160:161], v[160:161], 0, v[166:167]
	v_or_b32_e32 v202, 32, v162
	v_ashrrev_i32_e32 v203, 31, v202
	v_lshlrev_b64 v[202:203], 13, v[202:203]
	v_lshl_add_u64 v[202:203], s[76:77], 0, v[202:203]
	v_lshl_add_u64 v[202:203], v[202:203], 0, v[166:167]
	s_mov_b32 s1, 0x100000
	s_mov_b64 s[38:39], 0x100000
	v_readlane_b32 s54, v251, 23
	v_readlane_b32 s55, v251, 24
	v_readlane_b32 s54, v255, 43
	v_readlane_b32 s42, v251, 11
	v_readlane_b32 s43, v251, 12
	v_readlane_b32 s44, v251, 13
	v_readlane_b32 s45, v251, 14
	v_readlane_b32 s46, v251, 15
	v_readlane_b32 s47, v251, 16
	v_readlane_b32 s48, v251, 17
	v_readlane_b32 s49, v251, 18
	v_readlane_b32 s50, v251, 19
	v_readlane_b32 s51, v251, 20
	v_readlane_b32 s52, v251, 21
	v_readlane_b32 s53, v251, 22
	v_readlane_b32 s55, v255, 44
	s_waitcnt vmcnt(0)
	v_pk_fma_f32 v[172:173], v[130:131], v[146:147], v[172:173]
	v_pk_fma_f32 v[170:171], v[128:129], v[144:145], v[170:171]
	global_store_dwordx4 v[160:161], v[170:173], off
	s_nop 1
	v_pk_fma_f32 v[172:173], v[126:127], v[142:143], v[176:177]
	v_pk_fma_f32 v[170:171], v[124:125], v[140:141], v[174:175]
	global_store_dwordx4 v[160:161], v[170:173], off offset:64
	s_nop 1
	v_pk_fma_f32 v[172:173], v[114:115], v[138:139], v[180:181]
	v_pk_fma_f32 v[170:171], v[112:113], v[136:137], v[178:179]
	global_store_dwordx4 v[160:161], v[170:173], off offset:512
	s_nop 1
	v_pk_fma_f32 v[172:173], v[106:107], v[134:135], v[184:185]
	v_pk_fma_f32 v[170:171], v[104:105], v[132:133], v[182:183]
	global_store_dwordx4 v[160:161], v[170:173], off offset:576
	s_nop 1
	v_or_b32_e32 v170, 16, v162
	v_ashrrev_i32_e32 v171, 31, v170
	v_lshlrev_b64 v[170:171], 13, v[170:171]
	v_lshl_add_u64 v[170:171], s[76:77], 0, v[170:171]
	v_lshl_add_u64 v[174:175], v[170:171], 0, v[166:167]
	v_pk_fma_f32 v[172:173], v[122:123], v[146:147], v[188:189]
	v_pk_fma_f32 v[170:171], v[120:121], v[144:145], v[186:187]
	global_store_dwordx4 v[174:175], v[170:173], off
	v_add_u32_e32 v186, 0xffffff30, v162
	v_ashrrev_i32_e32 v187, 31, v186
	v_pk_fma_f32 v[172:173], v[118:119], v[142:143], v[192:193]
	v_pk_fma_f32 v[170:171], v[116:117], v[140:141], v[190:191]
	global_store_dwordx4 v[174:175], v[170:173], off offset:64
	v_lshlrev_b64 v[186:187], 13, v[186:187]
	s_nop 0
	v_pk_fma_f32 v[172:173], v[96:97], v[138:139], v[196:197]
	v_pk_fma_f32 v[170:171], v[94:95], v[136:137], v[194:195]
	global_store_dwordx4 v[174:175], v[170:173], off offset:512
	s_nop 1
	v_pk_fma_f32 v[172:173], v[88:89], v[134:135], v[200:201]
	v_pk_fma_f32 v[170:171], v[86:87], v[132:133], v[198:199]
	global_store_dwordx4 v[174:175], v[170:173], off offset:576
	v_lshl_add_u64 v[198:199], v[164:165], 0, v[186:187]
	s_nop 0
	v_add_u32_e32 v170, 0xffffff20, v162
	v_ashrrev_i32_e32 v171, 31, v170
	v_lshlrev_b64 v[170:171], 13, v[170:171]
	v_lshl_add_u64 v[182:183], v[164:165], 0, v[170:171]
	global_load_dwordx4 v[170:173], v[182:183], off
	global_load_dwordx4 v[174:177], v[182:183], off offset:64
	global_load_dwordx4 v[178:181], v[182:183], off offset:512
	s_nop 0
	global_load_dwordx4 v[182:185], v[182:183], off offset:576
	s_nop 0
	global_load_dwordx4 v[186:189], v[198:199], off
	global_load_dwordx4 v[190:193], v[198:199], off offset:64
	global_load_dwordx4 v[194:197], v[198:199], off offset:512
	s_nop 0
	global_load_dwordx4 v[198:201], v[198:199], off offset:576
	s_waitcnt vmcnt(0)
	v_pk_fma_f32 v[172:173], v[110:111], v[146:147], v[172:173]
	v_pk_fma_f32 v[170:171], v[108:109], v[144:145], v[170:171]
	global_store_dwordx4 v[202:203], v[170:173], off
	s_nop 1
	v_pk_fma_f32 v[172:173], v[102:103], v[142:143], v[176:177]
	v_pk_fma_f32 v[170:171], v[100:101], v[140:141], v[174:175]
	global_store_dwordx4 v[202:203], v[170:173], off offset:64
	s_nop 1
	v_pk_fma_f32 v[172:173], v[80:81], v[138:139], v[180:181]
	v_pk_fma_f32 v[170:171], v[78:79], v[136:137], v[178:179]
	global_store_dwordx4 v[202:203], v[170:173], off offset:512
	s_nop 1
	v_pk_fma_f32 v[172:173], v[76:77], v[134:135], v[184:185]
	v_pk_fma_f32 v[170:171], v[74:75], v[132:133], v[182:183]
	global_store_dwordx4 v[202:203], v[170:173], off offset:576
	v_add_co_u32_e32 v202, vcc, s1, v160
	s_nop 0
	v_or_b32_e32 v170, 48, v162
	v_ashrrev_i32_e32 v171, 31, v170
	v_lshlrev_b64 v[170:171], 13, v[170:171]
	v_lshl_add_u64 v[170:171], s[76:77], 0, v[170:171]
	v_lshl_add_u64 v[166:167], v[170:171], 0, v[166:167]
	v_pk_fma_f32 v[172:173], v[92:93], v[146:147], v[188:189]
	v_pk_fma_f32 v[170:171], v[90:91], v[144:145], v[186:187]
	global_store_dwordx4 v[166:167], v[170:173], off
	v_addc_co_u32_e32 v203, vcc, 0, v161, vcc
	s_nop 0
	v_pk_fma_f32 v[172:173], v[84:85], v[142:143], v[192:193]
	v_pk_fma_f32 v[170:171], v[82:83], v[140:141], v[190:191]
	global_store_dwordx4 v[166:167], v[170:173], off offset:64
	s_mov_b32 s1, 0x120000
	s_nop 0
	v_pk_fma_f32 v[172:173], v[72:73], v[138:139], v[196:197]
	v_pk_fma_f32 v[170:171], v[70:71], v[136:137], v[194:195]
	global_store_dwordx4 v[166:167], v[170:173], off offset:512
	s_nop 1
	v_pk_fma_f32 v[172:173], v[68:69], v[134:135], v[200:201]
	v_pk_fma_f32 v[170:171], v[66:67], v[132:133], v[198:199]
	global_store_dwordx4 v[166:167], v[170:173], off offset:576
	v_add_u32_e32 v166, 0xffffff80, v162
	v_ashrrev_i32_e32 v167, 31, v166
	v_lshlrev_b64 v[166:167], 13, v[166:167]
	v_lshl_add_u64 v[166:167], v[164:165], 0, v[166:167]
	global_load_dwordx4 v[170:173], v[166:167], off
	global_load_dwordx4 v[174:177], v[166:167], off offset:64
	global_load_dwordx4 v[178:181], v[166:167], off offset:512
	global_load_dwordx4 v[182:185], v[166:167], off offset:576
	v_add_u32_e32 v166, 0xffffff90, v162
	v_ashrrev_i32_e32 v167, 31, v166
	v_lshlrev_b64 v[166:167], 13, v[166:167]
	v_lshl_add_u64 v[166:167], v[164:165], 0, v[166:167]
	global_load_dwordx4 v[186:189], v[166:167], off
	global_load_dwordx4 v[190:193], v[166:167], off offset:64
	global_load_dwordx4 v[194:197], v[166:167], off offset:512
	global_load_dwordx4 v[198:201], v[166:167], off offset:576
	v_lshl_add_u64 v[166:167], v[160:161], 0, s[38:39]
	s_mov_b64 s[38:39], 0x120000
	s_waitcnt vmcnt(0)
	v_pk_fma_f32 v[172:173], v[64:65], v[146:147], v[172:173]
	v_pk_fma_f32 v[170:171], v[62:63], v[144:145], v[170:171]
	global_store_dwordx4 v[202:203], v[170:173], off
	s_nop 1
	v_pk_fma_f32 v[172:173], v[60:61], v[142:143], v[176:177]
	v_pk_fma_f32 v[170:171], v[58:59], v[140:141], v[174:175]
	global_store_dwordx4 v[166:167], v[170:173], off offset:64
	v_add_co_u32_e32 v174, vcc, s1, v160
	s_nop 0
	v_pk_fma_f32 v[172:173], v[48:49], v[138:139], v[180:181]
	v_pk_fma_f32 v[170:171], v[46:47], v[136:137], v[178:179]
	global_store_dwordx4 v[166:167], v[170:173], off offset:512
	v_addc_co_u32_e32 v175, vcc, 0, v161, vcc
	s_nop 0
	v_pk_fma_f32 v[172:173], v[40:41], v[134:135], v[184:185]
	v_pk_fma_f32 v[170:171], v[38:39], v[132:133], v[182:183]
	global_store_dwordx4 v[166:167], v[170:173], off offset:576
	v_lshl_add_u64 v[166:167], v[160:161], 0, s[38:39]
	s_mov_b32 s1, 0x140000
	v_pk_fma_f32 v[172:173], v[56:57], v[146:147], v[188:189]
	v_pk_fma_f32 v[170:171], v[54:55], v[144:145], v[186:187]
	global_store_dwordx4 v[174:175], v[170:173], off
	s_mov_b64 s[38:39], 0x140000
	s_nop 0
	v_pk_fma_f32 v[172:173], v[52:53], v[142:143], v[192:193]
	v_pk_fma_f32 v[170:171], v[50:51], v[140:141], v[190:191]
	global_store_dwordx4 v[166:167], v[170:173], off offset:64
	s_nop 1
	v_pk_fma_f32 v[172:173], v[32:33], v[138:139], v[196:197]
	v_pk_fma_f32 v[170:171], v[30:31], v[136:137], v[194:195]
	global_store_dwordx4 v[166:167], v[170:173], off offset:512
	s_nop 1
	v_pk_fma_f32 v[172:173], v[24:25], v[134:135], v[200:201]
	v_pk_fma_f32 v[170:171], v[22:23], v[132:133], v[198:199]
	global_store_dwordx4 v[166:167], v[170:173], off offset:576
	v_add_u32_e32 v166, 0xffffffa0, v162
	v_ashrrev_i32_e32 v167, 31, v166
	v_lshlrev_b64 v[166:167], 13, v[166:167]
	v_add_u32_e32 v162, 0xffffffb0, v162
	v_lshl_add_u64 v[166:167], v[164:165], 0, v[166:167]
	v_ashrrev_i32_e32 v163, 31, v162
	global_load_dwordx4 v[170:173], v[166:167], off
	global_load_dwordx4 v[174:177], v[166:167], off offset:64
	global_load_dwordx4 v[178:181], v[166:167], off offset:512
	global_load_dwordx4 v[182:185], v[166:167], off offset:576
	v_lshlrev_b64 v[162:163], 13, v[162:163]
	v_lshl_add_u64 v[166:167], v[164:165], 0, v[162:163]
	global_load_dwordx4 v[162:165], v[166:167], off
	global_load_dwordx4 v[186:189], v[166:167], off offset:64
	global_load_dwordx4 v[190:193], v[166:167], off offset:512
	global_load_dwordx4 v[194:197], v[166:167], off offset:576
	v_add_co_u32_e32 v198, vcc, s1, v160
	v_lshl_add_u64 v[166:167], v[160:161], 0, s[38:39]
	s_nop 0
	v_addc_co_u32_e32 v199, vcc, 0, v161, vcc
	s_mov_b64 s[38:39], 0x160000
	s_mov_b32 s1, 0x160000
	s_waitcnt vmcnt(0)
	v_pk_fma_f32 v[172:173], v[44:45], v[146:147], v[172:173]
	v_pk_fma_f32 v[170:171], v[42:43], v[144:145], v[170:171]
	global_store_dwordx4 v[198:199], v[170:173], off
	v_pk_fma_f32 v[146:147], v[28:29], v[146:147], v[164:165]
	v_pk_fma_f32 v[144:145], v[26:27], v[144:145], v[162:163]
	v_pk_fma_f32 v[172:173], v[36:37], v[142:143], v[176:177]
	v_pk_fma_f32 v[170:171], v[34:35], v[140:141], v[174:175]
	global_store_dwordx4 v[166:167], v[170:173], off offset:64
	v_pk_fma_f32 v[142:143], v[20:21], v[142:143], v[188:189]
	v_pk_fma_f32 v[140:141], v[18:19], v[140:141], v[186:187]
	v_pk_fma_f32 v[172:173], v[16:17], v[138:139], v[180:181]
	v_pk_fma_f32 v[170:171], v[14:15], v[136:137], v[178:179]
	global_store_dwordx4 v[166:167], v[170:173], off offset:512
	v_pk_fma_f32 v[138:139], v[8:9], v[138:139], v[192:193]
	v_pk_fma_f32 v[136:137], v[6:7], v[136:137], v[190:191]
	v_pk_fma_f32 v[172:173], v[12:13], v[134:135], v[184:185]
	v_pk_fma_f32 v[170:171], v[10:11], v[132:133], v[182:183]
	global_store_dwordx4 v[166:167], v[170:173], off offset:576
	v_lshl_add_u64 v[166:167], v[160:161], 0, s[38:39]
	v_add_co_u32_e32 v160, vcc, s1, v160
	v_pk_fma_f32 v[134:135], v[4:5], v[134:135], v[196:197]
	s_nop 0
	v_addc_co_u32_e32 v161, vcc, 0, v161, vcc
	v_pk_fma_f32 v[132:133], v[2:3], v[132:133], v[194:195]
	global_store_dwordx4 v[160:161], v[144:147], off
	global_store_dwordx4 v[166:167], v[140:143], off offset:64
	global_store_dwordx4 v[166:167], v[136:139], off offset:512
	global_store_dwordx4 v[166:167], v[132:135], off offset:576
	s_mov_b64 s[38:39], 0

.LBB0_1870:
	s_add_u32 s36, s26, 0x100
	s_addc_u32 s37, s27, 0
	s_add_u32 s40, s31, s26
	s_addc_u32 s41, s20, s27
	s_cmpk_eq_i32 s26, 0x700
	s_cselect_b64 vcc, -1, 0
	s_and_b64 s[38:39], vcc, exec
	s_cselect_b32 s48, 0, s36
	s_cselect_b32 s45, 0, s37
	s_cselect_b32 s38, s24, s40
	s_cselect_b32 s39, s25, s41
	s_add_u32 s40, s94, s48
	s_addc_u32 s41, s95, s45
	s_add_i32 s45, 0, 0x10000
	v_add_u32_e32 v98, s45, v165
	ds_read_b128 v[148:151], v98
	ds_read_b128 v[154:157], v98 offset:1024
	ds_read_b128 v[176:179], v98 offset:2048
	ds_read_b128 v[182:185], v98 offset:3072
	v_lshl_add_u64 v[170:171], v[144:145], 0, s[26:27]
	s_add_i32 m0, s35, 0xc000
	ds_read_b128 v[186:189], v169
	ds_read_b128 v[190:193], v169 offset:1024
	ds_read_b128 v[194:197], v169 offset:2048
	ds_read_b128 v[198:201], v169 offset:3072
	ds_read_b128 v[202:205], v169 offset:4096
	ds_read_b128 v[206:209], v169 offset:5120
	ds_read_b128 v[210:213], v169 offset:6144
	ds_read_b128 v[214:217], v169 offset:7168
	global_load_lds_dwordx4 v[170:171], off
	v_lshl_add_u64 v[170:171], v[146:147], 0, s[26:27]
	s_add_i32 m0, s35, 0xe000
	s_nop 0
	global_load_lds_dwordx4 v[170:171], off
	s_waitcnt lgkmcnt(8)
	s_barrier
	v_add_u32_e32 v250, 0x14000, v165
	ds_read_b128 v[222:225], v250
	ds_read_b128 v[230:233], v250 offset:1024
	ds_read_b128 v[236:239], v250 offset:2048
	ds_read_b128 v[240:243], v250 offset:3072
	s_waitcnt lgkmcnt(4)
	s_waitcnt lgkmcnt(4)
	v_mfma_i32_16x16x64_i8 v[128:131], v[148:151], v[186:189], v[128:131]
	v_mfma_i32_16x16x64_i8 v[120:123], v[176:179], v[186:189], v[120:123]
	v_mfma_i32_16x16x64_i8 v[112:115], v[148:151], v[194:197], v[112:115]
	v_mfma_i32_16x16x64_i8 v[108:111], v[176:179], v[194:197], v[108:111]
	v_mfma_i32_16x16x64_i8 v[94:97], v[148:151], v[202:205], v[94:97]
	v_mfma_i32_16x16x64_i8 v[90:93], v[176:179], v[202:205], v[90:93]
	v_mfma_i32_16x16x64_i8 v[78:81], v[148:151], v[210:213], v[78:81]
	v_mfma_i32_16x16x64_i8 v[74:77], v[176:179], v[210:213], v[74:77]
	v_mfma_i32_16x16x64_i8 v[128:131], v[154:157], v[190:193], v[128:131]
	v_mfma_i32_16x16x64_i8 v[120:123], v[182:185], v[190:193], v[120:123]
	v_mfma_i32_16x16x64_i8 v[112:115], v[154:157], v[198:201], v[112:115]
	v_mfma_i32_16x16x64_i8 v[108:111], v[182:185], v[198:201], v[108:111]
	v_mfma_i32_16x16x64_i8 v[94:97], v[154:157], v[206:209], v[94:97]
	v_mfma_i32_16x16x64_i8 v[90:93], v[182:185], v[206:209], v[90:93]
	v_mfma_i32_16x16x64_i8 v[78:81], v[154:157], v[214:217], v[78:81]
	v_mfma_i32_16x16x64_i8 v[74:77], v[182:185], v[214:217], v[74:77]
	s_barrier
	s_add_i32 s48, 0, 0x14000
	s_add_i32 s26, s45, s93
	v_add_u32_e32 v98, s48, v165
	v_lshl_add_u64 v[170:171], s[38:39], 0, v[132:133]
	s_mov_b32 m0, s26
	global_load_lds_dwordx4 v[170:171], off
	v_lshl_add_u64 v[218:219], s[38:39], 0, v[134:135]
	s_add_i32 m0, s26, 0x2000
	s_nop 0
	global_load_lds_dwordx4 v[218:219], off
	s_barrier
	s_waitcnt lgkmcnt(0)
	s_waitcnt lgkmcnt(0)
	v_mfma_i32_16x16x64_i8 v[124:127], v[222:225], v[186:189], v[124:127]
	v_mfma_i32_16x16x64_i8 v[116:119], v[236:239], v[186:189], v[116:119]
	v_mfma_i32_16x16x64_i8 v[104:107], v[222:225], v[194:197], v[104:107]
	v_mfma_i32_16x16x64_i8 v[100:103], v[236:239], v[194:197], v[100:103]
	v_mfma_i32_16x16x64_i8 v[86:89], v[222:225], v[202:205], v[86:89]
	v_mfma_i32_16x16x64_i8 v[82:85], v[236:239], v[202:205], v[82:85]
	v_mfma_i32_16x16x64_i8 v[70:73], v[222:225], v[210:213], v[70:73]
	v_mfma_i32_16x16x64_i8 v[66:69], v[236:239], v[210:213], v[66:69]
	v_mfma_i32_16x16x64_i8 v[124:127], v[230:233], v[190:193], v[124:127]
	v_mfma_i32_16x16x64_i8 v[116:119], v[240:243], v[190:193], v[116:119]
	v_mfma_i32_16x16x64_i8 v[104:107], v[230:233], v[198:201], v[104:107]
	v_mfma_i32_16x16x64_i8 v[100:103], v[240:243], v[198:201], v[100:103]
	v_mfma_i32_16x16x64_i8 v[86:89], v[230:233], v[206:209], v[86:89]
	v_mfma_i32_16x16x64_i8 v[82:85], v[240:243], v[206:209], v[82:85]
	v_mfma_i32_16x16x64_i8 v[70:73], v[230:233], v[214:217], v[70:73]
	v_mfma_i32_16x16x64_i8 v[66:69], v[240:243], v[214:217], v[66:69]
	s_mov_b32 m0, s35
	v_cndmask_b32_e32 v98, v136, v173, vcc
	s_barrier
	ds_read_b128 v[186:189], v169 offset:16384
	ds_read_b128 v[190:193], v169 offset:17408
	ds_read_b128 v[194:197], v169 offset:18432
	ds_read_b128 v[198:201], v169 offset:19456
	ds_read_b128 v[202:205], v169 offset:20480
	ds_read_b128 v[206:209], v169 offset:21504
	ds_read_b128 v[210:213], v169 offset:22528
	ds_read_b128 v[214:217], v169 offset:23552
	v_lshl_add_u64 v[244:245], s[40:41], 0, v[98:99]
	global_load_lds_dwordx4 v98, s[40:41]
	v_cndmask_b32_e32 v98, v138, v174, vcc
	s_mov_b32 m0, s18
	v_lshl_add_u64 v[246:247], s[40:41], 0, v[98:99]
	global_load_lds_dwordx4 v98, s[40:41]
	s_barrier
	s_waitcnt lgkmcnt(0)
	s_waitcnt lgkmcnt(0)
	v_mfma_i32_16x16x64_i8 v[62:65], v[148:151], v[186:189], v[62:65]
	v_mfma_i32_16x16x64_i8 v[58:61], v[176:179], v[186:189], v[58:61]
	v_mfma_i32_16x16x64_i8 v[46:49], v[148:151], v[194:197], v[46:49]
	v_mfma_i32_16x16x64_i8 v[42:45], v[176:179], v[194:197], v[42:45]
	v_mfma_i32_16x16x64_i8 v[30:33], v[148:151], v[202:205], v[30:33]
	v_mfma_i32_16x16x64_i8 v[26:29], v[176:179], v[202:205], v[26:29]
	v_mfma_i32_16x16x64_i8 v[14:17], v[148:151], v[210:213], v[14:17]
	v_mfma_i32_16x16x64_i8 v[10:13], v[176:179], v[210:213], v[10:13]
	v_mfma_i32_16x16x64_i8 v[62:65], v[154:157], v[190:193], v[62:65]
	v_mfma_i32_16x16x64_i8 v[58:61], v[182:185], v[190:193], v[58:61]
	v_mfma_i32_16x16x64_i8 v[46:49], v[154:157], v[198:201], v[46:49]
	v_mfma_i32_16x16x64_i8 v[42:45], v[182:185], v[198:201], v[42:45]
	v_mfma_i32_16x16x64_i8 v[30:33], v[154:157], v[206:209], v[30:33]
	v_mfma_i32_16x16x64_i8 v[26:29], v[182:185], v[206:209], v[26:29]
	v_mfma_i32_16x16x64_i8 v[14:17], v[154:157], v[214:217], v[14:17]
	v_mfma_i32_16x16x64_i8 v[10:13], v[182:185], v[214:217], v[10:13]
	s_barrier
	s_add_u32 s26, s38, 0x40000
	s_addc_u32 s27, s39, 0
	s_add_i32 s45, s48, s93
	v_lshl_add_u64 v[148:149], s[26:27], 0, v[132:133]
	s_mov_b32 m0, s45
	s_nop 0
	global_load_lds_dwordx4 v[148:149], off
	v_lshl_add_u64 v[148:149], s[26:27], 0, v[134:135]
	s_add_i32 m0, s45, 0x2000
	s_nop 0
	global_load_lds_dwordx4 v[148:149], off
	s_waitcnt vmcnt(6)
	s_barrier
	v_mfma_i32_16x16x64_i8 v[54:57], v[222:225], v[186:189], v[54:57]
	v_mfma_i32_16x16x64_i8 v[50:53], v[236:239], v[186:189], v[50:53]
	v_mfma_i32_16x16x64_i8 v[38:41], v[222:225], v[194:197], v[38:41]
	v_mfma_i32_16x16x64_i8 v[34:37], v[236:239], v[194:197], v[34:37]
	v_mfma_i32_16x16x64_i8 v[22:25], v[222:225], v[202:205], v[22:25]
	v_mfma_i32_16x16x64_i8 v[18:21], v[236:239], v[202:205], v[18:21]
	v_mfma_i32_16x16x64_i8 v[6:9], v[222:225], v[210:213], v[6:9]
	v_mfma_i32_16x16x64_i8 v[2:5], v[236:239], v[210:213], v[2:5]
	v_mfma_i32_16x16x64_i8 v[54:57], v[230:233], v[190:193], v[54:57]
	v_mfma_i32_16x16x64_i8 v[50:53], v[240:243], v[190:193], v[50:53]
	v_mfma_i32_16x16x64_i8 v[38:41], v[230:233], v[198:201], v[38:41]
	v_mfma_i32_16x16x64_i8 v[34:37], v[240:243], v[198:201], v[34:37]
	v_mfma_i32_16x16x64_i8 v[22:25], v[230:233], v[206:209], v[22:25]
	v_mfma_i32_16x16x64_i8 v[18:21], v[240:243], v[206:209], v[18:21]
	v_mfma_i32_16x16x64_i8 v[6:9], v[230:233], v[214:217], v[6:9]
	v_mfma_i32_16x16x64_i8 v[2:5], v[240:243], v[214:217], v[2:5]
	s_add_i32 s26, 0, 0x18000
	v_add_u32_e32 v98, s26, v165
	s_barrier
	ds_read_b128 v[148:151], v98
	ds_read_b128 v[154:157], v98 offset:1024
	ds_read_b128 v[176:179], v98 offset:2048
	ds_read_b128 v[182:185], v98 offset:3072
	s_mov_b32 m0, s19
	v_cndmask_b32_e32 v98, v140, v175, vcc
	ds_read_b128 v[186:189], v169 offset:32768
	ds_read_b128 v[190:193], v169 offset:33792
	ds_read_b128 v[194:197], v169 offset:34816
	ds_read_b128 v[198:201], v169 offset:35840
	ds_read_b128 v[202:205], v169 offset:36864
	ds_read_b128 v[206:209], v169 offset:37888
	ds_read_b128 v[210:213], v169 offset:38912
	ds_read_b128 v[214:217], v169 offset:39936
	global_load_lds_dwordx4 v98, s[40:41]
	v_cndmask_b32_e32 v98, v142, v180, vcc
	s_mov_b32 m0, s92
	s_nop 0
	global_load_lds_dwordx4 v98, s[40:41]
	s_waitcnt lgkmcnt(8)
	s_barrier
	v_add_u32_e32 v250, 0x1c000, v165
	ds_read_b128 v[222:225], v250
	ds_read_b128 v[230:233], v250 offset:1024
	ds_read_b128 v[236:239], v250 offset:2048
	ds_read_b128 v[240:243], v250 offset:3072
	s_waitcnt lgkmcnt(4)
	s_waitcnt lgkmcnt(4)
	v_mfma_i32_16x16x64_i8 v[128:131], v[148:151], v[186:189], v[128:131]
	v_mfma_i32_16x16x64_i8 v[120:123], v[176:179], v[186:189], v[120:123]
	v_mfma_i32_16x16x64_i8 v[112:115], v[148:151], v[194:197], v[112:115]
	v_mfma_i32_16x16x64_i8 v[108:111], v[176:179], v[194:197], v[108:111]
	v_mfma_i32_16x16x64_i8 v[94:97], v[148:151], v[202:205], v[94:97]
	v_mfma_i32_16x16x64_i8 v[90:93], v[176:179], v[202:205], v[90:93]
	v_mfma_i32_16x16x64_i8 v[78:81], v[148:151], v[210:213], v[78:81]
	v_mfma_i32_16x16x64_i8 v[74:77], v[176:179], v[210:213], v[74:77]
	v_mfma_i32_16x16x64_i8 v[128:131], v[154:157], v[190:193], v[128:131]
	v_mfma_i32_16x16x64_i8 v[120:123], v[182:185], v[190:193], v[120:123]
	v_mfma_i32_16x16x64_i8 v[112:115], v[154:157], v[198:201], v[112:115]
	v_mfma_i32_16x16x64_i8 v[108:111], v[182:185], v[198:201], v[108:111]
	v_mfma_i32_16x16x64_i8 v[94:97], v[154:157], v[206:209], v[94:97]
	v_mfma_i32_16x16x64_i8 v[90:93], v[182:185], v[206:209], v[90:93]
	v_mfma_i32_16x16x64_i8 v[78:81], v[154:157], v[214:217], v[78:81]
	v_mfma_i32_16x16x64_i8 v[74:77], v[182:185], v[214:217], v[74:77]
	s_barrier
	s_add_i32 s40, 0, 0x1c000
	s_add_i32 s26, s26, s93
	v_add_u32_e32 v98, s40, v165
	v_lshl_add_u64 v[170:171], v[170:171], 0, s[68:69]
	s_mov_b32 m0, s26
	global_load_lds_dwordx4 v[170:171], off
	v_lshl_add_u64 v[170:171], v[218:219], 0, s[68:69]
	s_add_i32 m0, s26, 0x2000
	s_nop 0
	global_load_lds_dwordx4 v[170:171], off
	s_barrier
	s_waitcnt lgkmcnt(0)
	s_waitcnt lgkmcnt(0)
	v_mfma_i32_16x16x64_i8 v[124:127], v[222:225], v[186:189], v[124:127]
	v_mfma_i32_16x16x64_i8 v[116:119], v[236:239], v[186:189], v[116:119]
	v_mfma_i32_16x16x64_i8 v[104:107], v[222:225], v[194:197], v[104:107]
	v_mfma_i32_16x16x64_i8 v[100:103], v[236:239], v[194:197], v[100:103]
	v_mfma_i32_16x16x64_i8 v[86:89], v[222:225], v[202:205], v[86:89]
	v_mfma_i32_16x16x64_i8 v[82:85], v[236:239], v[202:205], v[82:85]
	v_mfma_i32_16x16x64_i8 v[70:73], v[222:225], v[210:213], v[70:73]
	v_mfma_i32_16x16x64_i8 v[66:69], v[236:239], v[210:213], v[66:69]
	v_mfma_i32_16x16x64_i8 v[124:127], v[230:233], v[190:193], v[124:127]
	v_mfma_i32_16x16x64_i8 v[116:119], v[240:243], v[190:193], v[116:119]
	v_mfma_i32_16x16x64_i8 v[104:107], v[230:233], v[198:201], v[104:107]
	v_mfma_i32_16x16x64_i8 v[100:103], v[240:243], v[198:201], v[100:103]
	v_mfma_i32_16x16x64_i8 v[86:89], v[230:233], v[206:209], v[86:89]
	v_mfma_i32_16x16x64_i8 v[82:85], v[240:243], v[206:209], v[82:85]
	v_mfma_i32_16x16x64_i8 v[70:73], v[230:233], v[214:217], v[70:73]
	v_mfma_i32_16x16x64_i8 v[66:69], v[240:243], v[214:217], v[66:69]
	s_mov_b32 m0, s3
	v_lshl_add_u64 v[170:171], v[244:245], 0, s[68:69]
	s_barrier
	ds_read_b128 v[186:189], v169 offset:49152
	ds_read_b128 v[190:193], v169 offset:50176
	ds_read_b128 v[194:197], v169 offset:51200
	ds_read_b128 v[198:201], v169 offset:52224
	ds_read_b128 v[202:205], v169 offset:53248
	ds_read_b128 v[206:209], v169 offset:54272
	ds_read_b128 v[210:213], v169 offset:55296
	ds_read_b128 v[214:217], v169 offset:56320
	global_load_lds_dwordx4 v[170:171], off
	v_lshl_add_u64 v[170:171], v[246:247], 0, s[68:69]
	s_mov_b32 m0, s74
	s_nop 0
	global_load_lds_dwordx4 v[170:171], off
	s_barrier
	s_waitcnt lgkmcnt(0)
	s_waitcnt lgkmcnt(0)
	v_mfma_i32_16x16x64_i8 v[62:65], v[148:151], v[186:189], v[62:65]
	v_mfma_i32_16x16x64_i8 v[58:61], v[176:179], v[186:189], v[58:61]
	v_mfma_i32_16x16x64_i8 v[46:49], v[148:151], v[194:197], v[46:49]
	v_mfma_i32_16x16x64_i8 v[42:45], v[176:179], v[194:197], v[42:45]
	v_mfma_i32_16x16x64_i8 v[30:33], v[148:151], v[202:205], v[30:33]
	v_mfma_i32_16x16x64_i8 v[26:29], v[176:179], v[202:205], v[26:29]
	v_mfma_i32_16x16x64_i8 v[14:17], v[148:151], v[210:213], v[14:17]
	v_mfma_i32_16x16x64_i8 v[10:13], v[176:179], v[210:213], v[10:13]
	v_mfma_i32_16x16x64_i8 v[62:65], v[154:157], v[190:193], v[62:65]
	v_mfma_i32_16x16x64_i8 v[58:61], v[182:185], v[190:193], v[58:61]
	v_mfma_i32_16x16x64_i8 v[46:49], v[154:157], v[198:201], v[46:49]
	v_mfma_i32_16x16x64_i8 v[42:45], v[182:185], v[198:201], v[42:45]
	v_mfma_i32_16x16x64_i8 v[30:33], v[154:157], v[206:209], v[30:33]
	v_mfma_i32_16x16x64_i8 v[26:29], v[182:185], v[206:209], v[26:29]
	v_mfma_i32_16x16x64_i8 v[14:17], v[154:157], v[214:217], v[14:17]
	v_mfma_i32_16x16x64_i8 v[10:13], v[182:185], v[214:217], v[10:13]
	s_barrier
	s_add_u32 s26, s38, 0x40080
	s_addc_u32 s27, s39, 0
	s_add_i32 s38, s40, s93
	v_lshl_add_u64 v[148:149], s[26:27], 0, v[132:133]
	s_mov_b32 m0, s38
	s_nop 0
	global_load_lds_dwordx4 v[148:149], off
	v_lshl_add_u64 v[148:149], s[26:27], 0, v[134:135]
	s_add_i32 m0, s38, 0x2000
	s_nop 0
	global_load_lds_dwordx4 v[148:149], off
	s_waitcnt vmcnt(6)
	s_barrier
	v_mfma_i32_16x16x64_i8 v[54:57], v[222:225], v[186:189], v[54:57]
	v_mfma_i32_16x16x64_i8 v[50:53], v[236:239], v[186:189], v[50:53]
	v_mfma_i32_16x16x64_i8 v[38:41], v[222:225], v[194:197], v[38:41]
	v_mfma_i32_16x16x64_i8 v[34:37], v[236:239], v[194:197], v[34:37]
	v_mfma_i32_16x16x64_i8 v[22:25], v[222:225], v[202:205], v[22:25]
	v_mfma_i32_16x16x64_i8 v[18:21], v[236:239], v[202:205], v[18:21]
	v_mfma_i32_16x16x64_i8 v[6:9], v[222:225], v[210:213], v[6:9]
	v_mfma_i32_16x16x64_i8 v[2:5], v[236:239], v[210:213], v[2:5]
	v_mfma_i32_16x16x64_i8 v[54:57], v[230:233], v[190:193], v[54:57]
	v_mfma_i32_16x16x64_i8 v[50:53], v[240:243], v[190:193], v[50:53]
	v_mfma_i32_16x16x64_i8 v[38:41], v[230:233], v[198:201], v[38:41]
	v_mfma_i32_16x16x64_i8 v[34:37], v[240:243], v[198:201], v[34:37]
	v_mfma_i32_16x16x64_i8 v[22:25], v[230:233], v[206:209], v[22:25]
	v_mfma_i32_16x16x64_i8 v[18:21], v[240:243], v[206:209], v[18:21]
	v_mfma_i32_16x16x64_i8 v[6:9], v[230:233], v[214:217], v[6:9]
	v_mfma_i32_16x16x64_i8 v[2:5], v[240:243], v[214:217], v[2:5]
	s_add_i32 s42, s42, 2
	s_cmp_gt_u32 s42, 13
	s_mov_b64 s[26:27], s[36:37]
	s_barrier
	s_cbranch_scc0 .LBB0_1870
	v_lshl_add_u32 v136, s71, 8, v163
	v_readlane_b32 s26, v253, 52
	v_ashrrev_i32_e32 v137, 31, v136
	v_readlane_b32 s27, v253, 53
	s_mul_hi_i32 s20, s9, 0xb000
	s_mul_i32 s9, s9, 0xb000
	v_lshl_add_u64 v[138:139], v[136:137], 2, s[26:27]
	v_readlane_b32 s26, v254, 15
	s_add_u32 s9, s26, s9
	v_readlane_b32 s26, v254, 16
	s_addc_u32 s20, s26, s20
	s_lshl_b32 s26, s34, 8
	s_ashr_i32 s27, s26, 31
	s_lshl_b64 s[26:27], s[26:27], 2
	s_add_u32 s9, s9, s26
	s_addc_u32 s20, s20, s27
	s_add_u32 s26, s9, s85
	s_addc_u32 s27, s20, 0
	global_load_dword v168, v[138:139], off
	global_load_dword v166, v[138:139], off offset:64
	global_load_dword v164, v[138:139], off offset:128
	global_load_dword v162, v[138:139], off offset:192
	global_load_dword v160, v[138:139], off offset:512
	global_load_dword v158, v[138:139], off offset:576
	global_load_dword v152, v[138:139], off offset:640
	global_load_dword v98, v[138:139], off offset:704
	global_load_dwordx4 v[176:179], v172, s[26:27] offset:16
	global_load_dwordx4 v[140:143], v172, s[26:27]
	global_load_dwordx4 v[182:185], v172, s[26:27] offset:528
	global_load_dwordx4 v[144:147], v172, s[26:27] offset:512
	v_cvt_f32_i32_e32 v129, v129
	v_cvt_f32_i32_e32 v121, v121
	v_readlane_b32 s26, v254, 13
	v_readlane_b32 s27, v254, 14
	v_lshl_or_b32 v138, s34, 7, v167
	s_movk_i32 s9, 0x2c00
	v_mov_b64_e32 v[170:171], s[26:27]
	v_ashrrev_i32_e32 v139, 31, v138
	v_mad_i64_i32 v[170:171], s[26:27], v136, s9, v[170:171]
	s_waitcnt vmcnt(0)
	v_mov_b32_e32 v149, v140
	v_mov_b32_e32 v140, v145
	v_pk_mul_f32 v[154:155], v[140:141], s[58:59] op_sel_hi:[1,0]
	v_mov_b32_e32 v140, v146
	v_mov_b32_e32 v141, v142
	v_pk_mul_f32 v[150:151], v[140:141], s[58:59] op_sel_hi:[1,0]
	v_mov_b32_e32 v141, v176
	v_mov_b32_e32 v176, v183
	v_mov_b32_e32 v148, v144
	v_pk_mul_f32 v[144:145], v[176:177], s[58:59] op_sel_hi:[1,0]
	v_cvt_f32_i32_e32 v177, v128
	v_cvt_f32_i32_e32 v176, v124
	v_mov_b32_e32 v140, v182
	v_pk_mul_f32 v[156:157], v[148:149], s[58:59] op_sel_hi:[1,0]
	v_mov_b32_e32 v142, v147
	v_pk_mul_f32 v[146:147], v[140:141], s[58:59] op_sel_hi:[1,0]
	v_mov_b32_e32 v140, v184
	v_mov_b32_e32 v141, v178
	v_mov_b32_e32 v178, v185
	v_pk_mul_f32 v[148:149], v[142:143], s[58:59] op_sel_hi:[1,0]
	v_pk_mul_f32 v[142:143], v[140:141], s[58:59] op_sel_hi:[1,0]
	v_pk_mul_f32 v[140:141], v[178:179], s[58:59] op_sel_hi:[1,0]
	v_pk_mul_f32 v[178:179], v[168:169], v[156:157] op_sel_hi:[0,1]
	v_pk_mul_f32 v[176:177], v[178:179], v[176:177]
	v_cvt_f32_i32_e32 v128, v125
	v_mul_f32_e32 v124, 0xbfb8aa3b, v177
	v_exp_f32_e32 v124, v124
	s_nop 0
	v_add_f32_e32 v124, 1.0, v124
	v_rcp_f32_e32 v124, v124
	s_nop 0
	v_mul_f32_e32 v124, v177, v124
	v_mul_f32_e32 v124, v176, v124
	v_pk_mul_f32 v[176:177], v[168:169], v[154:155] op_sel_hi:[0,1]
	v_pk_mul_f32 v[128:129], v[176:177], v[128:129]
	v_pk_mul_f32 v[176:177], v[168:169], v[150:151] op_sel_hi:[0,1]
	v_mul_f32_e32 v125, 0xbfb8aa3b, v129
	v_exp_f32_e32 v125, v125
	s_nop 0
	v_add_f32_e32 v125, 1.0, v125
	v_rcp_f32_e32 v125, v125
	s_nop 0
	v_mul_f32_e32 v125, v129, v125
	v_mul_f32_e32 v125, v128, v125
	v_cvt_f32_i32_e32 v129, v130
	v_cvt_f32_i32_e32 v128, v126
	v_pk_mul_f32 v[128:129], v[176:177], v[128:129]
	s_nop 0
	v_mul_f32_e32 v126, 0xbfb8aa3b, v129
	v_exp_f32_e32 v126, v126
	s_nop 0
	v_add_f32_e32 v126, 1.0, v126
	v_rcp_f32_e32 v126, v126
	s_nop 0
	v_mul_f32_e32 v126, v129, v126
	v_mul_f32_e32 v126, v128, v126
	v_cvt_f32_i32_e32 v129, v131
	v_cvt_f32_i32_e32 v128, v127
	v_pk_mul_f32 v[130:131], v[168:169], v[148:149] op_sel_hi:[0,1]
	v_pk_mul_f32 v[128:129], v[130:131], v[128:129]
	s_nop 0
	v_mul_f32_e32 v127, 0xbfb8aa3b, v129
	v_exp_f32_e32 v127, v127
	v_pk_mul_f32 v[130:131], v[168:169], v[146:147] op_sel_hi:[0,1]
	v_add_f32_e32 v127, 1.0, v127
	v_rcp_f32_e32 v127, v127
	s_nop 0
	v_mul_f32_e32 v127, v129, v127
	v_mul_f32_e32 v127, v128, v127
	v_cvt_f32_i32_e32 v129, v120
	v_cvt_f32_i32_e32 v128, v116
	v_cvt_f32_i32_e32 v120, v117
	v_pk_mul_f32 v[128:129], v[130:131], v[128:129]
	s_nop 0
	v_mul_f32_e32 v116, 0xbfb8aa3b, v129
	v_exp_f32_e32 v116, v116
	s_nop 0
	v_add_f32_e32 v116, 1.0, v116
	v_rcp_f32_e32 v116, v116
	s_nop 0
	v_mul_f32_e32 v116, v129, v116
	v_mul_f32_e32 v128, v128, v116
	v_pk_mul_f32 v[116:117], v[168:169], v[144:145] op_sel_hi:[0,1]
	v_pk_mul_f32 v[116:117], v[116:117], v[120:121]
	s_nop 0
	v_mul_f32_e32 v120, 0xbfb8aa3b, v117
	v_exp_f32_e32 v120, v120
	s_nop 0
	v_add_f32_e32 v120, 1.0, v120
	v_rcp_f32_e32 v120, v120
	s_nop 0
	v_mul_f32_e32 v117, v117, v120
	v_mul_f32_e32 v129, v116, v117
	v_cvt_f32_i32_e32 v117, v122
	v_cvt_f32_i32_e32 v116, v118
	v_pk_mul_f32 v[120:121], v[168:169], v[142:143] op_sel_hi:[0,1]
	v_pk_mul_f32 v[116:117], v[120:121], v[116:117]
	s_nop 0
	v_mul_f32_e32 v118, 0xbfb8aa3b, v117
	v_exp_f32_e32 v118, v118
	v_lshl_add_u64 v[120:121], v[138:139], 1, v[170:171]
	v_add_f32_e32 v118, 1.0, v118
	v_rcp_f32_e32 v118, v118
	s_nop 0
	v_mul_f32_e32 v117, v117, v118
	v_mul_f32_e32 v122, v116, v117
	v_cvt_f32_i32_e32 v117, v123
	v_cvt_f32_i32_e32 v116, v119
	v_pk_mul_f32 v[118:119], v[168:169], v[140:141] op_sel_hi:[0,1]
	v_pk_mul_f32 v[116:117], v[118:119], v[116:117]
	s_nop 0
	v_mul_f32_e32 v118, 0xbfb8aa3b, v117
	v_exp_f32_e32 v118, v118
	s_nop 0
	v_add_f32_e32 v118, 1.0, v118
	v_rcp_f32_e32 v118, v118
	s_nop 0
	v_mul_f32_e32 v117, v117, v118
	v_mul_f32_e32 v123, v116, v117
	v_cvt_pk_bf16_f32 v116, v124, v125
	v_cvt_pk_bf16_f32 v117, v126, v127
	v_cvt_pk_bf16_f32 v118, v128, v129
	v_cvt_pk_bf16_f32 v119, v122, v123
	global_store_dwordx4 v[120:121], v[116:119], off
	s_nop 1
	v_max_f32_e64 v118, |v122|, |v123|
	v_max_f32_e64 v116, |v124|, |v125|
	v_max_f32_e64 v117, |v126|, |v127|
	v_max3_f32 v118, |v128|, |v129|, v118
	v_max3_f32 v116, v116, v117, v118
	v_mov_b32_e32 v117, v0
	s_nop 0
	v_lshlrev_b32_e32 v117, 2, v117
	v_bitop3_b32 v118, v117, 64, v220 bitop3:0x6c
	ds_bpermute_b32 v118, v118, v116
	v_bitop3_b32 v117, v117, s59, v220 bitop3:0x6c
	s_waitcnt lgkmcnt(0)
	v_max_f32_e32 v118, v118, v118
	v_max_f32_e32 v116, v116, v118
	ds_bpermute_b32 v117, v117, v116
	s_and_saveexec_b64 s[26:27], s[0:1]
	s_cbranch_execz .LBB0_1873
	v_readlane_b32 s36, v253, 57
	s_waitcnt lgkmcnt(0)
	v_max_f32_e32 v117, v117, v117
	v_max_f32_e32 v116, v116, v116
	v_readlane_b32 s37, v253, 58
	v_max_f32_e32 v118, v116, v117
	s_nop 0
	v_lshl_add_u64 v[116:117], v[136:137], 2, s[36:37]
	global_atomic_umax v[116:117], v118, off

.LBB0_2010:
	s_add_u32 s34, s30, 0x100
	s_addc_u32 s35, s31, 0
	s_add_i32 vcc_hi, 0, 0x10000
	v_add_u32_e32 v146, vcc_hi, v147
	ds_read_b128 v[132:135], v146
	ds_read_b128 v[150:153], v146 offset:1024
	ds_read_b128 v[154:157], v146 offset:2048
	ds_read_b128 v[158:161], v146 offset:3072
	s_cmp_eq_u32 vcc_lo, 40
	s_cselect_b32 s39, s23, s35
	s_cselect_b32 s38, s22, s34
	s_cselect_b32 s37, s25, s93
	s_cselect_b32 s36, s24, s71
	v_lshl_add_u64 v[196:197], s[30:31], 0, v[142:143]
	s_add_i32 m0, s8, 0xc000
	ds_read_b128 v[164:167], v163
	ds_read_b128 v[168:171], v163 offset:1024
	ds_read_b128 v[172:175], v163 offset:2048
	ds_read_b128 v[176:179], v163 offset:3072
	ds_read_b128 v[180:183], v163 offset:4096
	ds_read_b128 v[184:187], v163 offset:5120
	ds_read_b128 v[188:191], v163 offset:6144
	ds_read_b128 v[192:195], v163 offset:7168
	global_load_lds_dwordx4 v[196:197], off
	v_lshl_add_u64 v[196:197], s[30:31], 0, v[144:145]
	s_add_i32 m0, s8, 0xe000
	s_nop 0
	global_load_lds_dwordx4 v[196:197], off
	s_waitcnt lgkmcnt(8)
	s_barrier
	v_add_u32_e32 v250, 0x14000, v147
	ds_read_b128 v[196:199], v250
	ds_read_b128 v[200:203], v250 offset:1024
	ds_read_b128 v[204:207], v250 offset:2048
	ds_read_b128 v[208:211], v250 offset:3072
	s_waitcnt lgkmcnt(4)
	s_waitcnt lgkmcnt(4)
	v_mfma_i32_16x16x64_i8 v[128:131], v[132:135], v[164:167], v[128:131]
	v_mfma_i32_16x16x64_i8 v[124:127], v[154:157], v[164:167], v[124:127]
	v_mfma_i32_16x16x64_i8 v[120:123], v[132:135], v[172:175], v[120:123]
	v_mfma_i32_16x16x64_i8 v[116:119], v[154:157], v[172:175], v[116:119]
	v_mfma_i32_16x16x64_i8 v[112:115], v[132:135], v[180:183], v[112:115]
	v_mfma_i32_16x16x64_i8 v[108:111], v[154:157], v[180:183], v[108:111]
	v_mfma_i32_16x16x64_i8 v[104:107], v[132:135], v[188:191], v[104:107]
	v_mfma_i32_16x16x64_i8 v[100:103], v[154:157], v[188:191], v[100:103]
	v_mfma_i32_16x16x64_i8 v[128:131], v[150:153], v[168:171], v[128:131]
	v_mfma_i32_16x16x64_i8 v[124:127], v[158:161], v[168:171], v[124:127]
	v_mfma_i32_16x16x64_i8 v[120:123], v[150:153], v[176:179], v[120:123]
	v_mfma_i32_16x16x64_i8 v[116:119], v[158:161], v[176:179], v[116:119]
	v_mfma_i32_16x16x64_i8 v[112:115], v[150:153], v[184:187], v[112:115]
	v_mfma_i32_16x16x64_i8 v[108:111], v[158:161], v[184:187], v[108:111]
	v_mfma_i32_16x16x64_i8 v[104:107], v[150:153], v[192:195], v[104:107]
	v_mfma_i32_16x16x64_i8 v[100:103], v[158:161], v[192:195], v[100:103]
	s_barrier
	s_add_i32 s3, 0, 0x14000
	s_add_i32 s30, vcc_hi, s62
	v_add_u32_e32 v146, s3, v147
	v_lshl_add_u64 v[212:213], s[36:37], 0, v[98:99]
	s_mov_b32 m0, s30
	global_load_lds_dwordx4 v[212:213], off
	v_lshl_add_u64 v[214:215], s[36:37], 0, v[136:137]
	s_add_i32 m0, s30, 0x2000
	s_nop 0
	global_load_lds_dwordx4 v[214:215], off
	s_barrier
	s_waitcnt lgkmcnt(0)
	s_waitcnt lgkmcnt(0)
	v_mfma_i32_16x16x64_i8 v[94:97], v[196:199], v[164:167], v[94:97]
	v_mfma_i32_16x16x64_i8 v[90:93], v[204:207], v[164:167], v[90:93]
	v_mfma_i32_16x16x64_i8 v[86:89], v[196:199], v[172:175], v[86:89]
	v_mfma_i32_16x16x64_i8 v[82:85], v[204:207], v[172:175], v[82:85]
	v_mfma_i32_16x16x64_i8 v[78:81], v[196:199], v[180:183], v[78:81]
	v_mfma_i32_16x16x64_i8 v[74:77], v[204:207], v[180:183], v[74:77]
	v_mfma_i32_16x16x64_i8 v[70:73], v[196:199], v[188:191], v[70:73]
	v_mfma_i32_16x16x64_i8 v[66:69], v[204:207], v[188:191], v[66:69]
	v_mfma_i32_16x16x64_i8 v[94:97], v[200:203], v[168:171], v[94:97]
	v_mfma_i32_16x16x64_i8 v[90:93], v[208:211], v[168:171], v[90:93]
	v_mfma_i32_16x16x64_i8 v[86:89], v[200:203], v[176:179], v[86:89]
	v_mfma_i32_16x16x64_i8 v[82:85], v[208:211], v[176:179], v[82:85]
	v_mfma_i32_16x16x64_i8 v[78:81], v[200:203], v[184:187], v[78:81]
	v_mfma_i32_16x16x64_i8 v[74:77], v[208:211], v[184:187], v[74:77]
	v_mfma_i32_16x16x64_i8 v[70:73], v[200:203], v[192:195], v[70:73]
	v_mfma_i32_16x16x64_i8 v[66:69], v[208:211], v[192:195], v[66:69]
	s_mov_b32 m0, s8
	v_lshl_add_u64 v[216:217], s[38:39], 0, v[140:141]
	s_barrier
	ds_read_b128 v[164:167], v163 offset:16384
	ds_read_b128 v[168:171], v163 offset:17408
	ds_read_b128 v[172:175], v163 offset:18432
	ds_read_b128 v[176:179], v163 offset:19456
	ds_read_b128 v[180:183], v163 offset:20480
	ds_read_b128 v[184:187], v163 offset:21504
	ds_read_b128 v[188:191], v163 offset:22528
	ds_read_b128 v[192:195], v163 offset:23552
	global_load_lds_dwordx4 v[216:217], off
	v_lshl_add_u64 v[218:219], s[38:39], 0, v[138:139]
	s_mov_b32 m0, s64
	s_nop 0
	global_load_lds_dwordx4 v[218:219], off
	s_barrier
	s_waitcnt lgkmcnt(0)
	s_waitcnt lgkmcnt(0)
	v_mfma_i32_16x16x64_i8 v[62:65], v[132:135], v[164:167], v[62:65]
	v_mfma_i32_16x16x64_i8 v[58:61], v[154:157], v[164:167], v[58:61]
	v_mfma_i32_16x16x64_i8 v[54:57], v[132:135], v[172:175], v[54:57]
	v_mfma_i32_16x16x64_i8 v[50:53], v[154:157], v[172:175], v[50:53]
	v_mfma_i32_16x16x64_i8 v[46:49], v[132:135], v[180:183], v[46:49]
	v_mfma_i32_16x16x64_i8 v[42:45], v[154:157], v[180:183], v[42:45]
	v_mfma_i32_16x16x64_i8 v[38:41], v[132:135], v[188:191], v[38:41]
	v_mfma_i32_16x16x64_i8 v[34:37], v[154:157], v[188:191], v[34:37]
	v_mfma_i32_16x16x64_i8 v[62:65], v[150:153], v[168:171], v[62:65]
	v_mfma_i32_16x16x64_i8 v[58:61], v[158:161], v[168:171], v[58:61]
	v_mfma_i32_16x16x64_i8 v[54:57], v[150:153], v[176:179], v[54:57]
	v_mfma_i32_16x16x64_i8 v[50:53], v[158:161], v[176:179], v[50:53]
	v_mfma_i32_16x16x64_i8 v[46:49], v[150:153], v[184:187], v[46:49]
	v_mfma_i32_16x16x64_i8 v[42:45], v[158:161], v[184:187], v[42:45]
	v_mfma_i32_16x16x64_i8 v[38:41], v[150:153], v[192:195], v[38:41]
	v_mfma_i32_16x16x64_i8 v[34:37], v[158:161], v[192:195], v[34:37]
	s_barrier
	s_add_u32 s30, s36, 0xb0000
	s_addc_u32 s31, s37, 0
	s_add_i32 s3, s3, s62
	v_lshl_add_u64 v[132:133], s[30:31], 0, v[98:99]
	s_mov_b32 m0, s3
	s_nop 0
	global_load_lds_dwordx4 v[132:133], off
	v_lshl_add_u64 v[132:133], s[30:31], 0, v[136:137]
	s_add_i32 m0, s3, 0x2000
	s_nop 0
	global_load_lds_dwordx4 v[132:133], off
	s_waitcnt vmcnt(6)
	s_barrier
	v_mfma_i32_16x16x64_i8 v[30:33], v[196:199], v[164:167], v[30:33]
	v_mfma_i32_16x16x64_i8 v[26:29], v[204:207], v[164:167], v[26:29]
	v_mfma_i32_16x16x64_i8 v[22:25], v[196:199], v[172:175], v[22:25]
	v_mfma_i32_16x16x64_i8 v[18:21], v[204:207], v[172:175], v[18:21]
	v_mfma_i32_16x16x64_i8 v[14:17], v[196:199], v[180:183], v[14:17]
	v_mfma_i32_16x16x64_i8 v[10:13], v[204:207], v[180:183], v[10:13]
	v_mfma_i32_16x16x64_i8 v[6:9], v[196:199], v[188:191], v[6:9]
	v_mfma_i32_16x16x64_i8 v[2:5], v[204:207], v[188:191], v[2:5]
	v_mfma_i32_16x16x64_i8 v[30:33], v[200:203], v[168:171], v[30:33]
	v_mfma_i32_16x16x64_i8 v[26:29], v[208:211], v[168:171], v[26:29]
	v_mfma_i32_16x16x64_i8 v[22:25], v[200:203], v[176:179], v[22:25]
	v_mfma_i32_16x16x64_i8 v[18:21], v[208:211], v[176:179], v[18:21]
	v_mfma_i32_16x16x64_i8 v[14:17], v[200:203], v[184:187], v[14:17]
	v_mfma_i32_16x16x64_i8 v[10:13], v[208:211], v[184:187], v[10:13]
	v_mfma_i32_16x16x64_i8 v[6:9], v[200:203], v[192:195], v[6:9]
	v_mfma_i32_16x16x64_i8 v[2:5], v[208:211], v[192:195], v[2:5]
	s_add_i32 s3, 0, 0x18000
	v_add_u32_e32 v146, s3, v147
	s_barrier
	ds_read_b128 v[132:135], v146
	ds_read_b128 v[150:153], v146 offset:1024
	ds_read_b128 v[154:157], v146 offset:2048
	ds_read_b128 v[158:161], v146 offset:3072
	s_add_u32 s30, s38, 0xb0000
	s_addc_u32 s31, s39, 0
	s_mov_b32 m0, s65
	v_lshl_add_u64 v[196:197], s[30:31], 0, v[140:141]
	ds_read_b128 v[164:167], v163 offset:32768
	ds_read_b128 v[168:171], v163 offset:33792
	ds_read_b128 v[172:175], v163 offset:34816
	ds_read_b128 v[176:179], v163 offset:35840
	ds_read_b128 v[180:183], v163 offset:36864
	ds_read_b128 v[184:187], v163 offset:37888
	ds_read_b128 v[188:191], v163 offset:38912
	ds_read_b128 v[192:195], v163 offset:39936
	global_load_lds_dwordx4 v[196:197], off
	v_lshl_add_u64 v[196:197], s[30:31], 0, v[138:139]
	s_mov_b32 m0, s66
	s_nop 0
	global_load_lds_dwordx4 v[196:197], off
	s_waitcnt lgkmcnt(8)
	s_barrier
	v_add_u32_e32 v250, 0x1c000, v147
	ds_read_b128 v[196:199], v250
	ds_read_b128 v[200:203], v250 offset:1024
	ds_read_b128 v[204:207], v250 offset:2048
	ds_read_b128 v[208:211], v250 offset:3072
	s_waitcnt lgkmcnt(4)
	s_waitcnt lgkmcnt(4)
	v_mfma_i32_16x16x64_i8 v[128:131], v[132:135], v[164:167], v[128:131]
	v_mfma_i32_16x16x64_i8 v[124:127], v[154:157], v[164:167], v[124:127]
	v_mfma_i32_16x16x64_i8 v[120:123], v[132:135], v[172:175], v[120:123]
	v_mfma_i32_16x16x64_i8 v[116:119], v[154:157], v[172:175], v[116:119]
	v_mfma_i32_16x16x64_i8 v[112:115], v[132:135], v[180:183], v[112:115]
	v_mfma_i32_16x16x64_i8 v[108:111], v[154:157], v[180:183], v[108:111]
	v_mfma_i32_16x16x64_i8 v[104:107], v[132:135], v[188:191], v[104:107]
	v_mfma_i32_16x16x64_i8 v[100:103], v[154:157], v[188:191], v[100:103]
	v_mfma_i32_16x16x64_i8 v[128:131], v[150:153], v[168:171], v[128:131]
	v_mfma_i32_16x16x64_i8 v[124:127], v[158:161], v[168:171], v[124:127]
	v_mfma_i32_16x16x64_i8 v[120:123], v[150:153], v[176:179], v[120:123]
	v_mfma_i32_16x16x64_i8 v[116:119], v[158:161], v[176:179], v[116:119]
	v_mfma_i32_16x16x64_i8 v[112:115], v[150:153], v[184:187], v[112:115]
	v_mfma_i32_16x16x64_i8 v[108:111], v[158:161], v[184:187], v[108:111]
	v_mfma_i32_16x16x64_i8 v[104:107], v[150:153], v[192:195], v[104:107]
	v_mfma_i32_16x16x64_i8 v[100:103], v[158:161], v[192:195], v[100:103]
	s_barrier
	s_add_i32 s38, 0, 0x1c000
	s_add_i32 s3, s3, s62
	v_add_u32_e32 v146, s38, v147
	v_lshl_add_u64 v[212:213], v[212:213], 0, s[68:69]
	s_mov_b32 m0, s3
	global_load_lds_dwordx4 v[212:213], off
	v_lshl_add_u64 v[212:213], v[214:215], 0, s[68:69]
	s_add_i32 m0, s3, 0x2000
	s_nop 0
	global_load_lds_dwordx4 v[212:213], off
	s_barrier
	s_waitcnt lgkmcnt(0)
	s_waitcnt lgkmcnt(0)
	v_mfma_i32_16x16x64_i8 v[94:97], v[196:199], v[164:167], v[94:97]
	v_mfma_i32_16x16x64_i8 v[90:93], v[204:207], v[164:167], v[90:93]
	v_mfma_i32_16x16x64_i8 v[86:89], v[196:199], v[172:175], v[86:89]
	v_mfma_i32_16x16x64_i8 v[82:85], v[204:207], v[172:175], v[82:85]
	v_mfma_i32_16x16x64_i8 v[78:81], v[196:199], v[180:183], v[78:81]
	v_mfma_i32_16x16x64_i8 v[74:77], v[204:207], v[180:183], v[74:77]
	v_mfma_i32_16x16x64_i8 v[70:73], v[196:199], v[188:191], v[70:73]
	v_mfma_i32_16x16x64_i8 v[66:69], v[204:207], v[188:191], v[66:69]
	v_mfma_i32_16x16x64_i8 v[94:97], v[200:203], v[168:171], v[94:97]
	v_mfma_i32_16x16x64_i8 v[90:93], v[208:211], v[168:171], v[90:93]
	v_mfma_i32_16x16x64_i8 v[86:89], v[200:203], v[176:179], v[86:89]
	v_mfma_i32_16x16x64_i8 v[82:85], v[208:211], v[176:179], v[82:85]
	v_mfma_i32_16x16x64_i8 v[78:81], v[200:203], v[184:187], v[78:81]
	v_mfma_i32_16x16x64_i8 v[74:77], v[208:211], v[184:187], v[74:77]
	v_mfma_i32_16x16x64_i8 v[70:73], v[200:203], v[192:195], v[70:73]
	v_mfma_i32_16x16x64_i8 v[66:69], v[208:211], v[192:195], v[66:69]
	s_mov_b32 m0, s67
	v_lshl_add_u64 v[212:213], v[216:217], 0, s[68:69]
	s_barrier
	ds_read_b128 v[164:167], v163 offset:49152
	ds_read_b128 v[168:171], v163 offset:50176
	ds_read_b128 v[172:175], v163 offset:51200
	ds_read_b128 v[176:179], v163 offset:52224
	ds_read_b128 v[180:183], v163 offset:53248
	ds_read_b128 v[184:187], v163 offset:54272
	ds_read_b128 v[188:191], v163 offset:55296
	ds_read_b128 v[192:195], v163 offset:56320
	global_load_lds_dwordx4 v[212:213], off
	v_lshl_add_u64 v[212:213], v[218:219], 0, s[68:69]
	s_mov_b32 m0, s74
	s_nop 0
	global_load_lds_dwordx4 v[212:213], off
	s_barrier
	s_waitcnt lgkmcnt(0)
	s_waitcnt lgkmcnt(0)
	v_mfma_i32_16x16x64_i8 v[62:65], v[132:135], v[164:167], v[62:65]
	v_mfma_i32_16x16x64_i8 v[58:61], v[154:157], v[164:167], v[58:61]
	v_mfma_i32_16x16x64_i8 v[54:57], v[132:135], v[172:175], v[54:57]
	v_mfma_i32_16x16x64_i8 v[50:53], v[154:157], v[172:175], v[50:53]
	v_mfma_i32_16x16x64_i8 v[46:49], v[132:135], v[180:183], v[46:49]
	v_mfma_i32_16x16x64_i8 v[42:45], v[154:157], v[180:183], v[42:45]
	v_mfma_i32_16x16x64_i8 v[38:41], v[132:135], v[188:191], v[38:41]
	v_mfma_i32_16x16x64_i8 v[34:37], v[154:157], v[188:191], v[34:37]
	v_mfma_i32_16x16x64_i8 v[62:65], v[150:153], v[168:171], v[62:65]
	v_mfma_i32_16x16x64_i8 v[58:61], v[158:161], v[168:171], v[58:61]
	v_mfma_i32_16x16x64_i8 v[54:57], v[150:153], v[176:179], v[54:57]
	v_mfma_i32_16x16x64_i8 v[50:53], v[158:161], v[176:179], v[50:53]
	v_mfma_i32_16x16x64_i8 v[46:49], v[150:153], v[184:187], v[46:49]
	v_mfma_i32_16x16x64_i8 v[42:45], v[158:161], v[184:187], v[42:45]
	v_mfma_i32_16x16x64_i8 v[38:41], v[150:153], v[192:195], v[38:41]
	v_mfma_i32_16x16x64_i8 v[34:37], v[158:161], v[192:195], v[34:37]
	s_barrier
	s_add_u32 s30, s36, 0xb0080
	s_addc_u32 s31, s37, 0
	s_add_i32 s3, s38, s62
	v_lshl_add_u64 v[132:133], s[30:31], 0, v[98:99]
	s_mov_b32 m0, s3
	s_nop 0
	global_load_lds_dwordx4 v[132:133], off
	v_lshl_add_u64 v[132:133], s[30:31], 0, v[136:137]
	s_add_i32 m0, s3, 0x2000
	s_nop 0
	global_load_lds_dwordx4 v[132:133], off
	s_waitcnt vmcnt(6)
	s_barrier
	v_mfma_i32_16x16x64_i8 v[30:33], v[196:199], v[164:167], v[30:33]
	v_mfma_i32_16x16x64_i8 v[26:29], v[204:207], v[164:167], v[26:29]
	v_mfma_i32_16x16x64_i8 v[22:25], v[196:199], v[172:175], v[22:25]
	v_mfma_i32_16x16x64_i8 v[18:21], v[204:207], v[172:175], v[18:21]
	v_mfma_i32_16x16x64_i8 v[14:17], v[196:199], v[180:183], v[14:17]
	v_mfma_i32_16x16x64_i8 v[10:13], v[204:207], v[180:183], v[10:13]
	v_mfma_i32_16x16x64_i8 v[6:9], v[196:199], v[188:191], v[6:9]
	v_mfma_i32_16x16x64_i8 v[2:5], v[204:207], v[188:191], v[2:5]
	v_mfma_i32_16x16x64_i8 v[30:33], v[200:203], v[168:171], v[30:33]
	v_mfma_i32_16x16x64_i8 v[26:29], v[208:211], v[168:171], v[26:29]
	v_mfma_i32_16x16x64_i8 v[22:25], v[200:203], v[176:179], v[22:25]
	v_mfma_i32_16x16x64_i8 v[18:21], v[208:211], v[176:179], v[18:21]
	v_mfma_i32_16x16x64_i8 v[14:17], v[200:203], v[184:187], v[14:17]
	v_mfma_i32_16x16x64_i8 v[10:13], v[208:211], v[184:187], v[10:13]
	v_mfma_i32_16x16x64_i8 v[6:9], v[200:203], v[192:195], v[6:9]
	v_mfma_i32_16x16x64_i8 v[2:5], v[208:211], v[192:195], v[2:5]
	s_add_i32 vcc_lo, vcc_lo, 2
	s_add_u32 s71, s71, 0x100
	s_addc_u32 s93, s93, 0
	s_cmp_gt_u32 vcc_lo, 41
	s_mov_b64 s[30:31], s[34:35]
	s_barrier
	s_cbranch_scc0 .LBB0_2010
	v_lshl_add_u32 v208, s70, 8, v1
	v_readlane_b32 s30, v253, 57
	v_or_b32_e32 v204, 16, v208
	v_lshl_or_b32 v210, s29, 8, v149
	s_ashr_i32 s29, s28, 31
	v_ashrrev_i32_e32 v209, 31, v208
	v_readlane_b32 s31, v253, 58
	v_ashrrev_i32_e32 v205, 31, v204
	v_or_b32_e32 v200, 32, v208
	s_lshl_b64 s[28:29], s[28:29], 13
	v_readlane_b32 s3, v254, 21
	v_lshl_add_u64 v[132:133], v[208:209], 2, s[30:31]
	v_lshl_add_u64 v[134:135], v[204:205], 2, s[30:31]
	v_ashrrev_i32_e32 v201, 31, v200
	v_or_b32_e32 v188, 48, v208
	s_add_u32 s28, s3, s28
	v_readlane_b32 s3, v254, 22
	global_load_dword v206, v[132:133], off
	global_load_dword v202, v[134:135], off
	v_lshl_add_u64 v[134:135], v[200:201], 2, s[30:31]
	v_ashrrev_i32_e32 v189, 31, v188
	v_ashrrev_i32_e32 v211, 31, v210
	s_addc_u32 s29, s3, s29
	global_load_dword v190, v[134:135], off
	v_lshl_add_u64 v[134:135], v[188:189], 2, s[30:31]
	v_lshl_add_u64 v[212:213], v[210:211], 2, s[28:29]
	global_load_dword v174, v[134:135], off
	global_load_dword v168, v[132:133], off offset:512
	global_load_dword v162, v[132:133], off offset:576
	global_load_dword v148, v[132:133], off offset:640
	global_load_dword v146, v[132:133], off offset:704
	s_nop 0
	global_load_dwordx4 v[132:135], v[212:213], off offset:16
	global_load_dwordx4 v[150:153], v[212:213], off
	v_cvt_f32_i32_e32 v155, v9
	v_cvt_f32_i32_e32 v154, v8
	v_cvt_f32_i32_e32 v161, v7
	v_cvt_f32_i32_e32 v160, v6
	v_cvt_f32_i32_e32 v195, v27
	v_cvt_f32_i32_e32 v194, v26
	v_cvt_f32_i32_e32 v197, v33
	v_cvt_f32_i32_e32 v196, v32
	v_cvt_f32_i32_e32 v27, v53
	v_cvt_f32_i32_e32 v26, v52
	v_cvt_f32_i32_e32 v33, v55
	v_cvt_f32_i32_e32 v32, v54
	v_cvt_f32_i32_e32 v53, v101
	v_cvt_f32_i32_e32 v52, v100
	v_cvt_f32_i32_e32 v55, v107
	v_cvt_f32_i32_e32 v54, v106
	v_cvt_f32_i32_e32 v101, v127
	v_cvt_f32_i32_e32 v100, v126
	v_cvt_f32_i32_e32 v107, v129
	v_cvt_f32_i32_e32 v106, v128
	v_cvt_f32_i32_e32 v167, v11
	v_cvt_f32_i32_e32 v166, v10
	v_cvt_f32_i32_e32 v171, v17
	v_cvt_f32_i32_e32 v170, v16
	v_cvt_f32_i32_e32 v193, v29
	v_cvt_f32_i32_e32 v192, v28
	v_cvt_f32_i32_e32 v11, v37
	v_cvt_f32_i32_e32 v10, v36
	v_cvt_f32_i32_e32 v17, v39
	v_cvt_f32_i32_e32 v16, v38
	v_cvt_f32_i32_e32 v29, v51
	v_cvt_f32_i32_e32 v28, v50
	v_cvt_f32_i32_e32 v37, v59
	v_cvt_f32_i32_e32 v36, v58
	v_cvt_f32_i32_e32 v39, v65
	v_cvt_f32_i32_e32 v38, v64
	v_cvt_f32_i32_e32 v65, v79
	v_cvt_f32_i32_e32 v64, v78
	v_cvt_f32_i32_e32 v79, v89
	v_cvt_f32_i32_e32 v78, v88
	v_cvt_f32_i32_e32 v89, v93
	v_cvt_f32_i32_e32 v88, v92
	v_cvt_f32_i32_e32 v95, v95
	v_cvt_f32_i32_e32 v94, v94
	v_cvt_f32_i32_e32 v51, v103
	v_cvt_f32_i32_e32 v50, v102
	v_cvt_f32_i32_e32 v59, v105
	v_cvt_f32_i32_e32 v58, v104
	v_cvt_f32_i32_e32 v103, v125
	v_cvt_f32_i32_e32 v102, v124
	v_cvt_f32_i32_e32 v105, v131
	v_cvt_f32_i32_e32 v104, v130
	v_cvt_f32_i32_e32 v93, v91
	v_cvt_f32_i32_e32 v92, v90
	v_cvt_f32_i32_e32 v97, v97
	v_cvt_f32_i32_e32 v96, v96
	v_cvt_f32_i32_e32 v199, v31
	v_cvt_f32_i32_e32 v198, v30
	v_cvt_f32_i32_e32 v31, v57
	v_cvt_f32_i32_e32 v30, v56
	v_cvt_f32_i32_e32 v57, v77
	v_cvt_f32_i32_e32 v56, v76
	v_cvt_f32_i32_e32 v77, v83
	v_cvt_f32_i32_e32 v76, v82
	v_cvt_f32_i32_e32 v83, v119
	v_cvt_f32_i32_e32 v82, v118
	v_cvt_f32_i32_e32 v91, v121
	v_cvt_f32_i32_e32 v90, v120
	v_readlane_b32 s28, v252, 15
	v_cvt_f32_i32_e32 v173, v15
	v_cvt_f32_i32_e32 v172, v14
	v_cvt_f32_i32_e32 v181, v21
	v_cvt_f32_i32_e32 v180, v20
	v_cvt_f32_i32_e32 v183, v19
	v_cvt_f32_i32_e32 v182, v18
	v_cvt_f32_i32_e32 v185, v25
	v_cvt_f32_i32_e32 v184, v24
	v_cvt_f32_i32_e32 v15, v41
	v_cvt_f32_i32_e32 v14, v40
	s_waitcnt vmcnt(0)
	v_pk_mul_f32 v[156:157], v[152:153], s[58:59] op_sel_hi:[1,0]
	v_pk_mul_f32 v[158:159], v[150:151], s[58:59] op_sel_hi:[1,0]
	v_cvt_f32_i32_e32 v151, v5
	v_cvt_f32_i32_e32 v150, v4
	v_cvt_f32_i32_e32 v153, v3
	v_cvt_f32_i32_e32 v152, v2
	global_load_dwordx4 v[2:5], v[212:213], off offset:512
	global_load_dwordx4 v[6:9], v[212:213], off offset:528
	v_cvt_f32_i32_e32 v19, v45
	v_cvt_f32_i32_e32 v18, v44
	v_cvt_f32_i32_e32 v21, v43
	v_cvt_f32_i32_e32 v20, v42
	v_cvt_f32_i32_e32 v25, v47
	v_cvt_f32_i32_e32 v24, v46
	v_cvt_f32_i32_e32 v41, v63
	v_cvt_f32_i32_e32 v40, v62
	v_cvt_f32_i32_e32 v43, v69
	v_cvt_f32_i32_e32 v42, v68
	v_cvt_f32_i32_e32 v45, v67
	v_cvt_f32_i32_e32 v44, v66
	v_cvt_f32_i32_e32 v47, v73
	v_cvt_f32_i32_e32 v46, v72
	v_cvt_f32_i32_e32 v63, v81
	v_cvt_f32_i32_e32 v62, v80
	v_cvt_f32_i32_e32 v73, v85
	v_cvt_f32_i32_e32 v72, v84
	v_cvt_f32_i32_e32 v81, v87
	v_cvt_f32_i32_e32 v80, v86
	v_cvt_f32_i32_e32 v67, v111
	v_cvt_f32_i32_e32 v66, v110
	v_cvt_f32_i32_e32 v69, v109
	v_cvt_f32_i32_e32 v68, v108
	v_cvt_f32_i32_e32 v85, v117
	v_cvt_f32_i32_e32 v84, v116
	v_cvt_f32_i32_e32 v87, v123
	v_cvt_f32_i32_e32 v86, v122
	v_pk_mul_f32 v[110:111], v[134:135], s[58:59] op_sel_hi:[1,0]
	v_lshlrev_b64 v[108:109], 12, v[208:209]
	v_readlane_b32 s29, v252, 16
	v_pk_mul_f32 v[106:107], v[206:207], v[106:107] op_sel_hi:[0,1]
	v_pk_mul_f32 v[100:101], v[206:207], v[100:101] op_sel_hi:[0,1]
	v_cvt_f32_i32_e32 v165, v13
	v_cvt_f32_i32_e32 v164, v12
	v_cvt_f32_i32_e32 v187, v23
	v_cvt_f32_i32_e32 v186, v22
	v_cvt_f32_i32_e32 v13, v35
	v_cvt_f32_i32_e32 v12, v34
	v_cvt_f32_i32_e32 v23, v49
	v_cvt_f32_i32_e32 v22, v48
	v_cvt_f32_i32_e32 v35, v61
	v_cvt_f32_i32_e32 v34, v60
	v_cvt_f32_i32_e32 v49, v71
	v_cvt_f32_i32_e32 v48, v70
	v_cvt_f32_i32_e32 v61, v75
	v_cvt_f32_i32_e32 v60, v74
	v_cvt_f32_i32_e32 v71, v115
	v_cvt_f32_i32_e32 v70, v114
	v_cvt_f32_i32_e32 v75, v113
	v_cvt_f32_i32_e32 v74, v112
	v_pk_mul_f32 v[112:113], v[132:133], s[58:59] op_sel_hi:[1,0]
	v_lshl_add_u64 v[108:109], s[28:29], 0, v[108:109]
	v_lshlrev_b64 v[114:115], 1, v[210:211]
	v_pk_mul_f32 v[104:105], v[206:207], v[104:105] op_sel_hi:[0,1]
	v_pk_mul_f32 v[102:103], v[206:207], v[102:103] op_sel_hi:[0,1]
	v_pk_mul_f32 v[116:117], v[110:111], v[100:101]
	v_pk_mul_f32 v[100:101], v[158:159], v[106:107]
	v_pk_mul_f32 v[94:95], v[206:207], v[94:95] op_sel_hi:[0,1]
	v_pk_mul_f32 v[88:89], v[206:207], v[88:89] op_sel_hi:[0,1]
	v_lshl_add_u64 v[108:109], v[108:109], 0, v[114:115]
	v_pk_mul_f32 v[102:103], v[112:113], v[102:103]
	v_pk_mul_f32 v[104:105], v[156:157], v[104:105]
	v_cvt_pk_bf16_f32 v100, v100, v101
	v_pk_mul_f32 v[96:97], v[206:207], v[96:97] op_sel_hi:[0,1]
	v_cvt_pk_bf16_f32 v101, v104, v105
	v_pk_mul_f32 v[92:93], v[206:207], v[92:93] op_sel_hi:[0,1]
	v_cvt_pk_bf16_f32 v102, v102, v103
	v_cvt_pk_bf16_f32 v103, v116, v117
	global_store_dwordx4 v[108:109], v[100:103], off
	v_pk_mul_f32 v[90:91], v[202:203], v[90:91] op_sel_hi:[0,1]
	v_pk_mul_f32 v[82:83], v[202:203], v[82:83] op_sel_hi:[0,1]
	v_pk_mul_f32 v[86:87], v[202:203], v[86:87] op_sel_hi:[0,1]
	v_pk_mul_f32 v[84:85], v[202:203], v[84:85] op_sel_hi:[0,1]
	v_pk_mul_f32 v[78:79], v[202:203], v[78:79] op_sel_hi:[0,1]
	v_pk_mul_f32 v[72:73], v[202:203], v[72:73] op_sel_hi:[0,1]
	v_pk_mul_f32 v[84:85], v[112:113], v[84:85]
	v_pk_mul_f32 v[86:87], v[156:157], v[86:87]
	s_waitcnt vmcnt(0)
	v_pk_mul_f32 v[2:3], v[2:3], s[58:59] op_sel_hi:[1,0]
	v_pk_mul_f32 v[8:9], v[8:9], s[58:59] op_sel_hi:[1,0]
	v_pk_mul_f32 v[6:7], v[6:7], s[58:59] op_sel_hi:[1,0]
	v_pk_mul_f32 v[4:5], v[4:5], s[58:59] op_sel_hi:[1,0]
	v_pk_mul_f32 v[94:95], v[2:3], v[94:95]
	v_pk_mul_f32 v[88:89], v[8:9], v[88:89]
	v_pk_mul_f32 v[96:97], v[4:5], v[96:97]
	v_pk_mul_f32 v[100:101], v[6:7], v[92:93]
	v_cvt_pk_bf16_f32 v92, v94, v95
	v_cvt_pk_bf16_f32 v93, v96, v97
	v_pk_mul_f32 v[80:81], v[202:203], v[80:81] op_sel_hi:[0,1]
	v_cvt_pk_bf16_f32 v94, v100, v101
	v_cvt_pk_bf16_f32 v95, v88, v89
	v_lshlrev_b64 v[88:89], 12, v[204:205]
	global_store_dwordx4 v[108:109], v[92:95], off offset:256
	v_lshl_add_u64 v[88:89], s[28:29], 0, v[88:89]
	v_lshl_add_u64 v[88:89], v[88:89], 0, v[114:115]
	v_pk_mul_f32 v[92:93], v[110:111], v[82:83]
	v_pk_mul_f32 v[82:83], v[158:159], v[90:91]
	v_pk_mul_f32 v[76:77], v[202:203], v[76:77] op_sel_hi:[0,1]
	v_cvt_pk_bf16_f32 v82, v82, v83
	v_cvt_pk_bf16_f32 v83, v86, v87
	v_pk_mul_f32 v[78:79], v[4:5], v[78:79]
	v_pk_mul_f32 v[72:73], v[8:9], v[72:73]
	v_cvt_pk_bf16_f32 v84, v84, v85
	v_cvt_pk_bf16_f32 v85, v92, v93
	global_store_dwordx4 v[88:89], v[82:85], off
	v_pk_mul_f32 v[80:81], v[2:3], v[80:81]
	v_pk_mul_f32 v[74:75], v[190:191], v[74:75] op_sel_hi:[0,1]
	v_pk_mul_f32 v[82:83], v[6:7], v[76:77]
	v_cvt_pk_bf16_f32 v76, v80, v81
	v_cvt_pk_bf16_f32 v77, v78, v79
	v_pk_mul_f32 v[66:67], v[190:191], v[66:67] op_sel_hi:[0,1]
	v_cvt_pk_bf16_f32 v78, v82, v83
	v_cvt_pk_bf16_f32 v79, v72, v73
	v_lshlrev_b64 v[72:73], 12, v[200:201]
	global_store_dwordx4 v[88:89], v[76:79], off offset:256
	v_lshl_add_u64 v[72:73], s[28:29], 0, v[72:73]
	v_pk_mul_f32 v[70:71], v[190:191], v[70:71] op_sel_hi:[0,1]
	v_pk_mul_f32 v[68:69], v[190:191], v[68:69] op_sel_hi:[0,1]
	v_pk_mul_f32 v[76:77], v[110:111], v[66:67]
	v_pk_mul_f32 v[66:67], v[158:159], v[74:75]
	v_pk_mul_f32 v[62:63], v[190:191], v[62:63] op_sel_hi:[0,1]
	v_pk_mul_f32 v[56:57], v[190:191], v[56:57] op_sel_hi:[0,1]
	v_lshl_add_u64 v[72:73], v[72:73], 0, v[114:115]
	v_pk_mul_f32 v[68:69], v[112:113], v[68:69]
	v_pk_mul_f32 v[70:71], v[156:157], v[70:71]
	v_cvt_pk_bf16_f32 v66, v66, v67
	v_pk_mul_f32 v[64:65], v[190:191], v[64:65] op_sel_hi:[0,1]
	v_cvt_pk_bf16_f32 v67, v70, v71
	v_pk_mul_f32 v[60:61], v[190:191], v[60:61] op_sel_hi:[0,1]
	v_pk_mul_f32 v[62:63], v[4:5], v[62:63]
	v_pk_mul_f32 v[56:57], v[8:9], v[56:57]
	v_cvt_pk_bf16_f32 v68, v68, v69
	v_cvt_pk_bf16_f32 v69, v76, v77
	global_store_dwordx4 v[72:73], v[66:69], off
	v_pk_mul_f32 v[64:65], v[2:3], v[64:65]
	v_pk_mul_f32 v[58:59], v[174:175], v[58:59] op_sel_hi:[0,1]
	v_pk_mul_f32 v[66:67], v[6:7], v[60:61]
	v_cvt_pk_bf16_f32 v60, v64, v65
	v_cvt_pk_bf16_f32 v61, v62, v63
	v_pk_mul_f32 v[50:51], v[174:175], v[50:51] op_sel_hi:[0,1]
	v_cvt_pk_bf16_f32 v62, v66, v67
	v_cvt_pk_bf16_f32 v63, v56, v57
	v_lshlrev_b64 v[56:57], 12, v[188:189]
	global_store_dwordx4 v[72:73], v[60:63], off offset:256
	v_lshl_add_u64 v[56:57], s[28:29], 0, v[56:57]
	v_pk_mul_f32 v[54:55], v[174:175], v[54:55] op_sel_hi:[0,1]
	v_pk_mul_f32 v[52:53], v[174:175], v[52:53] op_sel_hi:[0,1]
	v_pk_mul_f32 v[60:61], v[110:111], v[50:51]
	v_pk_mul_f32 v[50:51], v[158:159], v[58:59]
	v_pk_mul_f32 v[44:45], v[174:175], v[44:45] op_sel_hi:[0,1]
	v_lshl_add_u64 v[56:57], v[56:57], 0, v[114:115]
	v_pk_mul_f32 v[52:53], v[112:113], v[52:53]
	v_pk_mul_f32 v[54:55], v[156:157], v[54:55]
	v_cvt_pk_bf16_f32 v50, v50, v51
	v_pk_mul_f32 v[48:49], v[174:175], v[48:49] op_sel_hi:[0,1]
	v_cvt_pk_bf16_f32 v51, v54, v55
	v_pk_mul_f32 v[46:47], v[174:175], v[46:47] op_sel_hi:[0,1]
	v_pk_mul_f32 v[42:43], v[174:175], v[42:43] op_sel_hi:[0,1]
	v_pk_mul_f32 v[44:45], v[6:7], v[44:45]
	v_cvt_pk_bf16_f32 v52, v52, v53
	v_cvt_pk_bf16_f32 v53, v60, v61
	global_store_dwordx4 v[56:57], v[50:53], off
	v_pk_mul_f32 v[46:47], v[4:5], v[46:47]
	v_pk_mul_f32 v[48:49], v[2:3], v[48:49]
	v_pk_mul_f32 v[50:51], v[8:9], v[42:43]
	v_cvt_pk_bf16_f32 v42, v48, v49
	v_cvt_pk_bf16_f32 v43, v46, v47
	v_cvt_pk_bf16_f32 v44, v44, v45
	s_mov_b64 s[28:29], 0x80000
	v_cvt_pk_bf16_f32 v45, v50, v51
	v_pk_mul_f32 v[40:41], v[168:169], v[40:41] op_sel_hi:[0,1]
	v_pk_mul_f32 v[38:39], v[168:169], v[38:39] op_sel_hi:[0,1]
	v_pk_mul_f32 v[34:35], v[168:169], v[34:35] op_sel_hi:[0,1]
	global_store_dwordx4 v[56:57], v[42:45], off offset:256
	v_pk_mul_f32 v[36:37], v[168:169], v[36:37] op_sel_hi:[0,1]
	v_pk_mul_f32 v[38:39], v[156:157], v[38:39]
	v_lshl_add_u64 v[42:43], v[108:109], 0, s[28:29]
	v_pk_mul_f32 v[44:45], v[110:111], v[34:35]
	v_pk_mul_f32 v[34:35], v[158:159], v[40:41]
	s_mov_b32 s28, 0x80000
	v_pk_mul_f32 v[36:37], v[112:113], v[36:37]
	v_cvt_pk_bf16_f32 v34, v34, v35
	v_cvt_pk_bf16_f32 v35, v38, v39
	v_add_co_u32_e32 v38, vcc, s28, v108
	v_cvt_pk_bf16_f32 v36, v36, v37
	v_cvt_pk_bf16_f32 v37, v44, v45
	v_pk_mul_f32 v[40:41], v[168:169], v[192:193] op_sel_hi:[0,1]
	s_nop 0
	v_addc_co_u32_e32 v39, vcc, 0, v109, vcc
	global_store_dwordx4 v[38:39], v[34:37], off
	v_pk_mul_f32 v[38:39], v[168:169], v[194:195] op_sel_hi:[0,1]
	v_pk_mul_f32 v[40:41], v[8:9], v[40:41]
	v_pk_mul_f32 v[34:35], v[168:169], v[198:199] op_sel_hi:[0,1]
	v_pk_mul_f32 v[36:37], v[168:169], v[196:197] op_sel_hi:[0,1]
	v_pk_mul_f32 v[36:37], v[4:5], v[36:37]
	v_pk_mul_f32 v[34:35], v[2:3], v[34:35]
	v_pk_mul_f32 v[38:39], v[6:7], v[38:39]
	v_cvt_pk_bf16_f32 v34, v34, v35
	v_cvt_pk_bf16_f32 v35, v36, v37
	s_mov_b64 s[28:29], 0x90000
	v_cvt_pk_bf16_f32 v36, v38, v39
	v_cvt_pk_bf16_f32 v37, v40, v41
	v_pk_mul_f32 v[32:33], v[162:163], v[32:33] op_sel_hi:[0,1]
	v_pk_mul_f32 v[30:31], v[162:163], v[30:31] op_sel_hi:[0,1]
	v_pk_mul_f32 v[26:27], v[162:163], v[26:27] op_sel_hi:[0,1]
	global_store_dwordx4 v[42:43], v[34:37], off offset:256
	v_pk_mul_f32 v[28:29], v[162:163], v[28:29] op_sel_hi:[0,1]
	v_pk_mul_f32 v[30:31], v[156:157], v[30:31]
	v_lshl_add_u64 v[34:35], v[108:109], 0, s[28:29]
	v_pk_mul_f32 v[36:37], v[110:111], v[26:27]
	v_pk_mul_f32 v[26:27], v[158:159], v[32:33]
	s_mov_b32 s28, 0x90000
	v_pk_mul_f32 v[28:29], v[112:113], v[28:29]
	v_cvt_pk_bf16_f32 v26, v26, v27
	v_cvt_pk_bf16_f32 v27, v30, v31
	v_add_co_u32_e32 v30, vcc, s28, v108
	v_cvt_pk_bf16_f32 v28, v28, v29
	v_cvt_pk_bf16_f32 v29, v36, v37
	v_pk_mul_f32 v[32:33], v[162:163], v[180:181] op_sel_hi:[0,1]
	s_nop 0
	v_addc_co_u32_e32 v31, vcc, 0, v109, vcc
	global_store_dwordx4 v[30:31], v[26:29], off
	v_pk_mul_f32 v[30:31], v[162:163], v[182:183] op_sel_hi:[0,1]
	v_pk_mul_f32 v[32:33], v[8:9], v[32:33]
	v_pk_mul_f32 v[26:27], v[162:163], v[186:187] op_sel_hi:[0,1]
	v_pk_mul_f32 v[28:29], v[162:163], v[184:185] op_sel_hi:[0,1]
	v_pk_mul_f32 v[28:29], v[4:5], v[28:29]
	v_pk_mul_f32 v[26:27], v[2:3], v[26:27]
	v_pk_mul_f32 v[30:31], v[6:7], v[30:31]
	v_cvt_pk_bf16_f32 v26, v26, v27
	v_cvt_pk_bf16_f32 v27, v28, v29
	s_mov_b64 s[28:29], 0xa0000
	v_cvt_pk_bf16_f32 v28, v30, v31
	v_cvt_pk_bf16_f32 v29, v32, v33
	v_pk_mul_f32 v[24:25], v[148:149], v[24:25] op_sel_hi:[0,1]
	v_pk_mul_f32 v[22:23], v[148:149], v[22:23] op_sel_hi:[0,1]
	v_pk_mul_f32 v[18:19], v[148:149], v[18:19] op_sel_hi:[0,1]
	global_store_dwordx4 v[34:35], v[26:29], off offset:256
	v_pk_mul_f32 v[20:21], v[148:149], v[20:21] op_sel_hi:[0,1]
	v_pk_mul_f32 v[22:23], v[156:157], v[22:23]
	v_lshl_add_u64 v[26:27], v[108:109], 0, s[28:29]
	v_pk_mul_f32 v[28:29], v[110:111], v[18:19]
	v_pk_mul_f32 v[18:19], v[158:159], v[24:25]
	s_mov_b32 s28, 0xa0000
	v_pk_mul_f32 v[20:21], v[112:113], v[20:21]
	v_cvt_pk_bf16_f32 v18, v18, v19
	v_cvt_pk_bf16_f32 v19, v22, v23
	v_add_co_u32_e32 v22, vcc, s28, v108
	v_cvt_pk_bf16_f32 v20, v20, v21
	v_cvt_pk_bf16_f32 v21, v28, v29
	v_pk_mul_f32 v[24:25], v[148:149], v[164:165] op_sel_hi:[0,1]
	s_nop 0
	v_addc_co_u32_e32 v23, vcc, 0, v109, vcc
	global_store_dwordx4 v[22:23], v[18:21], off
	v_pk_mul_f32 v[22:23], v[148:149], v[166:167] op_sel_hi:[0,1]
	v_pk_mul_f32 v[24:25], v[8:9], v[24:25]
	v_pk_mul_f32 v[18:19], v[148:149], v[172:173] op_sel_hi:[0,1]
	v_pk_mul_f32 v[20:21], v[148:149], v[170:171] op_sel_hi:[0,1]
	v_pk_mul_f32 v[20:21], v[4:5], v[20:21]
	v_pk_mul_f32 v[18:19], v[2:3], v[18:19]
	v_pk_mul_f32 v[22:23], v[6:7], v[22:23]
	v_cvt_pk_bf16_f32 v18, v18, v19
	v_cvt_pk_bf16_f32 v19, v20, v21
	s_mov_b64 s[28:29], 0xb0000
	v_cvt_pk_bf16_f32 v20, v22, v23
	v_cvt_pk_bf16_f32 v21, v24, v25
	v_pk_mul_f32 v[16:17], v[146:147], v[16:17] op_sel_hi:[0,1]
	v_pk_mul_f32 v[14:15], v[146:147], v[14:15] op_sel_hi:[0,1]
	v_pk_mul_f32 v[10:11], v[146:147], v[10:11] op_sel_hi:[0,1]
	global_store_dwordx4 v[26:27], v[18:21], off offset:256
	v_pk_mul_f32 v[12:13], v[146:147], v[12:13] op_sel_hi:[0,1]
	v_pk_mul_f32 v[14:15], v[156:157], v[14:15]
	v_lshl_add_u64 v[18:19], v[108:109], 0, s[28:29]
	v_pk_mul_f32 v[20:21], v[110:111], v[10:11]
	v_pk_mul_f32 v[10:11], v[158:159], v[16:17]
	s_mov_b32 s28, 0xb0000
	v_pk_mul_f32 v[12:13], v[112:113], v[12:13]
	v_cvt_pk_bf16_f32 v10, v10, v11
	v_cvt_pk_bf16_f32 v11, v14, v15
	v_add_co_u32_e32 v14, vcc, s28, v108
	v_cvt_pk_bf16_f32 v12, v12, v13
	v_cvt_pk_bf16_f32 v13, v20, v21
	v_pk_mul_f32 v[16:17], v[146:147], v[150:151] op_sel_hi:[0,1]
	s_nop 0
	v_addc_co_u32_e32 v15, vcc, 0, v109, vcc
	global_store_dwordx4 v[14:15], v[10:13], off
	v_pk_mul_f32 v[14:15], v[146:147], v[152:153] op_sel_hi:[0,1]
	s_and_b64 vcc, exec, s[0:1]
	v_pk_mul_f32 v[10:11], v[146:147], v[160:161] op_sel_hi:[0,1]
	v_pk_mul_f32 v[12:13], v[146:147], v[154:155] op_sel_hi:[0,1]
	v_pk_mul_f32 v[4:5], v[4:5], v[12:13]
	v_pk_mul_f32 v[2:3], v[2:3], v[10:11]
	s_mov_b32 s28, s84
	s_mov_b32 s29, s85
	s_mov_b32 s70, s92
	s_mov_b64 s[34:35], s[24:25]
	s_mov_b64 s[30:31], s[22:23]
	v_pk_mul_f32 v[8:9], v[8:9], v[16:17]
	v_pk_mul_f32 v[6:7], v[6:7], v[14:15]
	v_cvt_pk_bf16_f32 v2, v2, v3
	v_cvt_pk_bf16_f32 v3, v4, v5
	s_nop 0
	v_cvt_pk_bf16_f32 v4, v6, v7
	v_cvt_pk_bf16_f32 v5, v8, v9
	global_store_dwordx4 v[18:19], v[2:5], off offset:256
	s_cbranch_vccz .LBB0_2003
	s_waitcnt vmcnt(0)
	v_readlane_b32 s0, v255, 48
	v_readlane_b32 s84, v252, 13
	v_readlane_b32 s70, v252, 21
	v_readlane_b32 s74, v255, 49
	s_cmpk_gt_u32 s0, 0xff
	v_readlane_b32 s85, v252, 14
	v_readlane_b32 s71, v252, 22
	v_readlane_b32 s75, v255, 50
	s_cbranch_scc1 .LBB0_2014
	s_barrier

.LBB0_2088:
	s_add_u32 s40, s38, 0xfffc0080
	s_addc_u32 s41, s39, -1
	s_add_i32 s46, 0, 0x10000
	v_add_u32_e32 v144, s46, v145
	ds_read_b128 v[146:149], v144
	ds_read_b128 v[150:153], v144 offset:1024
	ds_read_b128 v[154:157], v144 offset:2048
	ds_read_b128 v[158:161], v144 offset:3072
	s_cmp_eq_u32 s45, 12
	s_cselect_b32 s43, s8, s41
	s_cselect_b32 s42, s27, s40
	s_cselect_b32 s41, s25, s44
	s_cselect_b32 s40, s35, s37
	v_lshl_add_u64 v[198:199], s[38:39], 0, v[140:141]
	s_add_i32 m0, s5, 0xc000
	ds_read_b128 v[164:167], v169
	ds_read_b128 v[170:173], v169 offset:1024
	ds_read_b128 v[174:177], v169 offset:2048
	ds_read_b128 v[178:181], v169 offset:3072
	ds_read_b128 v[182:185], v169 offset:4096
	ds_read_b128 v[186:189], v169 offset:5120
	ds_read_b128 v[190:193], v169 offset:6144
	ds_read_b128 v[194:197], v169 offset:7168
	global_load_lds_dwordx4 v[198:199], off
	v_lshl_add_u64 v[198:199], s[38:39], 0, v[142:143]
	s_add_i32 m0, s5, 0xe000
	s_nop 0
	global_load_lds_dwordx4 v[198:199], off
	s_waitcnt lgkmcnt(8)
	s_barrier
	v_add_u32_e32 v250, 0x14000, v145
	ds_read_b128 v[198:201], v250
	ds_read_b128 v[202:205], v250 offset:1024
	ds_read_b128 v[206:209], v250 offset:2048
	ds_read_b128 v[210:213], v250 offset:3072
	s_waitcnt lgkmcnt(4)
	s_waitcnt lgkmcnt(4)
	v_mfma_i32_16x16x64_i8 v[128:131], v[146:149], v[164:167], v[128:131]
	v_mfma_i32_16x16x64_i8 v[120:123], v[154:157], v[164:167], v[120:123]
	v_mfma_i32_16x16x64_i8 v[112:115], v[146:149], v[174:177], v[112:115]
	v_mfma_i32_16x16x64_i8 v[108:111], v[154:157], v[174:177], v[108:111]
	v_mfma_i32_16x16x64_i8 v[94:97], v[146:149], v[182:185], v[94:97]
	v_mfma_i32_16x16x64_i8 v[90:93], v[154:157], v[182:185], v[90:93]
	v_mfma_i32_16x16x64_i8 v[78:81], v[146:149], v[190:193], v[78:81]
	v_mfma_i32_16x16x64_i8 v[74:77], v[154:157], v[190:193], v[74:77]
	v_mfma_i32_16x16x64_i8 v[128:131], v[150:153], v[170:173], v[128:131]
	v_mfma_i32_16x16x64_i8 v[120:123], v[158:161], v[170:173], v[120:123]
	v_mfma_i32_16x16x64_i8 v[112:115], v[150:153], v[178:181], v[112:115]
	v_mfma_i32_16x16x64_i8 v[108:111], v[158:161], v[178:181], v[108:111]
	v_mfma_i32_16x16x64_i8 v[94:97], v[150:153], v[186:189], v[94:97]
	v_mfma_i32_16x16x64_i8 v[90:93], v[158:161], v[186:189], v[90:93]
	v_mfma_i32_16x16x64_i8 v[78:81], v[150:153], v[194:197], v[78:81]
	v_mfma_i32_16x16x64_i8 v[74:77], v[158:161], v[194:197], v[74:77]
	s_barrier
	s_add_i32 s48, 0, 0x14000
	s_add_i32 s46, s46, s3
	v_add_u32_e32 v144, s48, v145
	v_lshl_add_u64 v[214:215], s[40:41], 0, v[98:99]
	s_mov_b32 m0, s46
	global_load_lds_dwordx4 v[214:215], off
	v_lshl_add_u64 v[216:217], s[40:41], 0, v[136:137]
	s_add_i32 m0, s46, 0x2000
	s_nop 0
	global_load_lds_dwordx4 v[216:217], off
	s_barrier
	s_waitcnt lgkmcnt(0)
	s_waitcnt lgkmcnt(0)
	v_mfma_i32_16x16x64_i8 v[124:127], v[198:201], v[164:167], v[124:127]
	v_mfma_i32_16x16x64_i8 v[116:119], v[206:209], v[164:167], v[116:119]
	v_mfma_i32_16x16x64_i8 v[104:107], v[198:201], v[174:177], v[104:107]
	v_mfma_i32_16x16x64_i8 v[100:103], v[206:209], v[174:177], v[100:103]
	v_mfma_i32_16x16x64_i8 v[86:89], v[198:201], v[182:185], v[86:89]
	v_mfma_i32_16x16x64_i8 v[82:85], v[206:209], v[182:185], v[82:85]
	v_mfma_i32_16x16x64_i8 v[70:73], v[198:201], v[190:193], v[70:73]
	v_mfma_i32_16x16x64_i8 v[66:69], v[206:209], v[190:193], v[66:69]
	v_mfma_i32_16x16x64_i8 v[124:127], v[202:205], v[170:173], v[124:127]
	v_mfma_i32_16x16x64_i8 v[116:119], v[210:213], v[170:173], v[116:119]
	v_mfma_i32_16x16x64_i8 v[104:107], v[202:205], v[178:181], v[104:107]
	v_mfma_i32_16x16x64_i8 v[100:103], v[210:213], v[178:181], v[100:103]
	v_mfma_i32_16x16x64_i8 v[86:89], v[202:205], v[186:189], v[86:89]
	v_mfma_i32_16x16x64_i8 v[82:85], v[210:213], v[186:189], v[82:85]
	v_mfma_i32_16x16x64_i8 v[70:73], v[202:205], v[194:197], v[70:73]
	v_mfma_i32_16x16x64_i8 v[66:69], v[210:213], v[194:197], v[66:69]
	s_mov_b32 m0, s5
	v_lshl_add_u64 v[218:219], s[42:43], 0, v[132:133]
	s_barrier
	ds_read_b128 v[164:167], v169 offset:16384
	ds_read_b128 v[170:173], v169 offset:17408
	ds_read_b128 v[174:177], v169 offset:18432
	ds_read_b128 v[178:181], v169 offset:19456
	ds_read_b128 v[182:185], v169 offset:20480
	ds_read_b128 v[186:189], v169 offset:21504
	ds_read_b128 v[190:193], v169 offset:22528
	ds_read_b128 v[194:197], v169 offset:23552
	global_load_lds_dwordx4 v[218:219], off
	v_lshl_add_u64 v[222:223], s[42:43], 0, v[134:135]
	s_mov_b32 m0, s18
	s_nop 0
	global_load_lds_dwordx4 v[222:223], off
	s_barrier
	s_waitcnt lgkmcnt(0)
	s_waitcnt lgkmcnt(0)
	v_mfma_i32_16x16x64_i8 v[62:65], v[146:149], v[164:167], v[62:65]
	v_mfma_i32_16x16x64_i8 v[58:61], v[154:157], v[164:167], v[58:61]
	v_mfma_i32_16x16x64_i8 v[46:49], v[146:149], v[174:177], v[46:49]
	v_mfma_i32_16x16x64_i8 v[42:45], v[154:157], v[174:177], v[42:45]
	v_mfma_i32_16x16x64_i8 v[30:33], v[146:149], v[182:185], v[30:33]
	v_mfma_i32_16x16x64_i8 v[26:29], v[154:157], v[182:185], v[26:29]
	v_mfma_i32_16x16x64_i8 v[14:17], v[146:149], v[190:193], v[14:17]
	v_mfma_i32_16x16x64_i8 v[10:13], v[154:157], v[190:193], v[10:13]
	v_mfma_i32_16x16x64_i8 v[62:65], v[150:153], v[170:173], v[62:65]
	v_mfma_i32_16x16x64_i8 v[58:61], v[158:161], v[170:173], v[58:61]
	v_mfma_i32_16x16x64_i8 v[46:49], v[150:153], v[178:181], v[46:49]
	v_mfma_i32_16x16x64_i8 v[42:45], v[158:161], v[178:181], v[42:45]
	v_mfma_i32_16x16x64_i8 v[30:33], v[150:153], v[186:189], v[30:33]
	v_mfma_i32_16x16x64_i8 v[26:29], v[158:161], v[186:189], v[26:29]
	v_mfma_i32_16x16x64_i8 v[14:17], v[150:153], v[194:197], v[14:17]
	v_mfma_i32_16x16x64_i8 v[10:13], v[158:161], v[194:197], v[10:13]
	s_barrier
	s_add_u32 s46, s40, 0x40000
	s_addc_u32 s47, s41, 0
	s_add_i32 s48, s48, s3
	v_lshl_add_u64 v[146:147], s[46:47], 0, v[98:99]
	s_mov_b32 m0, s48
	s_nop 0
	global_load_lds_dwordx4 v[146:147], off
	v_lshl_add_u64 v[146:147], s[46:47], 0, v[136:137]
	s_add_i32 m0, s48, 0x2000
	s_nop 0
	global_load_lds_dwordx4 v[146:147], off
	s_waitcnt vmcnt(6)
	s_barrier
	v_mfma_i32_16x16x64_i8 v[54:57], v[198:201], v[164:167], v[54:57]
	v_mfma_i32_16x16x64_i8 v[50:53], v[206:209], v[164:167], v[50:53]
	v_mfma_i32_16x16x64_i8 v[38:41], v[198:201], v[174:177], v[38:41]
	v_mfma_i32_16x16x64_i8 v[34:37], v[206:209], v[174:177], v[34:37]
	v_mfma_i32_16x16x64_i8 v[22:25], v[198:201], v[182:185], v[22:25]
	v_mfma_i32_16x16x64_i8 v[18:21], v[206:209], v[182:185], v[18:21]
	v_mfma_i32_16x16x64_i8 v[6:9], v[198:201], v[190:193], v[6:9]
	v_mfma_i32_16x16x64_i8 v[2:5], v[206:209], v[190:193], v[2:5]
	v_mfma_i32_16x16x64_i8 v[54:57], v[202:205], v[170:173], v[54:57]
	v_mfma_i32_16x16x64_i8 v[50:53], v[210:213], v[170:173], v[50:53]
	v_mfma_i32_16x16x64_i8 v[38:41], v[202:205], v[178:181], v[38:41]
	v_mfma_i32_16x16x64_i8 v[34:37], v[210:213], v[178:181], v[34:37]
	v_mfma_i32_16x16x64_i8 v[22:25], v[202:205], v[186:189], v[22:25]
	v_mfma_i32_16x16x64_i8 v[18:21], v[210:213], v[186:189], v[18:21]
	v_mfma_i32_16x16x64_i8 v[6:9], v[202:205], v[194:197], v[6:9]
	v_mfma_i32_16x16x64_i8 v[2:5], v[210:213], v[194:197], v[2:5]
	s_add_i32 s46, 0, 0x18000
	v_add_u32_e32 v144, s46, v145
	s_barrier
	ds_read_b128 v[146:149], v144
	ds_read_b128 v[150:153], v144 offset:1024
	ds_read_b128 v[154:157], v144 offset:2048
	ds_read_b128 v[158:161], v144 offset:3072
	s_add_u32 s42, s42, 0x40000
	s_addc_u32 s43, s43, 0
	s_mov_b32 m0, s19
	v_lshl_add_u64 v[198:199], s[42:43], 0, v[132:133]
	ds_read_b128 v[164:167], v169 offset:32768
	ds_read_b128 v[170:173], v169 offset:33792
	ds_read_b128 v[174:177], v169 offset:34816
	ds_read_b128 v[178:181], v169 offset:35840
	ds_read_b128 v[182:185], v169 offset:36864
	ds_read_b128 v[186:189], v169 offset:37888
	ds_read_b128 v[190:193], v169 offset:38912
	ds_read_b128 v[194:197], v169 offset:39936
	global_load_lds_dwordx4 v[198:199], off
	v_lshl_add_u64 v[198:199], s[42:43], 0, v[134:135]
	s_mov_b32 m0, s20
	s_nop 0
	global_load_lds_dwordx4 v[198:199], off
	s_waitcnt lgkmcnt(8)
	s_barrier
	v_add_u32_e32 v250, 0x1c000, v145
	ds_read_b128 v[198:201], v250
	ds_read_b128 v[202:205], v250 offset:1024
	ds_read_b128 v[206:209], v250 offset:2048
	ds_read_b128 v[210:213], v250 offset:3072
	s_waitcnt lgkmcnt(4)
	s_waitcnt lgkmcnt(4)
	v_mfma_i32_16x16x64_i8 v[128:131], v[146:149], v[164:167], v[128:131]
	v_mfma_i32_16x16x64_i8 v[120:123], v[154:157], v[164:167], v[120:123]
	v_mfma_i32_16x16x64_i8 v[112:115], v[146:149], v[174:177], v[112:115]
	v_mfma_i32_16x16x64_i8 v[108:111], v[154:157], v[174:177], v[108:111]
	v_mfma_i32_16x16x64_i8 v[94:97], v[146:149], v[182:185], v[94:97]
	v_mfma_i32_16x16x64_i8 v[90:93], v[154:157], v[182:185], v[90:93]
	v_mfma_i32_16x16x64_i8 v[78:81], v[146:149], v[190:193], v[78:81]
	v_mfma_i32_16x16x64_i8 v[74:77], v[154:157], v[190:193], v[74:77]
	v_mfma_i32_16x16x64_i8 v[128:131], v[150:153], v[170:173], v[128:131]
	v_mfma_i32_16x16x64_i8 v[120:123], v[158:161], v[170:173], v[120:123]
	v_mfma_i32_16x16x64_i8 v[112:115], v[150:153], v[178:181], v[112:115]
	v_mfma_i32_16x16x64_i8 v[108:111], v[158:161], v[178:181], v[108:111]
	v_mfma_i32_16x16x64_i8 v[94:97], v[150:153], v[186:189], v[94:97]
	v_mfma_i32_16x16x64_i8 v[90:93], v[158:161], v[186:189], v[90:93]
	v_mfma_i32_16x16x64_i8 v[78:81], v[150:153], v[194:197], v[78:81]
	v_mfma_i32_16x16x64_i8 v[74:77], v[158:161], v[194:197], v[74:77]
	s_barrier
	s_add_i32 s42, 0, 0x1c000
	s_add_i32 s43, s46, s3
	v_add_u32_e32 v144, s42, v145
	v_lshl_add_u64 v[214:215], v[214:215], 0, s[68:69]
	s_mov_b32 m0, s43
	global_load_lds_dwordx4 v[214:215], off
	v_lshl_add_u64 v[214:215], v[216:217], 0, s[68:69]
	s_add_i32 m0, s43, 0x2000
	s_nop 0
	global_load_lds_dwordx4 v[214:215], off
	s_barrier
	s_waitcnt lgkmcnt(0)
	s_waitcnt lgkmcnt(0)
	v_mfma_i32_16x16x64_i8 v[124:127], v[198:201], v[164:167], v[124:127]
	v_mfma_i32_16x16x64_i8 v[116:119], v[206:209], v[164:167], v[116:119]
	v_mfma_i32_16x16x64_i8 v[104:107], v[198:201], v[174:177], v[104:107]
	v_mfma_i32_16x16x64_i8 v[100:103], v[206:209], v[174:177], v[100:103]
	v_mfma_i32_16x16x64_i8 v[86:89], v[198:201], v[182:185], v[86:89]
	v_mfma_i32_16x16x64_i8 v[82:85], v[206:209], v[182:185], v[82:85]
	v_mfma_i32_16x16x64_i8 v[70:73], v[198:201], v[190:193], v[70:73]
	v_mfma_i32_16x16x64_i8 v[66:69], v[206:209], v[190:193], v[66:69]
	v_mfma_i32_16x16x64_i8 v[124:127], v[202:205], v[170:173], v[124:127]
	v_mfma_i32_16x16x64_i8 v[116:119], v[210:213], v[170:173], v[116:119]
	v_mfma_i32_16x16x64_i8 v[104:107], v[202:205], v[178:181], v[104:107]
	v_mfma_i32_16x16x64_i8 v[100:103], v[210:213], v[178:181], v[100:103]
	v_mfma_i32_16x16x64_i8 v[86:89], v[202:205], v[186:189], v[86:89]
	v_mfma_i32_16x16x64_i8 v[82:85], v[210:213], v[186:189], v[82:85]
	v_mfma_i32_16x16x64_i8 v[70:73], v[202:205], v[194:197], v[70:73]
	v_mfma_i32_16x16x64_i8 v[66:69], v[210:213], v[194:197], v[66:69]
	s_mov_b32 m0, s9
	v_lshl_add_u64 v[214:215], v[218:219], 0, s[68:69]
	s_barrier
	ds_read_b128 v[164:167], v169 offset:49152
	ds_read_b128 v[170:173], v169 offset:50176
	ds_read_b128 v[174:177], v169 offset:51200
	ds_read_b128 v[178:181], v169 offset:52224
	ds_read_b128 v[182:185], v169 offset:53248
	ds_read_b128 v[186:189], v169 offset:54272
	ds_read_b128 v[190:193], v169 offset:55296
	ds_read_b128 v[194:197], v169 offset:56320
	global_load_lds_dwordx4 v[214:215], off
	v_lshl_add_u64 v[214:215], v[222:223], 0, s[68:69]
	s_mov_b32 m0, s21
	s_nop 0
	global_load_lds_dwordx4 v[214:215], off
	s_barrier
	s_waitcnt lgkmcnt(0)
	s_waitcnt lgkmcnt(0)
	v_mfma_i32_16x16x64_i8 v[62:65], v[146:149], v[164:167], v[62:65]
	v_mfma_i32_16x16x64_i8 v[58:61], v[154:157], v[164:167], v[58:61]
	v_mfma_i32_16x16x64_i8 v[46:49], v[146:149], v[174:177], v[46:49]
	v_mfma_i32_16x16x64_i8 v[42:45], v[154:157], v[174:177], v[42:45]
	v_mfma_i32_16x16x64_i8 v[30:33], v[146:149], v[182:185], v[30:33]
	v_mfma_i32_16x16x64_i8 v[26:29], v[154:157], v[182:185], v[26:29]
	v_mfma_i32_16x16x64_i8 v[14:17], v[146:149], v[190:193], v[14:17]
	v_mfma_i32_16x16x64_i8 v[10:13], v[154:157], v[190:193], v[10:13]
	v_mfma_i32_16x16x64_i8 v[62:65], v[150:153], v[170:173], v[62:65]
	v_mfma_i32_16x16x64_i8 v[58:61], v[158:161], v[170:173], v[58:61]
	v_mfma_i32_16x16x64_i8 v[46:49], v[150:153], v[178:181], v[46:49]
	v_mfma_i32_16x16x64_i8 v[42:45], v[158:161], v[178:181], v[42:45]
	v_mfma_i32_16x16x64_i8 v[30:33], v[150:153], v[186:189], v[30:33]
	v_mfma_i32_16x16x64_i8 v[26:29], v[158:161], v[186:189], v[26:29]
	v_mfma_i32_16x16x64_i8 v[14:17], v[150:153], v[194:197], v[14:17]
	v_mfma_i32_16x16x64_i8 v[10:13], v[158:161], v[194:197], v[10:13]
	s_barrier
	s_add_u32 s40, s40, 0x40080
	s_addc_u32 s41, s41, 0
	s_add_i32 s42, s42, s3
	v_lshl_add_u64 v[146:147], s[40:41], 0, v[98:99]
	s_mov_b32 m0, s42
	s_nop 0
	global_load_lds_dwordx4 v[146:147], off
	v_lshl_add_u64 v[146:147], s[40:41], 0, v[136:137]
	s_add_i32 m0, s42, 0x2000
	s_nop 0
	global_load_lds_dwordx4 v[146:147], off
	s_waitcnt vmcnt(6)
	s_barrier
	v_mfma_i32_16x16x64_i8 v[54:57], v[198:201], v[164:167], v[54:57]
	v_mfma_i32_16x16x64_i8 v[50:53], v[206:209], v[164:167], v[50:53]
	v_mfma_i32_16x16x64_i8 v[38:41], v[198:201], v[174:177], v[38:41]
	v_mfma_i32_16x16x64_i8 v[34:37], v[206:209], v[174:177], v[34:37]
	v_mfma_i32_16x16x64_i8 v[22:25], v[198:201], v[182:185], v[22:25]
	v_mfma_i32_16x16x64_i8 v[18:21], v[206:209], v[182:185], v[18:21]
	v_mfma_i32_16x16x64_i8 v[6:9], v[198:201], v[190:193], v[6:9]
	v_mfma_i32_16x16x64_i8 v[2:5], v[206:209], v[190:193], v[2:5]
	v_mfma_i32_16x16x64_i8 v[54:57], v[202:205], v[170:173], v[54:57]
	v_mfma_i32_16x16x64_i8 v[50:53], v[210:213], v[170:173], v[50:53]
	v_mfma_i32_16x16x64_i8 v[38:41], v[202:205], v[178:181], v[38:41]
	v_mfma_i32_16x16x64_i8 v[34:37], v[210:213], v[178:181], v[34:37]
	v_mfma_i32_16x16x64_i8 v[22:25], v[202:205], v[186:189], v[22:25]
	v_mfma_i32_16x16x64_i8 v[18:21], v[210:213], v[186:189], v[18:21]
	v_mfma_i32_16x16x64_i8 v[6:9], v[202:205], v[194:197], v[6:9]
	v_mfma_i32_16x16x64_i8 v[2:5], v[210:213], v[194:197], v[2:5]
	s_add_i32 s45, s45, 2
	s_add_u32 s38, s38, 0x100
	s_addc_u32 s39, s39, 0
	s_add_u32 s37, s37, 0x100
	s_addc_u32 s44, s44, 0
	s_cmp_gt_u32 s45, 13
	s_barrier
	s_cbranch_scc0 .LBB0_2088
	v_lshl_add_u32 v146, s36, 8, v1
	v_ashrrev_i32_e32 v147, 31, v146
	s_lshl_b32 s36, s34, 8
	v_lshl_add_u64 v[148:149], v[146:147], 2, s[54:55]
	s_ashr_i32 s37, s36, 31
	global_load_dword v182, v[148:149], off
	global_load_dword v180, v[148:149], off offset:64
	global_load_dword v174, v[148:149], off offset:128
	global_load_dword v172, v[148:149], off offset:192
	global_load_dword v170, v[148:149], off offset:512
	global_load_dword v168, v[148:149], off offset:576
	global_load_dword v162, v[148:149], off offset:640
	global_load_dword v144, v[148:149], off offset:704
	v_lshl_add_u64 v[148:149], s[36:37], 2, v[138:139]
	global_load_dwordx4 v[176:179], v[148:149], off offset:16
	global_load_dwordx4 v[150:153], v[148:149], off
	global_load_dwordx4 v[184:187], v[148:149], off offset:528
	global_load_dwordx4 v[154:157], v[148:149], off offset:512
	v_lshl_or_b32 v148, s34, 7, v163
	v_readlane_b32 s34, v252, 59
	v_readlane_b32 s35, v252, 60
	s_movk_i32 s8, 0x2c00
	v_cvt_f32_i32_e32 v129, v129
	v_cvt_f32_i32_e32 v121, v121
	v_ashrrev_i32_e32 v149, 31, v148
	s_waitcnt vmcnt(0)
	v_mov_b32_e32 v159, v150
	v_mov_b32_e32 v150, v155
	v_pk_mul_f32 v[164:165], v[150:151], s[58:59] op_sel_hi:[1,0]
	v_mov_b32_e32 v150, v156
	v_mov_b32_e32 v151, v152
	v_pk_mul_f32 v[160:161], v[150:151], s[58:59] op_sel_hi:[1,0]
	v_mov_b32_e32 v151, v176
	v_mov_b32_e32 v176, v185
	v_mov_b32_e32 v158, v154
	v_pk_mul_f32 v[154:155], v[176:177], s[58:59] op_sel_hi:[1,0]
	v_mov_b64_e32 v[176:177], s[34:35]
	v_mov_b32_e32 v150, v184
	v_mad_i64_i32 v[184:185], s[34:35], v146, s8, v[176:177]
	v_cvt_f32_i32_e32 v177, v128
	v_cvt_f32_i32_e32 v176, v124
	v_pk_mul_f32 v[166:167], v[158:159], s[58:59] op_sel_hi:[1,0]
	v_mov_b32_e32 v152, v157
	v_pk_mul_f32 v[156:157], v[150:151], s[58:59] op_sel_hi:[1,0]
	v_mov_b32_e32 v150, v186
	v_mov_b32_e32 v151, v178
	v_mov_b32_e32 v178, v187
	v_pk_mul_f32 v[158:159], v[152:153], s[58:59] op_sel_hi:[1,0]
	v_pk_mul_f32 v[152:153], v[150:151], s[58:59] op_sel_hi:[1,0]
	v_pk_mul_f32 v[150:151], v[178:179], s[58:59] op_sel_hi:[1,0]
	v_pk_mul_f32 v[178:179], v[182:183], v[166:167] op_sel_hi:[0,1]
	v_pk_mul_f32 v[176:177], v[178:179], v[176:177]
	v_cvt_f32_i32_e32 v128, v125
	v_mul_f32_e32 v124, 0xbfb8aa3b, v177
	v_exp_f32_e32 v124, v124
	s_nop 0
	v_add_f32_e32 v124, 1.0, v124
	v_rcp_f32_e32 v124, v124
	s_nop 0
	v_mul_f32_e32 v124, v177, v124
	v_mul_f32_e32 v124, v176, v124
	v_pk_mul_f32 v[176:177], v[182:183], v[164:165] op_sel_hi:[0,1]
	v_pk_mul_f32 v[128:129], v[176:177], v[128:129]
	v_pk_mul_f32 v[176:177], v[182:183], v[160:161] op_sel_hi:[0,1]
	v_mul_f32_e32 v125, 0xbfb8aa3b, v129
	v_exp_f32_e32 v125, v125
	s_nop 0
	v_add_f32_e32 v125, 1.0, v125
	v_rcp_f32_e32 v125, v125
	s_nop 0
	v_mul_f32_e32 v125, v129, v125
	v_mul_f32_e32 v125, v128, v125
	v_cvt_f32_i32_e32 v129, v130
	v_cvt_f32_i32_e32 v128, v126
	v_pk_mul_f32 v[128:129], v[176:177], v[128:129]
	s_nop 0
	v_mul_f32_e32 v126, 0xbfb8aa3b, v129
	v_exp_f32_e32 v126, v126
	s_nop 0
	v_add_f32_e32 v126, 1.0, v126
	v_rcp_f32_e32 v126, v126
	s_nop 0
	v_mul_f32_e32 v126, v129, v126
	v_mul_f32_e32 v126, v128, v126
	v_cvt_f32_i32_e32 v129, v131
	v_cvt_f32_i32_e32 v128, v127
	v_pk_mul_f32 v[130:131], v[182:183], v[158:159] op_sel_hi:[0,1]
	v_pk_mul_f32 v[128:129], v[130:131], v[128:129]
	s_nop 0
	v_mul_f32_e32 v127, 0xbfb8aa3b, v129
	v_exp_f32_e32 v127, v127
	v_pk_mul_f32 v[130:131], v[182:183], v[156:157] op_sel_hi:[0,1]
	v_add_f32_e32 v127, 1.0, v127
	v_rcp_f32_e32 v127, v127
	s_nop 0
	v_mul_f32_e32 v127, v129, v127
	v_mul_f32_e32 v127, v128, v127
	v_cvt_f32_i32_e32 v129, v120
	v_cvt_f32_i32_e32 v128, v116
	v_cvt_f32_i32_e32 v120, v117
	v_pk_mul_f32 v[128:129], v[130:131], v[128:129]
	s_nop 0
	v_mul_f32_e32 v116, 0xbfb8aa3b, v129
	v_exp_f32_e32 v116, v116
	s_nop 0
	v_add_f32_e32 v116, 1.0, v116
	v_rcp_f32_e32 v116, v116
	s_nop 0
	v_mul_f32_e32 v116, v129, v116
	v_mul_f32_e32 v128, v128, v116
	v_pk_mul_f32 v[116:117], v[182:183], v[154:155] op_sel_hi:[0,1]
	v_pk_mul_f32 v[116:117], v[116:117], v[120:121]
	s_nop 0
	v_mul_f32_e32 v120, 0xbfb8aa3b, v117
	v_exp_f32_e32 v120, v120
	s_nop 0
	v_add_f32_e32 v120, 1.0, v120
	v_rcp_f32_e32 v120, v120
	s_nop 0
	v_mul_f32_e32 v117, v117, v120
	v_mul_f32_e32 v129, v116, v117
	v_cvt_f32_i32_e32 v117, v122
	v_cvt_f32_i32_e32 v116, v118
	v_pk_mul_f32 v[120:121], v[182:183], v[152:153] op_sel_hi:[0,1]
	v_pk_mul_f32 v[116:117], v[120:121], v[116:117]
	s_nop 0
	v_mul_f32_e32 v118, 0xbfb8aa3b, v117
	v_exp_f32_e32 v118, v118
	v_lshl_add_u64 v[120:121], v[148:149], 1, v[184:185]
	v_add_f32_e32 v118, 1.0, v118
	v_rcp_f32_e32 v118, v118
	s_nop 0
	v_mul_f32_e32 v117, v117, v118
	v_mul_f32_e32 v122, v116, v117
	v_cvt_f32_i32_e32 v117, v123
	v_cvt_f32_i32_e32 v116, v119
	v_pk_mul_f32 v[118:119], v[182:183], v[150:151] op_sel_hi:[0,1]
	v_pk_mul_f32 v[116:117], v[118:119], v[116:117]
	s_nop 0
	v_mul_f32_e32 v118, 0xbfb8aa3b, v117
	v_exp_f32_e32 v118, v118
	s_nop 0
	v_add_f32_e32 v118, 1.0, v118
	v_rcp_f32_e32 v118, v118
	s_nop 0
	v_mul_f32_e32 v117, v117, v118
	v_mul_f32_e32 v123, v116, v117
	v_cvt_pk_bf16_f32 v116, v124, v125
	v_cvt_pk_bf16_f32 v117, v126, v127
	v_cvt_pk_bf16_f32 v118, v128, v129
	v_cvt_pk_bf16_f32 v119, v122, v123
	global_store_dwordx4 v[120:121], v[116:119], off
	s_nop 1
	v_max_f32_e64 v118, |v122|, |v123|
	v_max_f32_e64 v116, |v124|, |v125|
	v_max_f32_e64 v117, |v126|, |v127|
	v_max3_f32 v118, |v128|, |v129|, v118
	v_max3_f32 v116, v116, v117, v118
	v_mov_b32_e32 v117, v0
	s_nop 0
	v_lshlrev_b32_e32 v117, 2, v117
	v_bitop3_b32 v118, v117, 64, v220 bitop3:0x6c
	ds_bpermute_b32 v118, v118, v116
	v_bitop3_b32 v117, v117, s59, v220 bitop3:0x6c
	s_waitcnt lgkmcnt(0)
	v_max_f32_e32 v118, v118, v118
	v_max_f32_e32 v116, v116, v118
	ds_bpermute_b32 v117, v117, v116
	s_and_saveexec_b64 s[34:35], s[0:1]
	s_cbranch_execz .LBB0_2091
	v_readlane_b32 s36, v253, 57
	s_waitcnt lgkmcnt(0)
	v_max_f32_e32 v117, v117, v117
	v_max_f32_e32 v116, v116, v116
	v_readlane_b32 s37, v253, 58
	v_max_f32_e32 v118, v116, v117
	s_nop 0
	v_lshl_add_u64 v[116:117], v[146:147], 2, s[36:37]
	global_atomic_umax v[116:117], v118, off

.LBB0_2238:
	s_add_i32 s46, s30, 2
	s_add_u32 s28, s26, 0x100
	s_addc_u32 s29, s27, 0
	s_add_i32 s47, 0, 0x10000
	v_add_u32_e32 v142, s47, v1
	ds_read_b128 v[144:147], v142
	ds_read_b128 v[148:151], v142 offset:1024
	ds_read_b128 v[152:155], v142 offset:2048
	ds_read_b128 v[156:159], v142 offset:3072
	s_cmp_eq_u32 s19, s30
	s_cselect_b32 s30, s0, s33
	s_cselect_b32 s35, s25, s29
	s_cselect_b32 s34, s24, s28
	s_cselect_b32 s31, s1, s45
	v_lshl_add_u64 v[192:193], s[26:27], 0, v[138:139]
	s_add_i32 m0, s20, 0xc000
	ds_read_b128 v[160:163], v143
	ds_read_b128 v[164:167], v143 offset:1024
	ds_read_b128 v[168:171], v143 offset:2048
	ds_read_b128 v[172:175], v143 offset:3072
	ds_read_b128 v[176:179], v143 offset:4096
	ds_read_b128 v[180:183], v143 offset:5120
	ds_read_b128 v[184:187], v143 offset:6144
	ds_read_b128 v[188:191], v143 offset:7168
	global_load_lds_dwordx4 v[192:193], off
	v_lshl_add_u64 v[192:193], s[26:27], 0, v[140:141]
	s_add_i32 m0, s20, 0xe000
	s_nop 0
	global_load_lds_dwordx4 v[192:193], off
	s_waitcnt lgkmcnt(8)
	s_barrier
	v_add_u32_e32 v250, 0x14000, v1
	ds_read_b128 v[192:195], v250
	ds_read_b128 v[196:199], v250 offset:1024
	ds_read_b128 v[200:203], v250 offset:2048
	ds_read_b128 v[204:207], v250 offset:3072
	s_waitcnt lgkmcnt(4)
	s_waitcnt lgkmcnt(4)
	v_mfma_i32_16x16x64_i8 v[128:131], v[144:147], v[160:163], v[128:131]
	v_mfma_i32_16x16x64_i8 v[124:127], v[152:155], v[160:163], v[124:127]
	v_mfma_i32_16x16x64_i8 v[120:123], v[144:147], v[168:171], v[120:123]
	v_mfma_i32_16x16x64_i8 v[116:119], v[152:155], v[168:171], v[116:119]
	v_mfma_i32_16x16x64_i8 v[112:115], v[144:147], v[176:179], v[112:115]
	v_mfma_i32_16x16x64_i8 v[108:111], v[152:155], v[176:179], v[108:111]
	v_mfma_i32_16x16x64_i8 v[104:107], v[144:147], v[184:187], v[104:107]
	v_mfma_i32_16x16x64_i8 v[100:103], v[152:155], v[184:187], v[100:103]
	v_mfma_i32_16x16x64_i8 v[128:131], v[148:151], v[164:167], v[128:131]
	v_mfma_i32_16x16x64_i8 v[124:127], v[156:159], v[164:167], v[124:127]
	v_mfma_i32_16x16x64_i8 v[120:123], v[148:151], v[172:175], v[120:123]
	v_mfma_i32_16x16x64_i8 v[116:119], v[156:159], v[172:175], v[116:119]
	v_mfma_i32_16x16x64_i8 v[112:115], v[148:151], v[180:183], v[112:115]
	v_mfma_i32_16x16x64_i8 v[108:111], v[156:159], v[180:183], v[108:111]
	v_mfma_i32_16x16x64_i8 v[104:107], v[148:151], v[188:191], v[104:107]
	v_mfma_i32_16x16x64_i8 v[100:103], v[156:159], v[188:191], v[100:103]
	s_barrier
	s_add_i32 s48, 0, 0x14000
	s_add_i32 s26, s47, s5
	v_add_u32_e32 v142, s48, v1
	v_lshl_add_u64 v[208:209], s[30:31], 0, v[98:99]
	s_mov_b32 m0, s26
	global_load_lds_dwordx4 v[208:209], off
	v_lshl_add_u64 v[210:211], s[30:31], 0, v[132:133]
	s_add_i32 m0, s26, 0x2000
	s_nop 0
	global_load_lds_dwordx4 v[210:211], off
	s_barrier
	s_waitcnt lgkmcnt(0)
	s_waitcnt lgkmcnt(0)
	v_mfma_i32_16x16x64_i8 v[94:97], v[192:195], v[160:163], v[94:97]
	v_mfma_i32_16x16x64_i8 v[90:93], v[200:203], v[160:163], v[90:93]
	v_mfma_i32_16x16x64_i8 v[86:89], v[192:195], v[168:171], v[86:89]
	v_mfma_i32_16x16x64_i8 v[82:85], v[200:203], v[168:171], v[82:85]
	v_mfma_i32_16x16x64_i8 v[78:81], v[192:195], v[176:179], v[78:81]
	v_mfma_i32_16x16x64_i8 v[74:77], v[200:203], v[176:179], v[74:77]
	v_mfma_i32_16x16x64_i8 v[70:73], v[192:195], v[184:187], v[70:73]
	v_mfma_i32_16x16x64_i8 v[66:69], v[200:203], v[184:187], v[66:69]
	v_mfma_i32_16x16x64_i8 v[94:97], v[196:199], v[164:167], v[94:97]
	v_mfma_i32_16x16x64_i8 v[90:93], v[204:207], v[164:167], v[90:93]
	v_mfma_i32_16x16x64_i8 v[86:89], v[196:199], v[172:175], v[86:89]
	v_mfma_i32_16x16x64_i8 v[82:85], v[204:207], v[172:175], v[82:85]
	v_mfma_i32_16x16x64_i8 v[78:81], v[196:199], v[180:183], v[78:81]
	v_mfma_i32_16x16x64_i8 v[74:77], v[204:207], v[180:183], v[74:77]
	v_mfma_i32_16x16x64_i8 v[70:73], v[196:199], v[188:191], v[70:73]
	v_mfma_i32_16x16x64_i8 v[66:69], v[204:207], v[188:191], v[66:69]
	s_mov_b32 m0, s20
	v_lshl_add_u64 v[212:213], s[34:35], 0, v[98:99]
	s_barrier
	ds_read_b128 v[160:163], v143 offset:16384
	ds_read_b128 v[164:167], v143 offset:17408
	ds_read_b128 v[168:171], v143 offset:18432
	ds_read_b128 v[172:175], v143 offset:19456
	ds_read_b128 v[176:179], v143 offset:20480
	ds_read_b128 v[180:183], v143 offset:21504
	ds_read_b128 v[184:187], v143 offset:22528
	ds_read_b128 v[188:191], v143 offset:23552
	global_load_lds_dwordx4 v[212:213], off
	v_lshl_add_u64 v[214:215], s[34:35], 0, v[132:133]
	s_mov_b32 m0, s21
	s_nop 0
	global_load_lds_dwordx4 v[214:215], off
	s_barrier
	s_waitcnt lgkmcnt(0)
	s_waitcnt lgkmcnt(0)
	v_mfma_i32_16x16x64_i8 v[62:65], v[144:147], v[160:163], v[62:65]
	v_mfma_i32_16x16x64_i8 v[58:61], v[152:155], v[160:163], v[58:61]
	v_mfma_i32_16x16x64_i8 v[54:57], v[144:147], v[168:171], v[54:57]
	v_mfma_i32_16x16x64_i8 v[50:53], v[152:155], v[168:171], v[50:53]
	v_mfma_i32_16x16x64_i8 v[46:49], v[144:147], v[176:179], v[46:49]
	v_mfma_i32_16x16x64_i8 v[42:45], v[152:155], v[176:179], v[42:45]
	v_mfma_i32_16x16x64_i8 v[38:41], v[144:147], v[184:187], v[38:41]
	v_mfma_i32_16x16x64_i8 v[34:37], v[152:155], v[184:187], v[34:37]
	v_mfma_i32_16x16x64_i8 v[62:65], v[148:151], v[164:167], v[62:65]
	v_mfma_i32_16x16x64_i8 v[58:61], v[156:159], v[164:167], v[58:61]
	v_mfma_i32_16x16x64_i8 v[54:57], v[148:151], v[172:175], v[54:57]
	v_mfma_i32_16x16x64_i8 v[50:53], v[156:159], v[172:175], v[50:53]
	v_mfma_i32_16x16x64_i8 v[46:49], v[148:151], v[180:183], v[46:49]
	v_mfma_i32_16x16x64_i8 v[42:45], v[156:159], v[180:183], v[42:45]
	v_mfma_i32_16x16x64_i8 v[38:41], v[148:151], v[188:191], v[38:41]
	v_mfma_i32_16x16x64_i8 v[34:37], v[156:159], v[188:191], v[34:37]
	s_barrier
	s_add_u32 s26, s30, 0xb0000
	s_addc_u32 s27, s31, 0
	s_add_i32 s47, s48, s5
	v_lshl_add_u64 v[144:145], s[26:27], 0, v[98:99]
	s_mov_b32 m0, s47
	s_nop 0
	global_load_lds_dwordx4 v[144:145], off
	v_lshl_add_u64 v[144:145], s[26:27], 0, v[132:133]
	s_add_i32 m0, s47, 0x2000
	s_nop 0
	global_load_lds_dwordx4 v[144:145], off
	s_waitcnt vmcnt(6)
	s_barrier
	v_mfma_i32_16x16x64_i8 v[30:33], v[192:195], v[160:163], v[30:33]
	v_mfma_i32_16x16x64_i8 v[26:29], v[200:203], v[160:163], v[26:29]
	v_mfma_i32_16x16x64_i8 v[22:25], v[192:195], v[168:171], v[22:25]
	v_mfma_i32_16x16x64_i8 v[18:21], v[200:203], v[168:171], v[18:21]
	v_mfma_i32_16x16x64_i8 v[14:17], v[192:195], v[176:179], v[14:17]
	v_mfma_i32_16x16x64_i8 v[10:13], v[200:203], v[176:179], v[10:13]
	v_mfma_i32_16x16x64_i8 v[6:9], v[192:195], v[184:187], v[6:9]
	v_mfma_i32_16x16x64_i8 v[2:5], v[200:203], v[184:187], v[2:5]
	v_mfma_i32_16x16x64_i8 v[30:33], v[196:199], v[164:167], v[30:33]
	v_mfma_i32_16x16x64_i8 v[26:29], v[204:207], v[164:167], v[26:29]
	v_mfma_i32_16x16x64_i8 v[22:25], v[196:199], v[172:175], v[22:25]
	v_mfma_i32_16x16x64_i8 v[18:21], v[204:207], v[172:175], v[18:21]
	v_mfma_i32_16x16x64_i8 v[14:17], v[196:199], v[180:183], v[14:17]
	v_mfma_i32_16x16x64_i8 v[10:13], v[204:207], v[180:183], v[10:13]
	v_mfma_i32_16x16x64_i8 v[6:9], v[196:199], v[188:191], v[6:9]
	v_mfma_i32_16x16x64_i8 v[2:5], v[204:207], v[188:191], v[2:5]
	s_add_i32 s47, 0, 0x18000
	v_add_u32_e32 v142, s47, v1
	s_barrier
	ds_read_b128 v[144:147], v142
	ds_read_b128 v[148:151], v142 offset:1024
	ds_read_b128 v[152:155], v142 offset:2048
	ds_read_b128 v[156:159], v142 offset:3072
	s_add_u32 s26, s34, 0xb0000
	s_addc_u32 s27, s35, 0
	s_mov_b32 m0, s36
	v_lshl_add_u64 v[192:193], s[26:27], 0, v[98:99]
	ds_read_b128 v[160:163], v143 offset:32768
	ds_read_b128 v[164:167], v143 offset:33792
	ds_read_b128 v[168:171], v143 offset:34816
	ds_read_b128 v[172:175], v143 offset:35840
	ds_read_b128 v[176:179], v143 offset:36864
	ds_read_b128 v[180:183], v143 offset:37888
	ds_read_b128 v[184:187], v143 offset:38912
	ds_read_b128 v[188:191], v143 offset:39936
	global_load_lds_dwordx4 v[192:193], off
	v_lshl_add_u64 v[192:193], s[26:27], 0, v[132:133]
	s_mov_b32 m0, s37
	s_nop 0
	global_load_lds_dwordx4 v[192:193], off
	s_waitcnt lgkmcnt(8)
	s_barrier
	v_add_u32_e32 v250, 0x1c000, v1
	ds_read_b128 v[192:195], v250
	ds_read_b128 v[196:199], v250 offset:1024
	ds_read_b128 v[200:203], v250 offset:2048
	ds_read_b128 v[204:207], v250 offset:3072
	s_waitcnt lgkmcnt(4)
	s_waitcnt lgkmcnt(4)
	v_mfma_i32_16x16x64_i8 v[128:131], v[144:147], v[160:163], v[128:131]
	v_mfma_i32_16x16x64_i8 v[124:127], v[152:155], v[160:163], v[124:127]
	v_mfma_i32_16x16x64_i8 v[120:123], v[144:147], v[168:171], v[120:123]
	v_mfma_i32_16x16x64_i8 v[116:119], v[152:155], v[168:171], v[116:119]
	v_mfma_i32_16x16x64_i8 v[112:115], v[144:147], v[176:179], v[112:115]
	v_mfma_i32_16x16x64_i8 v[108:111], v[152:155], v[176:179], v[108:111]
	v_mfma_i32_16x16x64_i8 v[104:107], v[144:147], v[184:187], v[104:107]
	v_mfma_i32_16x16x64_i8 v[100:103], v[152:155], v[184:187], v[100:103]
	v_mfma_i32_16x16x64_i8 v[128:131], v[148:151], v[164:167], v[128:131]
	v_mfma_i32_16x16x64_i8 v[124:127], v[156:159], v[164:167], v[124:127]
	v_mfma_i32_16x16x64_i8 v[120:123], v[148:151], v[172:175], v[120:123]
	v_mfma_i32_16x16x64_i8 v[116:119], v[156:159], v[172:175], v[116:119]
	v_mfma_i32_16x16x64_i8 v[112:115], v[148:151], v[180:183], v[112:115]
	v_mfma_i32_16x16x64_i8 v[108:111], v[156:159], v[180:183], v[108:111]
	v_mfma_i32_16x16x64_i8 v[104:107], v[148:151], v[188:191], v[104:107]
	v_mfma_i32_16x16x64_i8 v[100:103], v[156:159], v[188:191], v[100:103]
	s_barrier
	s_add_i32 s34, 0, 0x1c000
	s_add_i32 s26, s47, s5
	v_add_u32_e32 v142, s34, v1
	v_lshl_add_u64 v[208:209], v[208:209], 0, s[68:69]
	s_mov_b32 m0, s26
	global_load_lds_dwordx4 v[208:209], off
	v_lshl_add_u64 v[208:209], v[210:211], 0, s[68:69]
	s_add_i32 m0, s26, 0x2000
	s_nop 0
	global_load_lds_dwordx4 v[208:209], off
	s_barrier
	s_waitcnt lgkmcnt(0)
	s_waitcnt lgkmcnt(0)
	v_mfma_i32_16x16x64_i8 v[94:97], v[192:195], v[160:163], v[94:97]
	v_mfma_i32_16x16x64_i8 v[90:93], v[200:203], v[160:163], v[90:93]
	v_mfma_i32_16x16x64_i8 v[86:89], v[192:195], v[168:171], v[86:89]
	v_mfma_i32_16x16x64_i8 v[82:85], v[200:203], v[168:171], v[82:85]
	v_mfma_i32_16x16x64_i8 v[78:81], v[192:195], v[176:179], v[78:81]
	v_mfma_i32_16x16x64_i8 v[74:77], v[200:203], v[176:179], v[74:77]
	v_mfma_i32_16x16x64_i8 v[70:73], v[192:195], v[184:187], v[70:73]
	v_mfma_i32_16x16x64_i8 v[66:69], v[200:203], v[184:187], v[66:69]
	v_mfma_i32_16x16x64_i8 v[94:97], v[196:199], v[164:167], v[94:97]
	v_mfma_i32_16x16x64_i8 v[90:93], v[204:207], v[164:167], v[90:93]
	v_mfma_i32_16x16x64_i8 v[86:89], v[196:199], v[172:175], v[86:89]
	v_mfma_i32_16x16x64_i8 v[82:85], v[204:207], v[172:175], v[82:85]
	v_mfma_i32_16x16x64_i8 v[78:81], v[196:199], v[180:183], v[78:81]
	v_mfma_i32_16x16x64_i8 v[74:77], v[204:207], v[180:183], v[74:77]
	v_mfma_i32_16x16x64_i8 v[70:73], v[196:199], v[188:191], v[70:73]
	v_mfma_i32_16x16x64_i8 v[66:69], v[204:207], v[188:191], v[66:69]
	s_mov_b32 m0, s38
	v_lshl_add_u64 v[208:209], v[212:213], 0, s[68:69]
	s_barrier
	ds_read_b128 v[160:163], v143 offset:49152
	ds_read_b128 v[164:167], v143 offset:50176
	ds_read_b128 v[168:171], v143 offset:51200
	ds_read_b128 v[172:175], v143 offset:52224
	ds_read_b128 v[176:179], v143 offset:53248
	ds_read_b128 v[180:183], v143 offset:54272
	ds_read_b128 v[184:187], v143 offset:55296
	ds_read_b128 v[188:191], v143 offset:56320
	global_load_lds_dwordx4 v[208:209], off
	v_lshl_add_u64 v[208:209], v[214:215], 0, s[68:69]
	s_mov_b32 m0, s39
	s_nop 0
	global_load_lds_dwordx4 v[208:209], off
	s_barrier
	s_waitcnt lgkmcnt(0)
	s_waitcnt lgkmcnt(0)
	v_mfma_i32_16x16x64_i8 v[62:65], v[144:147], v[160:163], v[62:65]
	v_mfma_i32_16x16x64_i8 v[58:61], v[152:155], v[160:163], v[58:61]
	v_mfma_i32_16x16x64_i8 v[54:57], v[144:147], v[168:171], v[54:57]
	v_mfma_i32_16x16x64_i8 v[50:53], v[152:155], v[168:171], v[50:53]
	v_mfma_i32_16x16x64_i8 v[46:49], v[144:147], v[176:179], v[46:49]
	v_mfma_i32_16x16x64_i8 v[42:45], v[152:155], v[176:179], v[42:45]
	v_mfma_i32_16x16x64_i8 v[38:41], v[144:147], v[184:187], v[38:41]
	v_mfma_i32_16x16x64_i8 v[34:37], v[152:155], v[184:187], v[34:37]
	v_mfma_i32_16x16x64_i8 v[62:65], v[148:151], v[164:167], v[62:65]
	v_mfma_i32_16x16x64_i8 v[58:61], v[156:159], v[164:167], v[58:61]
	v_mfma_i32_16x16x64_i8 v[54:57], v[148:151], v[172:175], v[54:57]
	v_mfma_i32_16x16x64_i8 v[50:53], v[156:159], v[172:175], v[50:53]
	v_mfma_i32_16x16x64_i8 v[46:49], v[148:151], v[180:183], v[46:49]
	v_mfma_i32_16x16x64_i8 v[42:45], v[156:159], v[180:183], v[42:45]
	v_mfma_i32_16x16x64_i8 v[38:41], v[148:151], v[188:191], v[38:41]
	v_mfma_i32_16x16x64_i8 v[34:37], v[156:159], v[188:191], v[34:37]
	s_barrier
	s_add_u32 s26, s30, 0xb0080
	s_addc_u32 s27, s31, 0
	s_add_i32 s30, s34, s5
	v_lshl_add_u64 v[144:145], s[26:27], 0, v[98:99]
	s_mov_b32 m0, s30
	s_nop 0
	global_load_lds_dwordx4 v[144:145], off
	v_lshl_add_u64 v[144:145], s[26:27], 0, v[132:133]
	s_add_i32 m0, s30, 0x2000
	s_nop 0
	global_load_lds_dwordx4 v[144:145], off
	s_waitcnt vmcnt(6)
	s_barrier
	v_mfma_i32_16x16x64_i8 v[30:33], v[192:195], v[160:163], v[30:33]
	v_mfma_i32_16x16x64_i8 v[26:29], v[200:203], v[160:163], v[26:29]
	v_mfma_i32_16x16x64_i8 v[22:25], v[192:195], v[168:171], v[22:25]
	v_mfma_i32_16x16x64_i8 v[18:21], v[200:203], v[168:171], v[18:21]
	v_mfma_i32_16x16x64_i8 v[14:17], v[192:195], v[176:179], v[14:17]
	v_mfma_i32_16x16x64_i8 v[10:13], v[200:203], v[176:179], v[10:13]
	v_mfma_i32_16x16x64_i8 v[6:9], v[192:195], v[184:187], v[6:9]
	v_mfma_i32_16x16x64_i8 v[2:5], v[200:203], v[184:187], v[2:5]
	v_mfma_i32_16x16x64_i8 v[30:33], v[196:199], v[164:167], v[30:33]
	v_mfma_i32_16x16x64_i8 v[26:29], v[204:207], v[164:167], v[26:29]
	v_mfma_i32_16x16x64_i8 v[22:25], v[196:199], v[172:175], v[22:25]
	v_mfma_i32_16x16x64_i8 v[18:21], v[204:207], v[172:175], v[18:21]
	v_mfma_i32_16x16x64_i8 v[14:17], v[196:199], v[180:183], v[14:17]
	v_mfma_i32_16x16x64_i8 v[10:13], v[204:207], v[180:183], v[10:13]
	v_mfma_i32_16x16x64_i8 v[6:9], v[196:199], v[188:191], v[6:9]
	v_mfma_i32_16x16x64_i8 v[2:5], v[204:207], v[188:191], v[2:5]
	s_add_u32 s33, s33, 0x100
	s_addc_u32 s45, s45, 0
	s_cmp_ge_i32 s46, s8
	s_mov_b64 s[26:27], s[28:29]
	s_mov_b32 s30, s46
	s_barrier
	s_cbranch_scc0 .LBB0_2238
	v_lshl_add_u32 v190, s9, 8, v134
	v_readlane_b32 s8, v253, 57
	v_ashrrev_i32_e32 v191, 31, v190
	v_readlane_b32 s9, v253, 58
	v_lshl_or_b32 v192, s3, 8, v135
	v_ashrrev_i32_e32 v193, 31, v192
	v_lshl_add_u64 v[158:159], v[190:191], 2, s[8:9]
	v_readlane_b32 s8, v254, 30
	v_readlane_b32 s9, v254, 31
	v_cvt_f32_i32_e32 v161, v129
	v_cvt_f32_i32_e32 v160, v128
	v_cvt_f32_i32_e32 v129, v127
	v_cvt_f32_i32_e32 v128, v126
	v_cvt_f32_i32_e32 v127, v87
	v_cvt_f32_i32_e32 v126, v86
	v_cvt_f32_i32_e32 v87, v77
	v_cvt_f32_i32_e32 v86, v76
	v_cvt_f32_i32_e32 v77, v31
	v_cvt_f32_i32_e32 v76, v30
	v_cvt_f32_i32_e32 v31, v21
	v_cvt_f32_i32_e32 v30, v20
	v_cvt_f32_i32_e32 v21, v7
	v_cvt_f32_i32_e32 v20, v6
	v_lshl_add_u64 v[6:7], v[192:193], 2, s[8:9]
	global_load_dword v156, v[158:159], off
	global_load_dword v154, v[158:159], off offset:64
	global_load_dword v152, v[158:159], off offset:128
	global_load_dword v150, v[158:159], off offset:192
	global_load_dword v148, v[158:159], off offset:512
	global_load_dword v146, v[158:159], off offset:576
	global_load_dword v144, v[158:159], off offset:640
	global_load_dword v142, v[158:159], off offset:704
	v_cvt_f32_i32_e32 v163, v93
	v_cvt_f32_i32_e32 v162, v92
	v_cvt_f32_i32_e32 v165, v91
	v_cvt_f32_i32_e32 v164, v90
	v_cvt_f32_i32_e32 v91, v81
	v_cvt_f32_i32_e32 v90, v80
	v_cvt_f32_i32_e32 v93, v79
	v_cvt_f32_i32_e32 v92, v78
	v_cvt_f32_i32_e32 v79, v69
	v_cvt_f32_i32_e32 v78, v68
	v_cvt_f32_i32_e32 v81, v67
	v_cvt_f32_i32_e32 v80, v66
	v_cvt_f32_i32_e32 v67, v29
	v_cvt_f32_i32_e32 v66, v28
	v_cvt_f32_i32_e32 v69, v27
	v_cvt_f32_i32_e32 v68, v26
	v_cvt_f32_i32_e32 v27, v17
	v_cvt_f32_i32_e32 v26, v16
	v_cvt_f32_i32_e32 v29, v15
	v_cvt_f32_i32_e32 v28, v14
	v_cvt_f32_i32_e32 v15, v5
	v_cvt_f32_i32_e32 v14, v4
	v_cvt_f32_i32_e32 v17, v3
	v_cvt_f32_i32_e32 v16, v2
	global_load_dwordx4 v[2:5], v[6:7], off
	v_cvt_f32_i32_e32 v159, v131
	v_cvt_f32_i32_e32 v158, v130
	v_cvt_f32_i32_e32 v131, v125
	v_cvt_f32_i32_e32 v130, v124
	v_cvt_f32_i32_e32 v123, v123
	v_cvt_f32_i32_e32 v122, v122
	v_cvt_f32_i32_e32 v121, v121
	v_cvt_f32_i32_e32 v120, v120
	v_cvt_f32_i32_e32 v119, v119
	v_cvt_f32_i32_e32 v118, v118
	v_cvt_f32_i32_e32 v117, v117
	v_cvt_f32_i32_e32 v116, v116
	v_cvt_f32_i32_e32 v115, v115
	v_cvt_f32_i32_e32 v114, v114
	v_cvt_f32_i32_e32 v113, v113
	v_cvt_f32_i32_e32 v112, v112
	v_cvt_f32_i32_e32 v111, v111
	v_cvt_f32_i32_e32 v110, v110
	v_cvt_f32_i32_e32 v109, v109
	v_cvt_f32_i32_e32 v108, v108
	v_cvt_f32_i32_e32 v107, v107
	v_cvt_f32_i32_e32 v106, v106
	v_cvt_f32_i32_e32 v105, v105
	v_cvt_f32_i32_e32 v104, v104
	v_cvt_f32_i32_e32 v103, v103
	v_cvt_f32_i32_e32 v102, v102
	v_cvt_f32_i32_e32 v101, v101
	v_cvt_f32_i32_e32 v100, v100
	v_cvt_f32_i32_e32 v167, v97
	v_cvt_f32_i32_e32 v166, v96
	v_cvt_f32_i32_e32 v169, v95
	v_cvt_f32_i32_e32 v168, v94
	v_cvt_f32_i32_e32 v125, v89
	v_cvt_f32_i32_e32 v124, v88
	v_cvt_f32_i32_e32 v95, v85
	v_cvt_f32_i32_e32 v94, v84
	v_cvt_f32_i32_e32 v97, v83
	v_cvt_f32_i32_e32 v96, v82
	v_cvt_f32_i32_e32 v89, v75
	v_cvt_f32_i32_e32 v88, v74
	v_cvt_f32_i32_e32 v83, v73
	v_cvt_f32_i32_e32 v82, v72
	v_cvt_f32_i32_e32 v85, v71
	v_cvt_f32_i32_e32 v84, v70
	v_cvt_f32_i32_e32 v71, v65
	v_cvt_f32_i32_e32 v70, v64
	v_cvt_f32_i32_e32 v73, v63
	v_cvt_f32_i32_e32 v72, v62
	v_cvt_f32_i32_e32 v63, v61
	v_cvt_f32_i32_e32 v62, v60
	v_cvt_f32_i32_e32 v65, v59
	v_cvt_f32_i32_e32 v64, v58
	v_cvt_f32_i32_e32 v57, v57
	v_cvt_f32_i32_e32 v56, v56
	v_cvt_f32_i32_e32 v55, v55
	v_cvt_f32_i32_e32 v54, v54
	v_cvt_f32_i32_e32 v53, v53
	v_cvt_f32_i32_e32 v52, v52
	v_cvt_f32_i32_e32 v51, v51
	v_cvt_f32_i32_e32 v50, v50
	v_cvt_f32_i32_e32 v49, v49
	v_cvt_f32_i32_e32 v48, v48
	v_cvt_f32_i32_e32 v47, v47
	v_cvt_f32_i32_e32 v46, v46
	v_cvt_f32_i32_e32 v45, v45
	v_cvt_f32_i32_e32 v44, v44
	v_cvt_f32_i32_e32 v43, v43
	v_cvt_f32_i32_e32 v42, v42
	v_cvt_f32_i32_e32 v41, v41
	v_cvt_f32_i32_e32 v40, v40
	v_cvt_f32_i32_e32 v39, v39
	v_cvt_f32_i32_e32 v38, v38
	v_cvt_f32_i32_e32 v37, v37
	v_cvt_f32_i32_e32 v36, v36
	v_cvt_f32_i32_e32 v35, v35
	v_cvt_f32_i32_e32 v34, v34
	v_cvt_f32_i32_e32 v75, v33
	v_cvt_f32_i32_e32 v74, v32
	v_cvt_f32_i32_e32 v59, v25
	s_waitcnt vmcnt(0)
	v_pk_mul_f32 v[170:171], v[4:5], s[58:59] op_sel_hi:[1,0]
	v_pk_mul_f32 v[172:173], v[2:3], s[58:59] op_sel_hi:[1,0]
	global_load_dwordx4 v[2:5], v[6:7], off offset:64
	v_cvt_f32_i32_e32 v58, v24
	v_cvt_f32_i32_e32 v61, v23
	v_cvt_f32_i32_e32 v60, v22
	v_cvt_f32_i32_e32 v33, v19
	v_cvt_f32_i32_e32 v32, v18
	v_cvt_f32_i32_e32 v23, v13
	v_cvt_f32_i32_e32 v22, v12
	v_cvt_f32_i32_e32 v25, v11
	v_cvt_f32_i32_e32 v24, v10
	v_cvt_f32_i32_e32 v19, v9
	v_cvt_f32_i32_e32 v18, v8
	s_mov_b64 s[26:27], -1
	s_cmp_lt_i32 s62, 0
	s_waitcnt vmcnt(0)
	v_pk_mul_f32 v[174:175], v[4:5], s[58:59] op_sel_hi:[1,0]
	v_pk_mul_f32 v[180:181], v[2:3], s[58:59] op_sel_hi:[1,0]
	global_load_dwordx4 v[2:5], v[6:7], off offset:512
	s_waitcnt vmcnt(0)
	v_pk_mul_f32 v[182:183], v[4:5], s[58:59] op_sel_hi:[1,0]
	v_pk_mul_f32 v[184:185], v[2:3], s[58:59] op_sel_hi:[1,0]
	global_load_dwordx4 v[2:5], v[6:7], off offset:576
	s_waitcnt vmcnt(0)
	v_pk_mul_f32 v[186:187], v[4:5], s[58:59] op_sel_hi:[1,0]
	v_pk_mul_f32 v[188:189], v[2:3], s[58:59] op_sel_hi:[1,0]
	s_cbranch_scc0 .LBB0_2241
	v_readlane_b32 s8, v254, 28
	v_lshlrev_b64 v[2:3], 2, v[192:193]
	v_readlane_b32 s9, v254, 29
	v_pk_mul_f32 v[218:219], v[156:157], v[160:161] op_sel_hi:[0,1]
	v_pk_mul_f32 v[244:245], v[152:153], v[112:113] op_sel_hi:[0,1]
	v_lshl_add_u64 v[8:9], s[8:9], 0, v[2:3]
	global_load_dwordx4 v[4:7], v[8:9], off
	v_readlane_b32 s8, v253, 28
	v_readlane_b32 s9, v253, 29
	s_mov_b32 s3, 0x100000
	s_mov_b64 s[26:27], 0
	v_lshl_add_u64 v[212:213], s[8:9], 0, v[2:3]
	s_mov_b64 s[8:9], 0x100000
	s_waitcnt vmcnt(0)
	v_pk_mul_f32 v[206:207], v[170:171], v[6:7]
	v_pk_mul_f32 v[208:209], v[172:173], v[4:5]
	global_load_dwordx4 v[4:7], v[8:9], off offset:64
	s_waitcnt vmcnt(0)
	v_pk_mul_f32 v[202:203], v[174:175], v[6:7]
	v_pk_mul_f32 v[204:205], v[180:181], v[4:5]
	global_load_dwordx4 v[4:7], v[8:9], off offset:512
	s_waitcnt vmcnt(0)
	v_pk_mul_f32 v[198:199], v[182:183], v[6:7]
	v_pk_mul_f32 v[200:201], v[184:185], v[4:5]
	global_load_dwordx4 v[4:7], v[8:9], off offset:576
	s_waitcnt vmcnt(0)
	v_pk_mul_f32 v[196:197], v[188:189], v[4:5]
	v_add_u32_e32 v4, 0xffffff00, v190
	v_ashrrev_i32_e32 v5, 31, v4
	v_lshlrev_b64 v[4:5], 13, v[4:5]
	v_lshl_add_u64 v[12:13], v[212:213], 0, v[4:5]
	v_pk_mul_f32 v[194:195], v[186:187], v[6:7]
	global_load_dwordx4 v[4:7], v[12:13], off
	global_load_dwordx4 v[8:11], v[12:13], off offset:64
	global_load_dwordx4 v[176:179], v[12:13], off offset:512
	global_load_dwordx4 v[214:217], v[12:13], off offset:576
	v_add_u32_e32 v12, 0xffffff10, v190
	v_ashrrev_i32_e32 v13, 31, v12
	v_lshlrev_b64 v[12:13], 13, v[12:13]
	v_lshl_add_u64 v[12:13], v[212:213], 0, v[12:13]
	global_load_dwordx4 v[222:225], v[12:13], off
	global_load_dwordx4 v[230:233], v[12:13], off offset:64
	global_load_dwordx4 v[236:239], v[12:13], off offset:512
	global_load_dwordx4 v[240:243], v[12:13], off offset:576
	v_lshlrev_b64 v[12:13], 13, v[190:191]
	v_lshl_add_u64 v[12:13], s[76:77], 0, v[12:13]
	v_lshl_add_u64 v[210:211], v[12:13], 0, v[2:3]
	v_pk_mul_f32 v[12:13], v[156:157], v[158:159] op_sel_hi:[0,1]
	s_waitcnt vmcnt(0)
	v_pk_fma_f32 v[6:7], v[12:13], v[206:207], v[6:7]
	v_pk_fma_f32 v[4:5], v[218:219], v[208:209], v[4:5]
	global_store_dwordx4 v[210:211], v[4:7], off
	v_pk_mul_f32 v[12:13], v[156:157], v[130:131] op_sel_hi:[0,1]
	v_pk_mul_f32 v[218:219], v[152:153], v[114:115] op_sel_hi:[0,1]
	v_pk_mul_f32 v[4:5], v[156:157], v[128:129] op_sel_hi:[0,1]
	v_pk_fma_f32 v[6:7], v[4:5], v[202:203], v[10:11]
	v_pk_fma_f32 v[4:5], v[12:13], v[204:205], v[8:9]
	global_store_dwordx4 v[210:211], v[4:7], off offset:64
	v_pk_mul_f32 v[8:9], v[156:157], v[168:169] op_sel_hi:[0,1]
	v_pk_mul_f32 v[10:11], v[154:155], v[120:121] op_sel_hi:[0,1]
	v_pk_mul_f32 v[4:5], v[156:157], v[166:167] op_sel_hi:[0,1]
	v_pk_fma_f32 v[6:7], v[4:5], v[198:199], v[178:179]
	v_pk_fma_f32 v[4:5], v[8:9], v[200:201], v[176:177]
	global_store_dwordx4 v[210:211], v[4:7], off offset:512
	v_pk_mul_f32 v[8:9], v[156:157], v[164:165] op_sel_hi:[0,1]
	s_nop 0
	v_pk_mul_f32 v[4:5], v[156:157], v[162:163] op_sel_hi:[0,1]
	v_pk_fma_f32 v[6:7], v[4:5], v[194:195], v[216:217]
	v_pk_fma_f32 v[4:5], v[8:9], v[196:197], v[214:215]
	global_store_dwordx4 v[210:211], v[4:7], off offset:576
	s_nop 1
	v_or_b32_e32 v4, 16, v190
	v_ashrrev_i32_e32 v5, 31, v4
	v_lshlrev_b64 v[4:5], 13, v[4:5]
	v_lshl_add_u64 v[4:5], s[76:77], 0, v[4:5]
	v_lshl_add_u64 v[8:9], v[4:5], 0, v[2:3]
	v_pk_mul_f32 v[4:5], v[154:155], v[122:123] op_sel_hi:[0,1]
	v_pk_fma_f32 v[6:7], v[4:5], v[206:207], v[224:225]
	v_pk_fma_f32 v[4:5], v[10:11], v[208:209], v[222:223]
	global_store_dwordx4 v[8:9], v[4:7], off
	v_pk_mul_f32 v[10:11], v[154:155], v[116:117] op_sel_hi:[0,1]
	s_nop 0
	v_pk_mul_f32 v[4:5], v[154:155], v[118:119] op_sel_hi:[0,1]
	v_pk_fma_f32 v[6:7], v[4:5], v[202:203], v[232:233]
	v_pk_fma_f32 v[4:5], v[10:11], v[204:205], v[230:231]
	global_store_dwordx4 v[8:9], v[4:7], off offset:64
	v_pk_mul_f32 v[10:11], v[154:155], v[126:127] op_sel_hi:[0,1]
	s_nop 0
	v_pk_mul_f32 v[4:5], v[154:155], v[124:125] op_sel_hi:[0,1]
	v_pk_fma_f32 v[6:7], v[4:5], v[198:199], v[238:239]
	v_pk_fma_f32 v[4:5], v[10:11], v[200:201], v[236:237]
	global_store_dwordx4 v[8:9], v[4:7], off offset:512
	v_pk_mul_f32 v[10:11], v[154:155], v[96:97] op_sel_hi:[0,1]
	s_nop 0
	v_pk_mul_f32 v[4:5], v[154:155], v[94:95] op_sel_hi:[0,1]
	v_pk_fma_f32 v[6:7], v[4:5], v[194:195], v[242:243]
	v_pk_fma_f32 v[4:5], v[10:11], v[196:197], v[240:241]
	global_store_dwordx4 v[8:9], v[4:7], off offset:576
	s_nop 1
	v_add_u32_e32 v4, 0xffffff20, v190
	v_ashrrev_i32_e32 v5, 31, v4
	v_lshlrev_b64 v[4:5], 13, v[4:5]
	v_lshl_add_u64 v[12:13], v[212:213], 0, v[4:5]
	global_load_dwordx4 v[4:7], v[12:13], off
	global_load_dwordx4 v[8:11], v[12:13], off offset:64
	global_load_dwordx4 v[176:179], v[12:13], off offset:512
	global_load_dwordx4 v[214:217], v[12:13], off offset:576
	v_add_u32_e32 v12, 0xffffff30, v190
	v_ashrrev_i32_e32 v13, 31, v12
	v_lshlrev_b64 v[12:13], 13, v[12:13]
	v_lshl_add_u64 v[12:13], v[212:213], 0, v[12:13]
	global_load_dwordx4 v[222:225], v[12:13], off
	global_load_dwordx4 v[230:233], v[12:13], off offset:64
	global_load_dwordx4 v[236:239], v[12:13], off offset:512
	global_load_dwordx4 v[240:243], v[12:13], off offset:576
	v_or_b32_e32 v12, 32, v190
	v_ashrrev_i32_e32 v13, 31, v12
	v_lshlrev_b64 v[12:13], 13, v[12:13]
	v_lshl_add_u64 v[12:13], s[76:77], 0, v[12:13]
	v_lshl_add_u64 v[12:13], v[12:13], 0, v[2:3]
	s_waitcnt vmcnt(0)
	v_pk_fma_f32 v[6:7], v[218:219], v[206:207], v[6:7]
	v_pk_fma_f32 v[4:5], v[244:245], v[208:209], v[4:5]
	global_store_dwordx4 v[12:13], v[4:7], off
	v_pk_mul_f32 v[218:219], v[152:153], v[108:109] op_sel_hi:[0,1]
	s_nop 0
	v_pk_mul_f32 v[4:5], v[152:153], v[110:111] op_sel_hi:[0,1]
	v_pk_fma_f32 v[6:7], v[4:5], v[202:203], v[10:11]
	v_pk_fma_f32 v[4:5], v[218:219], v[204:205], v[8:9]
	global_store_dwordx4 v[12:13], v[4:7], off offset:64
	v_pk_mul_f32 v[8:9], v[152:153], v[92:93] op_sel_hi:[0,1]
	s_nop 0
	v_pk_mul_f32 v[4:5], v[152:153], v[90:91] op_sel_hi:[0,1]
	v_pk_fma_f32 v[6:7], v[4:5], v[198:199], v[178:179]
	v_pk_fma_f32 v[4:5], v[8:9], v[200:201], v[176:177]
	global_store_dwordx4 v[12:13], v[4:7], off offset:512
	v_pk_mul_f32 v[8:9], v[152:153], v[88:89] op_sel_hi:[0,1]
	s_nop 0
	v_pk_mul_f32 v[4:5], v[152:153], v[86:87] op_sel_hi:[0,1]
	v_pk_fma_f32 v[6:7], v[4:5], v[194:195], v[216:217]
	v_pk_fma_f32 v[4:5], v[8:9], v[196:197], v[214:215]
	global_store_dwordx4 v[12:13], v[4:7], off offset:576
	v_pk_mul_f32 v[8:9], v[150:151], v[104:105] op_sel_hi:[0,1]
	v_add_u32_e32 v214, 0xffffff90, v190
	v_or_b32_e32 v4, 48, v190
	v_ashrrev_i32_e32 v5, 31, v4
	v_lshlrev_b64 v[4:5], 13, v[4:5]
	v_lshl_add_u64 v[4:5], s[76:77], 0, v[4:5]
	v_lshl_add_u64 v[6:7], v[4:5], 0, v[2:3]
	v_pk_mul_f32 v[2:3], v[150:151], v[106:107] op_sel_hi:[0,1]
	v_pk_fma_f32 v[4:5], v[2:3], v[206:207], v[224:225]
	v_pk_fma_f32 v[2:3], v[8:9], v[208:209], v[222:223]
	global_store_dwordx4 v[6:7], v[2:5], off
	v_pk_mul_f32 v[8:9], v[150:151], v[100:101] op_sel_hi:[0,1]
	v_ashrrev_i32_e32 v215, 31, v214
	v_pk_mul_f32 v[2:3], v[150:151], v[102:103] op_sel_hi:[0,1]
	v_pk_fma_f32 v[4:5], v[2:3], v[202:203], v[232:233]
	v_pk_fma_f32 v[2:3], v[8:9], v[204:205], v[230:231]
	global_store_dwordx4 v[6:7], v[2:5], off offset:64
	v_pk_mul_f32 v[8:9], v[150:151], v[84:85] op_sel_hi:[0,1]
	v_lshlrev_b64 v[214:215], 13, v[214:215]
	v_pk_mul_f32 v[2:3], v[150:151], v[82:83] op_sel_hi:[0,1]
	v_pk_fma_f32 v[4:5], v[2:3], v[198:199], v[238:239]
	v_pk_fma_f32 v[2:3], v[8:9], v[200:201], v[236:237]
	global_store_dwordx4 v[6:7], v[2:5], off offset:512
	v_pk_mul_f32 v[8:9], v[150:151], v[80:81] op_sel_hi:[0,1]
	v_lshl_add_u64 v[218:219], v[212:213], 0, v[214:215]
	v_pk_mul_f32 v[2:3], v[150:151], v[78:79] op_sel_hi:[0,1]
	v_pk_fma_f32 v[4:5], v[2:3], v[194:195], v[242:243]
	v_pk_fma_f32 v[2:3], v[8:9], v[196:197], v[240:241]
	global_store_dwordx4 v[6:7], v[2:5], off offset:576
	v_pk_mul_f32 v[240:241], v[148:149], v[70:71] op_sel_hi:[0,1]
	v_pk_mul_f32 v[242:243], v[148:149], v[72:73] op_sel_hi:[0,1]
	v_add_u32_e32 v2, 0xffffff80, v190
	v_ashrrev_i32_e32 v3, 31, v2
	v_lshlrev_b64 v[2:3], 13, v[2:3]
	v_lshl_add_u64 v[2:3], v[212:213], 0, v[2:3]
	global_load_dwordx4 v[10:13], v[2:3], off
	global_load_dwordx4 v[176:179], v[2:3], off offset:64
	global_load_dwordx4 v[6:9], v[2:3], off offset:512
	s_nop 0
	global_load_dwordx4 v[2:5], v[2:3], off offset:576
	s_nop 0
	global_load_dwordx4 v[214:217], v[218:219], off
	global_load_dwordx4 v[222:225], v[218:219], off offset:64
	global_load_dwordx4 v[230:233], v[218:219], off offset:512
	global_load_dwordx4 v[236:239], v[218:219], off offset:576
	v_lshl_add_u64 v[218:219], v[210:211], 0, s[8:9]
	s_mov_b64 s[8:9], 0x120000
	s_waitcnt vmcnt(0)
	v_pk_fma_f32 v[12:13], v[240:241], v[206:207], v[12:13]
	v_add_co_u32_e32 v240, vcc, s3, v210
	v_pk_fma_f32 v[10:11], v[242:243], v[208:209], v[10:11]
	s_nop 0
	v_addc_co_u32_e32 v241, vcc, 0, v211, vcc
	global_store_dwordx4 v[240:241], v[10:13], off
	v_pk_mul_f32 v[240:241], v[148:149], v[64:65] op_sel_hi:[0,1]
	s_mov_b32 s3, 0x120000
	v_pk_mul_f32 v[10:11], v[148:149], v[62:63] op_sel_hi:[0,1]
	v_pk_fma_f32 v[12:13], v[10:11], v[202:203], v[178:179]
	v_pk_fma_f32 v[10:11], v[240:241], v[204:205], v[176:177]
	global_store_dwordx4 v[218:219], v[10:13], off offset:64
	s_nop 1
	v_pk_mul_f32 v[10:11], v[148:149], v[74:75] op_sel_hi:[0,1]
	v_pk_mul_f32 v[12:13], v[148:149], v[76:77] op_sel_hi:[0,1]
	v_pk_fma_f32 v[8:9], v[10:11], v[198:199], v[8:9]
	v_pk_fma_f32 v[6:7], v[12:13], v[200:201], v[6:7]
	global_store_dwordx4 v[218:219], v[6:9], off offset:512
	s_nop 1
	v_pk_mul_f32 v[6:7], v[148:149], v[66:67] op_sel_hi:[0,1]
	v_pk_mul_f32 v[8:9], v[148:149], v[68:69] op_sel_hi:[0,1]
	v_pk_fma_f32 v[4:5], v[6:7], v[194:195], v[4:5]
	v_pk_fma_f32 v[2:3], v[8:9], v[196:197], v[2:3]
	global_store_dwordx4 v[218:219], v[2:5], off offset:576
	v_pk_mul_f32 v[8:9], v[146:147], v[54:55] op_sel_hi:[0,1]
	v_lshl_add_u64 v[6:7], v[210:211], 0, s[8:9]
	v_pk_mul_f32 v[2:3], v[146:147], v[56:57] op_sel_hi:[0,1]
	v_pk_fma_f32 v[4:5], v[2:3], v[206:207], v[216:217]
	v_pk_fma_f32 v[2:3], v[8:9], v[208:209], v[214:215]
	v_add_co_u32_e32 v8, vcc, s3, v210
	s_mov_b32 s3, 0x140000
	s_nop 0
	v_addc_co_u32_e32 v9, vcc, 0, v211, vcc
	global_store_dwordx4 v[8:9], v[2:5], off
	v_pk_mul_f32 v[8:9], v[146:147], v[50:51] op_sel_hi:[0,1]
	v_pk_mul_f32 v[218:219], v[144:145], v[46:47] op_sel_hi:[0,1]
	v_pk_mul_f32 v[2:3], v[146:147], v[52:53] op_sel_hi:[0,1]
	v_pk_fma_f32 v[4:5], v[2:3], v[202:203], v[224:225]
	v_pk_fma_f32 v[2:3], v[8:9], v[204:205], v[222:223]
	global_store_dwordx4 v[6:7], v[2:5], off offset:64
	v_pk_mul_f32 v[8:9], v[146:147], v[60:61] op_sel_hi:[0,1]
	s_mov_b64 s[8:9], 0x140000
	v_pk_mul_f32 v[2:3], v[146:147], v[58:59] op_sel_hi:[0,1]
	v_pk_fma_f32 v[4:5], v[2:3], v[198:199], v[232:233]
	v_pk_fma_f32 v[2:3], v[8:9], v[200:201], v[230:231]
	global_store_dwordx4 v[6:7], v[2:5], off offset:512
	v_pk_mul_f32 v[8:9], v[146:147], v[32:33] op_sel_hi:[0,1]
	s_nop 0
	v_pk_mul_f32 v[2:3], v[146:147], v[30:31] op_sel_hi:[0,1]
	v_pk_fma_f32 v[4:5], v[2:3], v[194:195], v[238:239]
	v_pk_fma_f32 v[2:3], v[8:9], v[196:197], v[236:237]
	global_store_dwordx4 v[6:7], v[2:5], off offset:576
	s_nop 1
	v_add_u32_e32 v2, 0xffffffa0, v190
	v_ashrrev_i32_e32 v3, 31, v2
	v_lshlrev_b64 v[2:3], 13, v[2:3]
	v_lshl_add_u64 v[2:3], v[212:213], 0, v[2:3]
	global_load_dwordx4 v[176:179], v[2:3], off
	global_load_dwordx4 v[214:217], v[2:3], off offset:64
	global_load_dwordx4 v[10:13], v[2:3], off offset:512
	global_load_dwordx4 v[6:9], v[2:3], off offset:576
	v_add_u32_e32 v2, 0xffffffb0, v190
	v_ashrrev_i32_e32 v3, 31, v2
	v_lshlrev_b64 v[2:3], 13, v[2:3]
	v_lshl_add_u64 v[2:3], v[212:213], 0, v[2:3]
	global_load_dwordx4 v[222:225], v[2:3], off
	global_load_dwordx4 v[230:233], v[2:3], off offset:64
	global_load_dwordx4 v[236:239], v[2:3], off offset:512
	s_nop 0
	global_load_dwordx4 v[2:5], v[2:3], off offset:576
	v_pk_mul_f32 v[212:213], v[144:145], v[48:49] op_sel_hi:[0,1]
	v_lshl_add_u64 v[190:191], v[210:211], 0, s[8:9]
	s_mov_b64 s[8:9], 0x160000
	s_waitcnt vmcnt(0)
	v_pk_fma_f32 v[178:179], v[212:213], v[206:207], v[178:179]
	v_add_co_u32_e32 v212, vcc, s3, v210
	v_pk_fma_f32 v[176:177], v[218:219], v[208:209], v[176:177]
	s_nop 0
	v_addc_co_u32_e32 v213, vcc, 0, v211, vcc
	global_store_dwordx4 v[212:213], v[176:179], off
	v_pk_mul_f32 v[212:213], v[144:145], v[42:43] op_sel_hi:[0,1]
	s_mov_b32 s3, 0x160000
	v_pk_mul_f32 v[176:177], v[144:145], v[44:45] op_sel_hi:[0,1]
	v_pk_fma_f32 v[178:179], v[176:177], v[202:203], v[216:217]
	v_pk_fma_f32 v[176:177], v[212:213], v[204:205], v[214:215]
	global_store_dwordx4 v[190:191], v[176:179], off offset:64
	s_nop 1
	v_pk_mul_f32 v[176:177], v[144:145], v[26:27] op_sel_hi:[0,1]
	v_pk_mul_f32 v[178:179], v[144:145], v[28:29] op_sel_hi:[0,1]
	v_pk_fma_f32 v[12:13], v[176:177], v[198:199], v[12:13]
	v_pk_fma_f32 v[10:11], v[178:179], v[200:201], v[10:11]
	global_store_dwordx4 v[190:191], v[10:13], off offset:512
	s_nop 1
	v_pk_mul_f32 v[10:11], v[144:145], v[22:23] op_sel_hi:[0,1]
	v_pk_mul_f32 v[12:13], v[144:145], v[24:25] op_sel_hi:[0,1]
	v_pk_fma_f32 v[8:9], v[10:11], v[194:195], v[8:9]
	v_pk_fma_f32 v[6:7], v[12:13], v[196:197], v[6:7]
	global_store_dwordx4 v[190:191], v[6:9], off offset:576
	v_pk_mul_f32 v[12:13], v[142:143], v[38:39] op_sel_hi:[0,1]
	v_lshl_add_u64 v[10:11], v[210:211], 0, s[8:9]
	v_pk_mul_f32 v[6:7], v[142:143], v[40:41] op_sel_hi:[0,1]
	v_pk_fma_f32 v[8:9], v[6:7], v[206:207], v[224:225]
	v_pk_fma_f32 v[6:7], v[12:13], v[208:209], v[222:223]
	v_add_co_u32_e32 v12, vcc, s3, v210
	s_nop 1
	v_addc_co_u32_e32 v13, vcc, 0, v211, vcc
	global_store_dwordx4 v[12:13], v[6:9], off
	v_pk_mul_f32 v[12:13], v[142:143], v[34:35] op_sel_hi:[0,1]
	s_nop 0
	v_pk_mul_f32 v[6:7], v[142:143], v[36:37] op_sel_hi:[0,1]
	v_pk_fma_f32 v[8:9], v[6:7], v[202:203], v[232:233]
	v_pk_fma_f32 v[6:7], v[12:13], v[204:205], v[230:231]
	global_store_dwordx4 v[10:11], v[6:9], off offset:64
	v_pk_mul_f32 v[12:13], v[142:143], v[20:21] op_sel_hi:[0,1]
	s_nop 0
	v_pk_mul_f32 v[6:7], v[142:143], v[18:19] op_sel_hi:[0,1]
	v_pk_fma_f32 v[8:9], v[6:7], v[198:199], v[238:239]
	v_pk_fma_f32 v[6:7], v[12:13], v[200:201], v[236:237]
	global_store_dwordx4 v[10:11], v[6:9], off offset:512
	s_nop 1
	v_pk_mul_f32 v[6:7], v[142:143], v[14:15] op_sel_hi:[0,1]
	v_pk_mul_f32 v[8:9], v[142:143], v[16:17] op_sel_hi:[0,1]
	v_pk_fma_f32 v[4:5], v[6:7], v[194:195], v[4:5]
	v_pk_fma_f32 v[2:3], v[8:9], v[196:197], v[2:3]
	global_store_dwordx4 v[10:11], v[2:5], off offset:576
